# NA window-mask selects without EXEC branches; LDS-DMA issue blocks trimmed (no m0 save/restore)
# speedup vs baseline: 1.0195x; 1.0037x over previous
.LBB0_299:
	s_andn2_b64 vcc, exec, s[0:1]
	s_cbranch_vccnz .LBB0_384
	v_readlane_b32 s3, v255, 0
	s_cmpk_gt_i32 s3, 0x6e7
	v_mbcnt_lo_u32_b32 v0, -1, 0
	v_mbcnt_hi_u32_b32 v0, -1, v0
	s_cbranch_scc1 .LBB0_322
	v_readlane_b32 s4, v254, 62
	v_readlane_b32 s5, v254, 63
	s_add_u32 s29, s4, 0x2000000
	s_mul_i32 s30, s67, 0x340000
	s_addc_u32 s38, s5, 0
	s_lshl_b64 s[0:1], s[30:31], 1
	s_add_u32 s0, s4, s0
	s_addc_u32 s1, s5, s1
	s_add_u32 s30, s0, 0x20900000
	s_addc_u32 s39, s1, 0
	s_lshl_b32 s8, s56, 10
	v_lshl_or_b32 v1, v0, 4, s8
	v_ashrrev_i32_e32 v2, 31, v1
	v_lshrrev_b32_e32 v2, 22, v2
	v_add_u32_e32 v2, v1, v2
	v_ashrrev_i32_e32 v2, 10, v2
	v_mul_i32_i24_e32 v3, 0x400, v2
	v_sub_u32_e32 v3, v1, v3
	v_lshrrev_b32_e32 v4, 4, v3
	s_add_i32 s40, s8, 0
	v_bitop3_b32 v3, v4, v3, 32 bitop3:0x6c
	s_ashr_i32 s1, s56, 2
	s_add_i32 s41, s40, 0x10000
	s_add_i32 s42, s40, 0x12000
	s_add_i32 s43, s40, 0x14000
	s_add_i32 s44, s40, 0x16000
	s_add_i32 s45, s40, 0x2000
	s_add_i32 s46, s40, 0x4000
	s_add_i32 s47, s40, 0x6000
	v_ashrrev_i32_e32 v5, 31, v3
	s_cmp_eq_u32 s1, 1
	v_lshrrev_b32_e32 v5, 26, v5
	s_cselect_b64 s[4:5], -1, 0
	s_ashr_i32 s48, s3, 31
	v_lshlrev_b32_e32 v4, 3, v2
	v_add_u32_e32 v5, v3, v5
	s_lshr_b32 s0, s48, 29
	v_and_b32_e32 v4, -16, v4
	s_waitcnt vmcnt(0)
	v_ashrrev_i32_e32 v6, 6, v5
	v_and_b32_e32 v5, 0xc0, v5
	s_add_i32 s0, s3, s0
	v_add_u32_e32 v4, v6, v4
	v_sub_u32_e32 v3, v3, v5
	s_ashr_i32 s2, s0, 3
	s_and_b32 s0, s0, -8
	v_lshlrev_b32_e32 v2, 5, v2
	v_ashrrev_i16_sdwa v3, v193, sext(v3) dst_sel:DWORD dst_unused:UNUSED_PAD src0_sel:DWORD src1_sel:BYTE_0
	v_lshlrev_b32_e32 v5, 1, v4
	v_lshrrev_b32_e32 v7, 2, v4
	v_and_b32_e32 v6, 3, v6
	s_mov_b32 s8, 0x1fffe0
	s_sub_i32 s0, s3, s0
	v_and_b32_e32 v2, 32, v2
	v_bfe_i32 v3, v3, 0, 16
	v_and_b32_e32 v5, 24, v5
	v_and_b32_e32 v7, 4, v7
	v_and_or_b32 v6, v4, s8, v6
	s_cmp_lt_i32 s0, 0
	s_movk_i32 s3, 0xde
	v_or3_b32 v5, v6, v7, v5
	v_add_lshl_u32 v2, v2, v3, 1
	v_add_u32_e32 v1, 0x2000, v1
	s_cselect_b32 s3, s3, 0xdd
	v_lshl_add_u32 v65, v4, 11, v2
	v_lshl_add_u32 v114, v5, 11, v2
	v_ashrrev_i32_e32 v2, 31, v1
	s_mul_i32 s0, s0, s3
	v_lshrrev_b32_e32 v2, 22, v2
	s_add_i32 s0, s0, s2
	v_add_u32_e32 v2, v1, v2
	s_mul_hi_i32 s2, s0, 0x4ec4ec4f
	v_ashrrev_i32_e32 v2, 10, v2
	s_lshr_b32 s3, s2, 31
	s_ashr_i32 s2, s2, 5
	v_mul_i32_i24_e32 v3, 0x400, v2
	s_add_i32 s2, s2, s3
	v_sub_u32_e32 v1, v1, v3
	s_lshl_b32 s3, s2, 3
	s_mulk_i32 s2, 0x68
	v_lshrrev_b32_e32 v3, 4, v1
	s_sub_i32 s2, s0, s2
	v_bitop3_b32 v1, v3, v1, 32 bitop3:0x6c
	s_bfe_i32 s0, s2, 0x80000
	v_ashrrev_i32_e32 v4, 31, v1
	s_bfe_u32 s0, s0, 0x3000c
	v_lshrrev_b32_e32 v4, 26, v4
	s_add_i32 s6, s2, s0
	v_add_u32_e32 v4, v1, v4
	s_bfe_i32 s0, s6, 0x80000
	s_and_b32 s6, s6, 0xf8
	v_ashrrev_i32_e32 v5, 6, v4
	v_and_b32_e32 v4, 0xffc0, v4
	s_sub_i32 s2, s2, s6
	v_sub_u32_e32 v1, v1, v4
	s_sext_i32_i16 s0, s0
	s_sext_i32_i8 s2, s2
	v_lshlrev_b32_e32 v3, 3, v2
	v_lshrrev_b16_e32 v4, 7, v1
	s_lshr_b32 s0, s0, 3
	s_add_i32 s20, s3, s2
	v_and_b32_e32 v3, -16, v3
	v_and_b32_e32 v4, 1, v4
	s_ashr_i32 s21, s20, 31
	s_bfe_i64 s[6:7], s[0:1], 0x100000
	v_add_u32_e32 v3, v5, v3
	v_add_u16_e32 v1, v1, v4
	s_lshl_b64 s[2:3], s[20:21], 19
	s_lshl_b64 s[6:7], s[6:7], 19
	v_lshlrev_b32_e32 v2, 5, v2
	v_ashrrev_i16_sdwa v1, v193, sext(v1) dst_sel:DWORD dst_unused:UNUSED_PAD src0_sel:DWORD src1_sel:BYTE_0
	v_lshlrev_b32_e32 v4, 1, v3
	v_lshrrev_b32_e32 v6, 2, v3
	v_and_b32_e32 v5, 3, v5
	s_add_u32 s24, s30, s6
	v_and_b32_e32 v2, 32, v2
	v_bfe_i32 v1, v1, 0, 16
	v_and_b32_e32 v4, 24, v4
	v_and_b32_e32 v6, 4, v6
	v_and_or_b32 v5, v3, s8, v5
	s_addc_u32 s25, s39, s7
	v_or3_b32 v4, v5, v6, v4
	v_add_lshl_u32 v1, v2, v1, 1
	s_mov_b32 m0, s41
	s_nop 0
	global_load_lds_dwordx4 v114, s[24:25]
	s_add_u32 s6, s24, 0x40000
	s_waitcnt vmcnt(0)
	v_lshl_add_u32 v135, v4, 11, v1
	s_mov_b32 m0, s42
	s_nop 0
	global_load_lds_dwordx4 v135, s[24:25]
	s_addc_u32 s7, s25, 0
	s_mov_b32 m0, s43
	s_nop 0
	global_load_lds_dwordx4 v114, s[6:7]
	s_add_u32 s22, s29, s2
	s_mov_b32 m0, s44
	s_nop 0
	global_load_lds_dwordx4 v135, s[6:7]
	s_addc_u32 s23, s38, s3
	s_mov_b32 m0, s40
	s_nop 0
	global_load_lds_dwordx4 v65, s[22:23]
	s_add_u32 s2, s22, 0x40000
	v_lshl_add_u32 v134, v3, 11, v1
	s_mov_b32 m0, s45
	s_nop 0
	global_load_lds_dwordx4 v134, s[22:23]
	s_addc_u32 s3, s23, 0
	s_mov_b32 m0, s46
	s_nop 0
	global_load_lds_dwordx4 v65, s[2:3]
	s_cmp_lg_u32 s1, 1
	s_mov_b32 m0, s47
	s_nop 0
	global_load_lds_dwordx4 v134, s[2:3]
	s_cbranch_scc1 .LBB0_303
	s_barrier
.LBB0_303:
	v_readlane_b32 s2, v254, 62
	v_readlane_b32 s3, v254, 63
	s_add_u32 s6, s2, 0x6400000
	s_addc_u32 s7, s3, 0
	s_add_u32 s8, s2, 0x1400000
	s_sext_i32_i8 s60, s0
	s_addc_u32 s9, s3, 0
	s_and_b32 s0, s56, 3
	s_lshl_b32 s49, s1, 6
	s_lshl_b32 s1, s1, 13
	s_lshl_b32 s50, s0, 5
	s_lshl_b32 s2, s0, 12
	s_add_i32 s51, s40, 0x18000
	s_add_i32 s52, s40, 0x1a000
	s_add_i32 s53, s40, 0x8000
	s_add_i32 s54, s40, 0xa000
	s_add_i32 s55, s40, 0x1c000
	s_mov_b32 s3, s56
	s_add_i32 s56, s40, 0x1e000
	s_add_i32 s57, s40, 0xc000
	s_cmp_lt_u32 s3, 4
	s_cselect_b64 s[12:13], -1, 0
	s_cmp_eq_u32 s0, 0
	s_cselect_b64 s[14:15], -1, 0
	s_add_i32 s59, s40, 0xe000
	v_and_b32_e32 v1, 48, v0
	v_lshlrev_b32_e32 v2, 6, v0
	s_movk_i32 s0, 0x3c0
	v_lshlrev_b32_e32 v0, 2, v0
	v_and_or_b32 v1, v2, s0, v1
	v_and_b32_e32 v0, 32, v0
	s_add_u32 s0, s24, 0x80
	v_bitop3_b32 v2, v1, s1, v0 bitop3:0xde
	v_bitop3_b32 v0, v1, s2, v0 bitop3:0xde
	s_waitcnt vmcnt(2)
	s_barrier
	s_addc_u32 s1, s25, 0
	s_mov_b32 m0, s51
	s_nop 0
	global_load_lds_dwordx4 v114, s[0:1]
	s_mov_b32 s58, 0
	s_mov_b32 m0, s52
	s_nop 0
	global_load_lds_dwordx4 v135, s[0:1]
	s_add_u32 s0, s22, 0x80
	s_addc_u32 s1, s23, 0
	s_mov_b32 m0, s53
	s_nop 0
	global_load_lds_dwordx4 v65, s[0:1]
	v_add_u32_e32 v136, 0, v0
	s_mov_b32 m0, s54
	s_nop 0
	global_load_lds_dwordx4 v134, s[0:1]
	s_add_u32 s0, s24, 0x40080
	s_addc_u32 s1, s25, 0
	s_mov_b32 m0, s55
	s_nop 0
	global_load_lds_dwordx4 v114, s[0:1]
	v_add_u32_e32 v137, 0, v2
	s_mov_b32 m0, s56
	s_nop 0
	global_load_lds_dwordx4 v135, s[0:1]
	s_waitcnt vmcnt(6)
	s_barrier
	s_branch .LBB0_306

.LBB0_309:
	s_add_u32 s33, s22, s2
	s_addc_u32 s61, s23, s3
	v_add_u32_e32 v132, 0x10000, v136
	v_add_u32_e32 v138, 0x14000, v136
	s_add_u32 s34, s33, 0x100
	ds_read_b128 v[140:143], v132
	ds_read_b128 v[144:147], v132 offset:1024
	ds_read_b128 v[148:151], v132 offset:2048
	ds_read_b128 v[152:155], v132 offset:3072
	ds_read_b128 v[156:159], v138
	ds_read_b128 v[160:163], v138 offset:1024
	ds_read_b128 v[164:167], v138 offset:2048
	ds_read_b128 v[168:171], v138 offset:3072
	s_addc_u32 s35, s61, 0
	s_add_u32 s26, s33, 0x180
	s_addc_u32 s27, s61, 0
	s_add_u32 s19, s24, s2
	s_addc_u32 s21, s25, s3
	s_add_u32 s36, s19, 0x100
	s_addc_u32 s37, s21, 0
	ds_read_b128 v[172:175], v137
	ds_read_b128 v[176:179], v137 offset:1024
	ds_read_b128 v[180:183], v137 offset:2048
	ds_read_b128 v[184:187], v137 offset:3072
	ds_read_b128 v[188:191], v137 offset:4096
	ds_read_b128 v[194:197], v137 offset:5120
	ds_read_b128 v[202:205], v137 offset:6144
	ds_read_b128 v[206:209], v137 offset:7168
	s_add_u32 s62, s33, 0x40080
	s_addc_u32 s63, s61, 0
	s_mov_b32 m0, s57
	s_nop 0
	global_load_lds_dwordx4 v65, s[62:63]
	s_nop 0
	s_mov_b32 m0, s59
	s_nop 0
	global_load_lds_dwordx4 v134, s[62:63]
	s_waitcnt vmcnt(8)
	s_waitcnt lgkmcnt(0)
	s_barrier
	s_setprio 1
	s_waitcnt lgkmcnt(0)
	v_mfma_f32_16x16x32_bf16 v[128:131], v[140:143], v[172:175], v[128:131]
	v_mfma_f32_16x16x32_bf16 v[124:127], v[148:151], v[172:175], v[124:127]
	v_mfma_f32_16x16x32_bf16 v[120:123], v[140:143], v[180:183], v[120:123]
	v_mfma_f32_16x16x32_bf16 v[116:119], v[148:151], v[180:183], v[116:119]
	v_mfma_f32_16x16x32_bf16 v[110:113], v[140:143], v[188:191], v[110:113]
	v_mfma_f32_16x16x32_bf16 v[106:109], v[148:151], v[188:191], v[106:109]
	v_mfma_f32_16x16x32_bf16 v[102:105], v[140:143], v[202:205], v[102:105]
	v_mfma_f32_16x16x32_bf16 v[98:101], v[148:151], v[202:205], v[98:101]
	v_mfma_f32_16x16x32_bf16 v[128:131], v[144:147], v[176:179], v[128:131]
	v_mfma_f32_16x16x32_bf16 v[124:127], v[152:155], v[176:179], v[124:127]
	v_mfma_f32_16x16x32_bf16 v[120:123], v[144:147], v[184:187], v[120:123]
	v_mfma_f32_16x16x32_bf16 v[116:119], v[152:155], v[184:187], v[116:119]
	v_mfma_f32_16x16x32_bf16 v[110:113], v[144:147], v[194:197], v[110:113]
	v_mfma_f32_16x16x32_bf16 v[106:109], v[152:155], v[194:197], v[106:109]
	v_mfma_f32_16x16x32_bf16 v[102:105], v[144:147], v[206:209], v[102:105]
	v_mfma_f32_16x16x32_bf16 v[98:101], v[152:155], v[206:209], v[98:101]
	s_setprio 0
	s_setprio 1
	v_mfma_f32_16x16x32_bf16 v[94:97], v[156:159], v[172:175], v[94:97]
	v_mfma_f32_16x16x32_bf16 v[90:93], v[164:167], v[172:175], v[90:93]
	v_mfma_f32_16x16x32_bf16 v[86:89], v[156:159], v[180:183], v[86:89]
	v_mfma_f32_16x16x32_bf16 v[82:85], v[164:167], v[180:183], v[82:85]
	v_mfma_f32_16x16x32_bf16 v[78:81], v[156:159], v[188:191], v[78:81]
	v_mfma_f32_16x16x32_bf16 v[74:77], v[164:167], v[188:191], v[74:77]
	v_mfma_f32_16x16x32_bf16 v[70:73], v[156:159], v[202:205], v[70:73]
	v_mfma_f32_16x16x32_bf16 v[66:69], v[164:167], v[202:205], v[66:69]
	v_mfma_f32_16x16x32_bf16 v[94:97], v[160:163], v[176:179], v[94:97]
	v_mfma_f32_16x16x32_bf16 v[90:93], v[168:171], v[176:179], v[90:93]
	v_mfma_f32_16x16x32_bf16 v[86:89], v[160:163], v[184:187], v[86:89]
	v_mfma_f32_16x16x32_bf16 v[82:85], v[168:171], v[184:187], v[82:85]
	v_mfma_f32_16x16x32_bf16 v[78:81], v[160:163], v[194:197], v[78:81]
	v_mfma_f32_16x16x32_bf16 v[74:77], v[168:171], v[194:197], v[74:77]
	v_mfma_f32_16x16x32_bf16 v[70:73], v[160:163], v[206:209], v[70:73]
	v_mfma_f32_16x16x32_bf16 v[66:69], v[168:171], v[206:209], v[66:69]
	s_setprio 0
	s_barrier
	ds_read_b128 v[172:175], v137 offset:16384
	ds_read_b128 v[176:179], v137 offset:17408
	ds_read_b128 v[180:183], v137 offset:18432
	ds_read_b128 v[184:187], v137 offset:19456
	ds_read_b128 v[188:191], v137 offset:20480
	ds_read_b128 v[194:197], v137 offset:21504
	ds_read_b128 v[202:205], v137 offset:22528
	ds_read_b128 v[206:209], v137 offset:23552
	s_mov_b32 m0, s41
	s_nop 0
	global_load_lds_dwordx4 v114, s[36:37]
	s_nop 0
	s_mov_b32 m0, s42
	s_nop 0
	global_load_lds_dwordx4 v135, s[36:37]
	s_add_u32 s36, s19, 0x40100
	s_addc_u32 s37, s21, 0
	s_mov_b32 m0, s43
	s_nop 0
	global_load_lds_dwordx4 v114, s[36:37]
	s_nop 0
	s_mov_b32 m0, s44
	s_nop 0
	global_load_lds_dwordx4 v135, s[36:37]
	s_mov_b32 m0, s40
	s_nop 0
	global_load_lds_dwordx4 v65, s[34:35]
	s_nop 0
	s_mov_b32 m0, s45
	s_nop 0
	global_load_lds_dwordx4 v134, s[34:35]
	s_waitcnt vmcnt(8)
	s_waitcnt lgkmcnt(0)
	s_barrier
	s_setprio 1
	s_waitcnt lgkmcnt(0)
	v_mfma_f32_16x16x32_bf16 v[60:63], v[140:143], v[172:175], v[60:63]
	v_mfma_f32_16x16x32_bf16 v[56:59], v[148:151], v[172:175], v[56:59]
	s_waitcnt lgkmcnt(5)
	v_mfma_f32_16x16x32_bf16 v[52:55], v[140:143], v[180:183], v[52:55]
	v_mfma_f32_16x16x32_bf16 v[48:51], v[148:151], v[180:183], v[48:51]
	s_waitcnt lgkmcnt(3)
	v_mfma_f32_16x16x32_bf16 v[44:47], v[140:143], v[188:191], v[44:47]
	v_mfma_f32_16x16x32_bf16 v[40:43], v[148:151], v[188:191], v[40:43]
	s_waitcnt lgkmcnt(1)
	v_mfma_f32_16x16x32_bf16 v[36:39], v[140:143], v[202:205], v[36:39]
	v_mfma_f32_16x16x32_bf16 v[32:35], v[148:151], v[202:205], v[32:35]
	v_mfma_f32_16x16x32_bf16 v[60:63], v[144:147], v[176:179], v[60:63]
	v_mfma_f32_16x16x32_bf16 v[56:59], v[152:155], v[176:179], v[56:59]
	v_mfma_f32_16x16x32_bf16 v[52:55], v[144:147], v[184:187], v[52:55]
	v_mfma_f32_16x16x32_bf16 v[48:51], v[152:155], v[184:187], v[48:51]
	v_mfma_f32_16x16x32_bf16 v[44:47], v[144:147], v[194:197], v[44:47]
	v_mfma_f32_16x16x32_bf16 v[40:43], v[152:155], v[194:197], v[40:43]
	s_waitcnt lgkmcnt(0)
	v_mfma_f32_16x16x32_bf16 v[36:39], v[144:147], v[206:209], v[36:39]
	v_mfma_f32_16x16x32_bf16 v[32:35], v[152:155], v[206:209], v[32:35]
	s_setprio 0
	s_setprio 1
	v_mfma_f32_16x16x32_bf16 v[28:31], v[156:159], v[172:175], v[28:31]
	v_mfma_f32_16x16x32_bf16 v[24:27], v[164:167], v[172:175], v[24:27]
	v_mfma_f32_16x16x32_bf16 v[20:23], v[156:159], v[180:183], v[20:23]
	v_mfma_f32_16x16x32_bf16 v[16:19], v[164:167], v[180:183], v[16:19]
	v_mfma_f32_16x16x32_bf16 v[12:15], v[156:159], v[188:191], v[12:15]
	v_mfma_f32_16x16x32_bf16 v[8:11], v[164:167], v[188:191], v[8:11]
	v_mfma_f32_16x16x32_bf16 v[4:7], v[156:159], v[202:205], v[4:7]
	v_mfma_f32_16x16x32_bf16 v[0:3], v[164:167], v[202:205], v[0:3]
	v_mfma_f32_16x16x32_bf16 v[28:31], v[160:163], v[176:179], v[28:31]
	v_mfma_f32_16x16x32_bf16 v[24:27], v[168:171], v[176:179], v[24:27]
	v_mfma_f32_16x16x32_bf16 v[20:23], v[160:163], v[184:187], v[20:23]
	v_mfma_f32_16x16x32_bf16 v[16:19], v[168:171], v[184:187], v[16:19]
	v_mfma_f32_16x16x32_bf16 v[12:15], v[160:163], v[194:197], v[12:15]
	v_mfma_f32_16x16x32_bf16 v[8:11], v[168:171], v[194:197], v[8:11]
	v_mfma_f32_16x16x32_bf16 v[4:7], v[160:163], v[206:209], v[4:7]
	v_mfma_f32_16x16x32_bf16 v[0:3], v[168:171], v[206:209], v[0:3]
	s_setprio 0
	s_barrier
	v_add_u32_e32 v133, 0x18000, v136
	v_add_u32_e32 v139, 0x1c000, v136
	ds_read_b128 v[140:143], v133
	ds_read_b128 v[144:147], v133 offset:1024
	ds_read_b128 v[148:151], v133 offset:2048
	ds_read_b128 v[152:155], v133 offset:3072
	ds_read_b128 v[156:159], v139
	ds_read_b128 v[160:163], v139 offset:1024
	ds_read_b128 v[164:167], v139 offset:2048
	ds_read_b128 v[168:171], v139 offset:3072
	ds_read_b128 v[172:175], v137 offset:32768
	ds_read_b128 v[176:179], v137 offset:33792
	ds_read_b128 v[180:183], v137 offset:34816
	ds_read_b128 v[184:187], v137 offset:35840
	ds_read_b128 v[188:191], v137 offset:36864
	ds_read_b128 v[194:197], v137 offset:37888
	ds_read_b128 v[202:205], v137 offset:38912
	ds_read_b128 v[206:209], v137 offset:39936
	s_add_u32 s34, s33, 0x40100
	s_addc_u32 s35, s61, 0
	s_mov_b32 m0, s46
	s_nop 0
	global_load_lds_dwordx4 v65, s[34:35]
	s_nop 0
	s_mov_b32 m0, s47
	s_nop 0
	global_load_lds_dwordx4 v134, s[34:35]
	s_waitcnt vmcnt(8)
	s_waitcnt lgkmcnt(0)
	s_barrier
	s_setprio 1
	s_waitcnt lgkmcnt(0)
	v_mfma_f32_16x16x32_bf16 v[128:131], v[140:143], v[172:175], v[128:131]
	v_mfma_f32_16x16x32_bf16 v[124:127], v[148:151], v[172:175], v[124:127]
	s_waitcnt lgkmcnt(5)
	v_mfma_f32_16x16x32_bf16 v[120:123], v[140:143], v[180:183], v[120:123]
	v_mfma_f32_16x16x32_bf16 v[116:119], v[148:151], v[180:183], v[116:119]
	s_waitcnt lgkmcnt(3)
	v_mfma_f32_16x16x32_bf16 v[110:113], v[140:143], v[188:191], v[110:113]
	v_mfma_f32_16x16x32_bf16 v[106:109], v[148:151], v[188:191], v[106:109]
	s_waitcnt lgkmcnt(1)
	v_mfma_f32_16x16x32_bf16 v[102:105], v[140:143], v[202:205], v[102:105]
	v_mfma_f32_16x16x32_bf16 v[98:101], v[148:151], v[202:205], v[98:101]
	v_mfma_f32_16x16x32_bf16 v[128:131], v[144:147], v[176:179], v[128:131]
	v_mfma_f32_16x16x32_bf16 v[124:127], v[152:155], v[176:179], v[124:127]
	v_mfma_f32_16x16x32_bf16 v[120:123], v[144:147], v[184:187], v[120:123]
	v_mfma_f32_16x16x32_bf16 v[116:119], v[152:155], v[184:187], v[116:119]
	v_mfma_f32_16x16x32_bf16 v[110:113], v[144:147], v[194:197], v[110:113]
	v_mfma_f32_16x16x32_bf16 v[106:109], v[152:155], v[194:197], v[106:109]
	s_waitcnt lgkmcnt(0)
	v_mfma_f32_16x16x32_bf16 v[102:105], v[144:147], v[206:209], v[102:105]
	v_mfma_f32_16x16x32_bf16 v[98:101], v[152:155], v[206:209], v[98:101]
	s_setprio 0
	s_setprio 1
	v_mfma_f32_16x16x32_bf16 v[94:97], v[156:159], v[172:175], v[94:97]
	v_mfma_f32_16x16x32_bf16 v[90:93], v[164:167], v[172:175], v[90:93]
	v_mfma_f32_16x16x32_bf16 v[86:89], v[156:159], v[180:183], v[86:89]
	v_mfma_f32_16x16x32_bf16 v[82:85], v[164:167], v[180:183], v[82:85]
	v_mfma_f32_16x16x32_bf16 v[78:81], v[156:159], v[188:191], v[78:81]
	v_mfma_f32_16x16x32_bf16 v[74:77], v[164:167], v[188:191], v[74:77]
	v_mfma_f32_16x16x32_bf16 v[70:73], v[156:159], v[202:205], v[70:73]
	v_mfma_f32_16x16x32_bf16 v[66:69], v[164:167], v[202:205], v[66:69]
	v_mfma_f32_16x16x32_bf16 v[94:97], v[160:163], v[176:179], v[94:97]
	v_mfma_f32_16x16x32_bf16 v[90:93], v[168:171], v[176:179], v[90:93]
	v_mfma_f32_16x16x32_bf16 v[86:89], v[160:163], v[184:187], v[86:89]
	v_mfma_f32_16x16x32_bf16 v[82:85], v[168:171], v[184:187], v[82:85]
	v_mfma_f32_16x16x32_bf16 v[78:81], v[160:163], v[194:197], v[78:81]
	v_mfma_f32_16x16x32_bf16 v[74:77], v[168:171], v[194:197], v[74:77]
	v_mfma_f32_16x16x32_bf16 v[70:73], v[160:163], v[206:209], v[70:73]
	v_mfma_f32_16x16x32_bf16 v[66:69], v[168:171], v[206:209], v[66:69]
	s_setprio 0
	s_barrier
	ds_read_b128 v[172:175], v137 offset:49152
	ds_read_b128 v[176:179], v137 offset:50176
	ds_read_b128 v[180:183], v137 offset:51200
	ds_read_b128 v[184:187], v137 offset:52224
	ds_read_b128 v[188:191], v137 offset:53248
	ds_read_b128 v[194:197], v137 offset:54272
	ds_read_b128 v[202:205], v137 offset:55296
	ds_read_b128 v[206:209], v137 offset:56320
	s_add_u32 s34, s19, 0x180
	s_addc_u32 s35, s21, 0
	s_mov_b32 m0, s51
	s_nop 0
	global_load_lds_dwordx4 v114, s[34:35]
	s_nop 0
	s_mov_b32 m0, s52
	s_nop 0
	global_load_lds_dwordx4 v135, s[34:35]
	s_add_u32 s34, s19, 0x40180
	s_addc_u32 s35, s21, 0
	s_mov_b32 m0, s55
	s_nop 0
	global_load_lds_dwordx4 v114, s[34:35]
	s_nop 0
	s_mov_b32 m0, s56
	s_nop 0
	global_load_lds_dwordx4 v135, s[34:35]
	s_nop 0
	s_mov_b32 m0, s53
	s_nop 0
	global_load_lds_dwordx4 v65, s[26:27]
	s_nop 0
	s_mov_b32 m0, s54
	s_nop 0
	global_load_lds_dwordx4 v134, s[26:27]
	s_waitcnt vmcnt(8)
	s_waitcnt lgkmcnt(0)
	s_barrier
	s_setprio 1
	s_waitcnt lgkmcnt(0)
	v_mfma_f32_16x16x32_bf16 v[60:63], v[140:143], v[172:175], v[60:63]
	v_mfma_f32_16x16x32_bf16 v[56:59], v[148:151], v[172:175], v[56:59]
	s_waitcnt lgkmcnt(5)
	v_mfma_f32_16x16x32_bf16 v[52:55], v[140:143], v[180:183], v[52:55]
	v_mfma_f32_16x16x32_bf16 v[48:51], v[148:151], v[180:183], v[48:51]
	s_waitcnt lgkmcnt(3)
	v_mfma_f32_16x16x32_bf16 v[44:47], v[140:143], v[188:191], v[44:47]
	v_mfma_f32_16x16x32_bf16 v[40:43], v[148:151], v[188:191], v[40:43]
	s_waitcnt lgkmcnt(1)
	v_mfma_f32_16x16x32_bf16 v[36:39], v[140:143], v[202:205], v[36:39]
	v_mfma_f32_16x16x32_bf16 v[32:35], v[148:151], v[202:205], v[32:35]
	v_mfma_f32_16x16x32_bf16 v[60:63], v[144:147], v[176:179], v[60:63]
	v_mfma_f32_16x16x32_bf16 v[56:59], v[152:155], v[176:179], v[56:59]
	v_mfma_f32_16x16x32_bf16 v[52:55], v[144:147], v[184:187], v[52:55]
	v_mfma_f32_16x16x32_bf16 v[48:51], v[152:155], v[184:187], v[48:51]
	v_mfma_f32_16x16x32_bf16 v[44:47], v[144:147], v[194:197], v[44:47]
	v_mfma_f32_16x16x32_bf16 v[40:43], v[152:155], v[194:197], v[40:43]
	s_waitcnt lgkmcnt(0)
	v_mfma_f32_16x16x32_bf16 v[36:39], v[144:147], v[206:209], v[36:39]
	v_mfma_f32_16x16x32_bf16 v[32:35], v[152:155], v[206:209], v[32:35]
	s_setprio 0
	s_setprio 1
	v_mfma_f32_16x16x32_bf16 v[28:31], v[156:159], v[172:175], v[28:31]
	v_mfma_f32_16x16x32_bf16 v[24:27], v[164:167], v[172:175], v[24:27]
	v_mfma_f32_16x16x32_bf16 v[20:23], v[156:159], v[180:183], v[20:23]
	v_mfma_f32_16x16x32_bf16 v[16:19], v[164:167], v[180:183], v[16:19]
	v_mfma_f32_16x16x32_bf16 v[12:15], v[156:159], v[188:191], v[12:15]
	v_mfma_f32_16x16x32_bf16 v[8:11], v[164:167], v[188:191], v[8:11]
	v_mfma_f32_16x16x32_bf16 v[4:7], v[156:159], v[202:205], v[4:7]
	v_mfma_f32_16x16x32_bf16 v[0:3], v[164:167], v[202:205], v[0:3]
	v_mfma_f32_16x16x32_bf16 v[28:31], v[160:163], v[176:179], v[28:31]
	v_mfma_f32_16x16x32_bf16 v[24:27], v[168:171], v[176:179], v[24:27]
	v_mfma_f32_16x16x32_bf16 v[20:23], v[160:163], v[184:187], v[20:23]
	v_mfma_f32_16x16x32_bf16 v[16:19], v[168:171], v[184:187], v[16:19]
	v_mfma_f32_16x16x32_bf16 v[12:15], v[160:163], v[194:197], v[12:15]
	v_mfma_f32_16x16x32_bf16 v[8:11], v[168:171], v[194:197], v[8:11]
	v_mfma_f32_16x16x32_bf16 v[4:7], v[160:163], v[206:209], v[4:7]
	v_mfma_f32_16x16x32_bf16 v[0:3], v[168:171], v[206:209], v[0:3]
	s_setprio 0
	s_barrier
	s_add_i32 s17, s17, 2
	s_add_u32 s2, s2, 0x100
	s_addc_u32 s3, s3, 0
	s_cmp_lt_u32 s17, 12
	s_cbranch_scc1 .LBB0_309
	s_ashr_i32 s19, s18, 31
	s_ashr_i32 s17, s16, 31
	ds_read_b128 v[140:143], v132
	ds_read_b128 v[144:147], v132 offset:1024
	ds_read_b128 v[148:151], v132 offset:2048
	ds_read_b128 v[152:155], v132 offset:3072
	ds_read_b128 v[156:159], v138
	ds_read_b128 v[160:163], v138 offset:1024
	ds_read_b128 v[164:167], v138 offset:2048
	ds_read_b128 v[168:171], v138 offset:3072
	s_lshl_b64 s[2:3], s[18:19], 19
	s_lshl_b64 s[26:27], s[16:17], 19
	s_add_u32 s2, s29, s2
	s_addc_u32 s3, s38, s3
	s_add_u32 s26, s30, s26
	s_addc_u32 s27, s39, s27
	s_and_b64 s[34:35], s[0:1], exec
	s_cselect_b32 s36, s2, s22
	s_cselect_b32 s37, s3, s23
	s_add_u32 s34, s36, 0x80
	s_addc_u32 s35, s37, 0
	s_and_b64 s[62:63], s[0:1], exec
	s_cselect_b32 s25, s27, s25
	s_cselect_b32 s24, s26, s24
	ds_read_b128 v[172:175], v137
	ds_read_b128 v[176:179], v137 offset:1024
	ds_read_b128 v[180:183], v137 offset:2048
	ds_read_b128 v[184:187], v137 offset:3072
	ds_read_b128 v[188:191], v137 offset:4096
	ds_read_b128 v[194:197], v137 offset:5120
	ds_read_b128 v[202:205], v137 offset:6144
	ds_read_b128 v[206:209], v137 offset:7168
	s_add_u32 s22, s22, 0x40780
	s_addc_u32 s23, s23, 0
	s_mov_b32 m0, s57
	s_nop 0
	global_load_lds_dwordx4 v65, s[22:23]
	s_nop 0
	s_mov_b32 m0, s59
	s_nop 0
	global_load_lds_dwordx4 v134, s[22:23]
	s_waitcnt vmcnt(8)
	s_waitcnt lgkmcnt(0)
	s_barrier
	s_setprio 1
	s_waitcnt lgkmcnt(0)
	v_mfma_f32_16x16x32_bf16 v[128:131], v[140:143], v[172:175], v[128:131]
	v_mfma_f32_16x16x32_bf16 v[124:127], v[148:151], v[172:175], v[124:127]
	s_waitcnt lgkmcnt(5)
	v_mfma_f32_16x16x32_bf16 v[120:123], v[140:143], v[180:183], v[120:123]
	v_mfma_f32_16x16x32_bf16 v[116:119], v[148:151], v[180:183], v[116:119]
	s_waitcnt lgkmcnt(1)
	v_mfma_f32_16x16x32_bf16 v[102:105], v[140:143], v[202:205], v[102:105]
	v_mfma_f32_16x16x32_bf16 v[98:101], v[148:151], v[202:205], v[98:101]
	v_mfma_f32_16x16x32_bf16 v[128:131], v[144:147], v[176:179], v[128:131]
	v_mfma_f32_16x16x32_bf16 v[124:127], v[152:155], v[176:179], v[124:127]
	v_mfma_f32_16x16x32_bf16 v[120:123], v[144:147], v[184:187], v[120:123]
	v_mfma_f32_16x16x32_bf16 v[116:119], v[152:155], v[184:187], v[116:119]
	v_mfma_f32_16x16x32_bf16 v[110:113], v[140:143], v[188:191], v[110:113]
	v_mfma_f32_16x16x32_bf16 v[106:109], v[148:151], v[188:191], v[106:109]
	s_waitcnt lgkmcnt(0)
	v_mfma_f32_16x16x32_bf16 v[102:105], v[144:147], v[206:209], v[102:105]
	v_mfma_f32_16x16x32_bf16 v[98:101], v[152:155], v[206:209], v[98:101]
	v_mfma_f32_16x16x32_bf16 v[210:213], v[144:147], v[194:197], v[110:113]
	v_mfma_f32_16x16x32_bf16 v[214:217], v[152:155], v[194:197], v[106:109]
	s_setprio 0
	s_setprio 1
	v_mfma_f32_16x16x32_bf16 v[94:97], v[156:159], v[172:175], v[94:97]
	v_mfma_f32_16x16x32_bf16 v[90:93], v[164:167], v[172:175], v[90:93]
	v_mfma_f32_16x16x32_bf16 v[86:89], v[156:159], v[180:183], v[86:89]
	v_mfma_f32_16x16x32_bf16 v[82:85], v[164:167], v[180:183], v[82:85]
	v_mfma_f32_16x16x32_bf16 v[70:73], v[156:159], v[202:205], v[70:73]
	v_mfma_f32_16x16x32_bf16 v[66:69], v[164:167], v[202:205], v[66:69]
	v_mfma_f32_16x16x32_bf16 v[94:97], v[160:163], v[176:179], v[94:97]
	v_mfma_f32_16x16x32_bf16 v[90:93], v[168:171], v[176:179], v[90:93]
	v_mfma_f32_16x16x32_bf16 v[86:89], v[160:163], v[184:187], v[86:89]
	v_mfma_f32_16x16x32_bf16 v[82:85], v[168:171], v[184:187], v[82:85]
	v_mfma_f32_16x16x32_bf16 v[78:81], v[156:159], v[188:191], v[78:81]
	v_mfma_f32_16x16x32_bf16 v[74:77], v[164:167], v[188:191], v[74:77]
	v_mfma_f32_16x16x32_bf16 v[70:73], v[160:163], v[206:209], v[70:73]
	v_mfma_f32_16x16x32_bf16 v[66:69], v[168:171], v[206:209], v[66:69]
	v_mfma_f32_16x16x32_bf16 v[172:175], v[160:163], v[194:197], v[78:81]
	v_mfma_f32_16x16x32_bf16 v[176:179], v[168:171], v[194:197], v[74:77]
	s_setprio 0
	s_barrier
	s_nop 1
	ds_read_b128 v[74:77], v137 offset:16384
	ds_read_b128 v[78:81], v137 offset:17408
	ds_read_b128 v[106:109], v137 offset:18432
	ds_read_b128 v[110:113], v137 offset:19456
	ds_read_b128 v[180:183], v137 offset:20480
	ds_read_b128 v[184:187], v137 offset:21504
	ds_read_b128 v[188:191], v137 offset:22528
	ds_read_b128 v[194:197], v137 offset:23552
	s_mov_b32 m0, s41
	s_nop 0
	global_load_lds_dwordx4 v114, s[24:25]
	s_add_u32 s22, s24, 0x40000
	s_mov_b32 m0, s42
	s_nop 0
	global_load_lds_dwordx4 v135, s[24:25]
	s_addc_u32 s23, s25, 0
	s_mov_b32 m0, s43
	s_nop 0
	global_load_lds_dwordx4 v114, s[22:23]
	s_nop 0
	s_mov_b32 m0, s44
	s_nop 0
	global_load_lds_dwordx4 v135, s[22:23]
	s_nop 0
	s_mov_b32 m0, s40
	s_nop 0
	global_load_lds_dwordx4 v65, s[36:37]
	s_nop 0
	s_mov_b32 m0, s45
	s_nop 0
	global_load_lds_dwordx4 v134, s[36:37]
	s_waitcnt vmcnt(8)
	s_waitcnt lgkmcnt(0)
	s_barrier
	s_setprio 1
	s_waitcnt lgkmcnt(0)
	v_mfma_f32_16x16x32_bf16 v[52:55], v[140:143], v[106:109], v[52:55]
	v_mfma_f32_16x16x32_bf16 v[48:51], v[148:151], v[106:109], v[48:51]
	v_mfma_f32_16x16x32_bf16 v[60:63], v[140:143], v[74:77], v[60:63]
	v_mfma_f32_16x16x32_bf16 v[56:59], v[148:151], v[74:77], v[56:59]
	s_waitcnt lgkmcnt(4)
	v_mfma_f32_16x16x32_bf16 v[52:55], v[144:147], v[110:113], v[52:55]
	v_mfma_f32_16x16x32_bf16 v[48:51], v[152:155], v[110:113], v[48:51]
	s_waitcnt lgkmcnt(3)
	v_mfma_f32_16x16x32_bf16 v[44:47], v[140:143], v[180:183], v[44:47]
	v_mfma_f32_16x16x32_bf16 v[40:43], v[148:151], v[180:183], v[40:43]
	s_waitcnt lgkmcnt(1)
	v_mfma_f32_16x16x32_bf16 v[36:39], v[140:143], v[188:191], v[36:39]
	v_mfma_f32_16x16x32_bf16 v[32:35], v[148:151], v[188:191], v[32:35]
	v_mfma_f32_16x16x32_bf16 v[202:205], v[144:147], v[78:81], v[60:63]
	v_mfma_f32_16x16x32_bf16 v[206:209], v[152:155], v[78:81], v[56:59]
	v_mfma_f32_16x16x32_bf16 v[218:221], v[144:147], v[184:187], v[44:47]
	v_mfma_f32_16x16x32_bf16 v[222:225], v[152:155], v[184:187], v[40:43]
	s_waitcnt lgkmcnt(0)
	v_mfma_f32_16x16x32_bf16 v[140:143], v[144:147], v[194:197], v[36:39]
	v_mfma_f32_16x16x32_bf16 v[144:147], v[152:155], v[194:197], v[32:35]
	s_setprio 0
	s_setprio 1
	v_mfma_f32_16x16x32_bf16 v[20:23], v[156:159], v[106:109], v[20:23]
	v_mfma_f32_16x16x32_bf16 v[16:19], v[164:167], v[106:109], v[16:19]
	v_mfma_f32_16x16x32_bf16 v[28:31], v[156:159], v[74:77], v[28:31]
	v_mfma_f32_16x16x32_bf16 v[24:27], v[164:167], v[74:77], v[24:27]
	v_mfma_f32_16x16x32_bf16 v[20:23], v[160:163], v[110:113], v[20:23]
	v_mfma_f32_16x16x32_bf16 v[16:19], v[168:171], v[110:113], v[16:19]
	v_mfma_f32_16x16x32_bf16 v[12:15], v[156:159], v[180:183], v[12:15]
	v_mfma_f32_16x16x32_bf16 v[8:11], v[164:167], v[180:183], v[8:11]
	v_mfma_f32_16x16x32_bf16 v[4:7], v[156:159], v[188:191], v[4:7]
	v_mfma_f32_16x16x32_bf16 v[0:3], v[164:167], v[188:191], v[0:3]
	v_mfma_f32_16x16x32_bf16 v[148:151], v[160:163], v[78:81], v[28:31]
	v_mfma_f32_16x16x32_bf16 v[152:155], v[168:171], v[78:81], v[24:27]
	v_mfma_f32_16x16x32_bf16 v[226:229], v[160:163], v[184:187], v[12:15]
	v_mfma_f32_16x16x32_bf16 v[180:183], v[168:171], v[184:187], v[8:11]
	v_mfma_f32_16x16x32_bf16 v[156:159], v[160:163], v[194:197], v[4:7]
	v_mfma_f32_16x16x32_bf16 v[160:163], v[168:171], v[194:197], v[0:3]
	s_setprio 0
	s_barrier
	s_nop 0
	ds_read_b128 v[0:3], v133
	ds_read_b128 v[4:7], v133 offset:1024
	ds_read_b128 v[164:167], v133 offset:2048
	ds_read_b128 v[168:171], v133 offset:3072
	ds_read_b128 v[184:187], v139
	ds_read_b128 v[188:191], v139 offset:1024
	ds_read_b128 v[194:197], v139 offset:2048
	ds_read_b128 v[230:233], v139 offset:3072
	ds_read_b128 v[24:27], v137 offset:32768
	ds_read_b128 v[28:31], v137 offset:33792
	ds_read_b128 v[32:35], v137 offset:34816
	ds_read_b128 v[36:39], v137 offset:35840
	ds_read_b128 v[60:63], v137 offset:36864
	ds_read_b128 v[244:247], v137 offset:37888
	ds_read_b128 v[248:251], v137 offset:38912
	ds_read_b128 v[198:201], v137 offset:39936
	s_add_u32 s22, s36, 0x40000
	s_addc_u32 s23, s37, 0
	s_mov_b32 m0, s46
	s_nop 0
	global_load_lds_dwordx4 v65, s[22:23]
	s_nop 0
	s_mov_b32 m0, s47
	s_nop 0
	global_load_lds_dwordx4 v134, s[22:23]
	s_waitcnt vmcnt(8)
	s_waitcnt lgkmcnt(0)
	s_barrier
	s_setprio 1
	s_waitcnt lgkmcnt(0)
	v_mfma_f32_16x16x32_bf16 v[8:11], v[0:3], v[24:27], v[128:131]
	s_waitcnt lgkmcnt(6)
	v_mfma_f32_16x16x32_bf16 v[106:109], v[4:7], v[28:31], v[8:11]
	v_mfma_f32_16x16x32_bf16 v[8:11], v[164:167], v[24:27], v[124:127]
	v_mfma_f32_16x16x32_bf16 v[110:113], v[168:171], v[28:31], v[8:11]
	s_waitcnt lgkmcnt(5)
	v_mfma_f32_16x16x32_bf16 v[8:11], v[0:3], v[32:35], v[120:123]
	s_waitcnt lgkmcnt(4)
	v_mfma_f32_16x16x32_bf16 v[74:77], v[4:7], v[36:39], v[8:11]
	v_mfma_f32_16x16x32_bf16 v[8:11], v[164:167], v[32:35], v[116:119]
	v_mfma_f32_16x16x32_bf16 v[78:81], v[168:171], v[36:39], v[8:11]
	s_waitcnt lgkmcnt(3)
	v_mfma_f32_16x16x32_bf16 v[8:11], v[0:3], v[60:63], v[210:213]
	s_waitcnt lgkmcnt(2)
	v_mfma_f32_16x16x32_bf16 v[40:43], v[4:7], v[244:247], v[8:11]
	v_mfma_f32_16x16x32_bf16 v[8:11], v[164:167], v[60:63], v[214:217]
	v_mfma_f32_16x16x32_bf16 v[44:47], v[168:171], v[244:247], v[8:11]
	s_waitcnt lgkmcnt(1)
	v_mfma_f32_16x16x32_bf16 v[8:11], v[0:3], v[248:251], v[102:105]
	v_mfma_f32_16x16x32_bf16 v[12:15], v[164:167], v[248:251], v[98:101]
	s_waitcnt lgkmcnt(0)
	v_mfma_f32_16x16x32_bf16 v[8:11], v[4:7], v[198:201], v[8:11]
	v_mfma_f32_16x16x32_bf16 v[12:15], v[168:171], v[198:201], v[12:15]
	s_setprio 0
	s_setprio 1
	v_mfma_f32_16x16x32_bf16 v[56:59], v[184:187], v[24:27], v[94:97]
	v_mfma_f32_16x16x32_bf16 v[24:27], v[194:197], v[24:27], v[90:93]
	v_mfma_f32_16x16x32_bf16 v[128:131], v[230:233], v[28:31], v[24:27]
	v_mfma_f32_16x16x32_bf16 v[24:27], v[184:187], v[32:35], v[86:89]
	v_mfma_f32_16x16x32_bf16 v[90:93], v[188:191], v[36:39], v[24:27]
	v_mfma_f32_16x16x32_bf16 v[24:27], v[194:197], v[32:35], v[82:85]
	v_mfma_f32_16x16x32_bf16 v[94:97], v[230:233], v[36:39], v[24:27]
	v_mfma_f32_16x16x32_bf16 v[24:27], v[184:187], v[60:63], v[172:175]
	v_mfma_f32_16x16x32_bf16 v[124:127], v[188:191], v[28:31], v[56:59]
	v_mfma_f32_16x16x32_bf16 v[56:59], v[188:191], v[244:247], v[24:27]
	v_mfma_f32_16x16x32_bf16 v[24:27], v[194:197], v[60:63], v[176:179]
	v_mfma_f32_16x16x32_bf16 v[60:63], v[230:233], v[244:247], v[24:27]
	v_mfma_f32_16x16x32_bf16 v[24:27], v[184:187], v[248:251], v[70:73]
	v_mfma_f32_16x16x32_bf16 v[28:31], v[194:197], v[248:251], v[66:69]
	v_mfma_f32_16x16x32_bf16 v[24:27], v[188:191], v[198:201], v[24:27]
	v_mfma_f32_16x16x32_bf16 v[28:31], v[230:233], v[198:201], v[28:31]
	s_setprio 0
	s_barrier
	ds_read_b128 v[82:85], v137 offset:49152
	ds_read_b128 v[86:89], v137 offset:50176
	ds_read_b128 v[172:175], v137 offset:51200
	ds_read_b128 v[176:179], v137 offset:52224
	ds_read_b128 v[198:201], v137 offset:53248
	ds_read_b128 v[210:213], v137 offset:54272
	ds_read_b128 v[214:217], v137 offset:55296
	ds_read_b128 v[244:247], v137 offset:56320
	s_add_u32 s22, s24, 0x80
	s_addc_u32 s23, s25, 0
	s_mov_b32 m0, s51
	s_nop 0
	global_load_lds_dwordx4 v114, s[22:23]
	s_nop 0
	s_mov_b32 m0, s52
	s_nop 0
	global_load_lds_dwordx4 v135, s[22:23]
	s_add_u32 s22, s24, 0x40080
	s_addc_u32 s23, s25, 0
	s_mov_b32 m0, s55
	s_nop 0
	global_load_lds_dwordx4 v114, s[22:23]
	s_nop 0
	s_mov_b32 m0, s56
	s_nop 0
	global_load_lds_dwordx4 v135, s[22:23]
	s_nop 0
	s_mov_b32 m0, s53
	s_nop 0
	global_load_lds_dwordx4 v65, s[34:35]
	s_nop 0
	s_mov_b32 m0, s54
	s_nop 0
	global_load_lds_dwordx4 v134, s[34:35]
	s_waitcnt vmcnt(8)
	s_waitcnt lgkmcnt(0)
	s_barrier
	s_setprio 1
	s_waitcnt lgkmcnt(0)
	v_mfma_f32_16x16x32_bf16 v[32:35], v[0:3], v[82:85], v[202:205]
	s_waitcnt lgkmcnt(6)
	v_mfma_f32_16x16x32_bf16 v[98:101], v[4:7], v[86:89], v[32:35]
	v_mfma_f32_16x16x32_bf16 v[32:35], v[164:167], v[82:85], v[206:209]
	v_mfma_f32_16x16x32_bf16 v[102:105], v[168:171], v[86:89], v[32:35]
	s_waitcnt lgkmcnt(5)
	v_mfma_f32_16x16x32_bf16 v[32:35], v[0:3], v[172:175], v[52:55]
	s_waitcnt lgkmcnt(4)
	v_mfma_f32_16x16x32_bf16 v[66:69], v[4:7], v[176:179], v[32:35]
	v_mfma_f32_16x16x32_bf16 v[32:35], v[164:167], v[172:175], v[48:51]
	v_mfma_f32_16x16x32_bf16 v[70:73], v[168:171], v[176:179], v[32:35]
	s_waitcnt lgkmcnt(3)
	v_mfma_f32_16x16x32_bf16 v[32:35], v[0:3], v[198:201], v[218:221]
	s_waitcnt lgkmcnt(1)
	v_mfma_f32_16x16x32_bf16 v[0:3], v[0:3], v[214:217], v[140:143]
	v_mfma_f32_16x16x32_bf16 v[32:35], v[4:7], v[210:213], v[32:35]
	v_mfma_f32_16x16x32_bf16 v[36:39], v[164:167], v[198:201], v[222:225]
	s_waitcnt lgkmcnt(0)
	v_mfma_f32_16x16x32_bf16 v[0:3], v[4:7], v[244:247], v[0:3]
	v_mfma_f32_16x16x32_bf16 v[4:7], v[164:167], v[214:217], v[144:147]
	v_mfma_f32_16x16x32_bf16 v[36:39], v[168:171], v[210:213], v[36:39]
	v_mfma_f32_16x16x32_bf16 v[4:7], v[168:171], v[244:247], v[4:7]
	s_setprio 0
	s_setprio 1
	v_mfma_f32_16x16x32_bf16 v[48:51], v[184:187], v[82:85], v[148:151]
	v_mfma_f32_16x16x32_bf16 v[116:119], v[188:191], v[86:89], v[48:51]
	v_mfma_f32_16x16x32_bf16 v[48:51], v[194:197], v[82:85], v[152:155]
	v_mfma_f32_16x16x32_bf16 v[16:19], v[194:197], v[172:175], v[16:19]
	v_mfma_f32_16x16x32_bf16 v[120:123], v[230:233], v[86:89], v[48:51]
	v_mfma_f32_16x16x32_bf16 v[86:89], v[230:233], v[176:179], v[16:19]
	v_mfma_f32_16x16x32_bf16 v[16:19], v[184:187], v[198:201], v[226:229]
	v_mfma_f32_16x16x32_bf16 v[20:23], v[184:187], v[172:175], v[20:23]
	v_mfma_f32_16x16x32_bf16 v[48:51], v[188:191], v[210:213], v[16:19]
	v_mfma_f32_16x16x32_bf16 v[16:19], v[194:197], v[198:201], v[180:183]
	v_mfma_f32_16x16x32_bf16 v[82:85], v[188:191], v[176:179], v[20:23]
	v_mfma_f32_16x16x32_bf16 v[52:55], v[230:233], v[210:213], v[16:19]
	v_mfma_f32_16x16x32_bf16 v[16:19], v[184:187], v[214:217], v[156:159]
	v_mfma_f32_16x16x32_bf16 v[20:23], v[194:197], v[214:217], v[160:163]
	v_mfma_f32_16x16x32_bf16 v[16:19], v[188:191], v[244:247], v[16:19]
	v_mfma_f32_16x16x32_bf16 v[20:23], v[230:233], v[244:247], v[20:23]
	s_setprio 0
	s_barrier
	s_andn2_b64 vcc, exec, s[12:13]
	s_cbranch_vccnz .LBB0_312
	s_barrier

.LBB0_386:
	s_andn2_b64 vcc, exec, s[0:1]
	s_cbranch_vccnz .LBB0_562
	v_writelane_b32 v255, s67, 15
	s_lshl_b32 s0, s56, 6
	v_writelane_b32 v255, s0, 31
	s_lshl_b32 s0, s56, 4
	v_writelane_b32 v255, s0, 14
	s_lshl_b32 s0, s56, 10
	v_writelane_b32 v255, s0, 5
	s_ashr_i32 s0, s56, 1
	s_lshl_b32 s29, s0, 12
	s_lshl_b32 s0, s0, 4
	v_writelane_b32 v255, s0, 18
	v_readlane_b32 s0, v254, 61
	s_cmpk_lt_i32 s0, 0x1100
	v_readlane_b32 s0, v253, 8
	v_readlane_b32 s2, v253, 10
	v_readlane_b32 s3, v253, 11
	v_readlane_b32 s6, v253, 14
	v_readlane_b32 s7, v253, 15
	s_mov_b64 s[2:3], s[6:7]
	v_readlane_b32 s1, v253, 9
	v_readlane_b32 s4, v253, 12
	v_readlane_b32 s5, v253, 13
	v_mbcnt_lo_u32_b32 v2, -1, 0
	v_mbcnt_hi_u32_b32 v2, -1, v2
	s_cbranch_scc0 .LBB0_415
	v_readlane_b32 s9, v255, 7
	s_lshl_b32 s4, s9, 2
	v_readlane_b32 s5, v255, 14
	s_and_b32 s10, s5, 48
	s_or_b32 s5, s4, 1
	s_lshl_b32 s0, s9, 7
	s_lshl_b32 s6, s5, 2
	s_lshl_b32 s80, s5, 10
	s_or_b32 s5, s4, 2
	s_or_b32 s4, s4, 3
	v_readlane_b32 s8, v254, 61
	s_and_b32 s0, s0, 0xfffffe00
	s_and_b32 s11, s6, 52
	s_lshl_b32 s6, s5, 2
	s_lshl_b32 s83, s5, 10
	s_lshl_b32 s5, s4, 2
	s_bfe_u32 s12, s8, 0x10002
	s_ashr_i32 s1, s0, 31
	s_lshl_b32 s78, s9, 12
	s_and_b32 s18, s6, 56
	s_and_b32 s19, s5, 60
	s_lshl_b32 s84, s4, 10
	s_cmp_lt_i32 s9, 4
	s_cselect_b64 s[20:21], -1, 0
	s_add_u32 s6, s2, 0x6400000
	s_addc_u32 s7, s3, 0
	s_add_u32 s4, s2, 0x1400000
	v_writelane_b32 v255, s4, 16
	s_addc_u32 s4, s3, 0
	s_and_b32 s5, s8, 3
	s_mul_i32 s5, s5, 17
	s_ashr_i32 s13, s8, 8
	v_writelane_b32 v255, s4, 17
	s_add_i32 s4, 0, 0xe000
	s_add_i32 s5, s5, s13
	s_add_i32 s14, s84, s4
	s_add_i32 s15, s83, s4
	s_add_i32 s16, s80, s4
	s_add_i32 s17, s78, s4
	s_bfe_u32 s4, s8, 0x30005
	s_sub_i32 s13, 3, s5
	s_add_i32 s30, s5, -4
	s_sub_i32 s33, 0x43, s5
	s_cmp_eq_u32 s12, 0
	s_cselect_b32 s13, s5, s13
	s_cselect_b32 s30, s30, s33
	s_lshl_b32 s13, s13, 6
	s_addk_i32 s13, 0x1000
	s_lshl_b32 s30, s30, 6
	s_cmp_lt_i32 s5, 4
	s_mulk_i32 s4, 0x1100
	s_cselect_b32 s13, s13, s30
	s_add_i32 s13, s13, s4
	s_lshl_b32 s4, s8, 5
	s_and_b32 s4, s4, 0x300
	s_add_u32 s30, s6, s4
	s_addc_u32 s33, s7, 0
	s_lshl_b64 s[4:5], s[0:1], 1
	v_ashrrev_i32_e32 v1, 4, v2
	s_add_u32 s30, s30, s4
	s_movk_i32 s0, 0x1800
	s_addc_u32 s33, s33, s5
	v_mul_lo_u32 v3, v1, s0
	s_or_b32 s0, s13, s10
	v_and_b32_e32 v0, 15, v2
	s_mul_hi_i32 s1, s0, 0x1800
	s_mulk_i32 s0, 0x1800
	v_lshlrev_b32_e32 v4, 4, v0
	s_add_u32 s0, s30, s0
	s_addc_u32 s1, s33, s1
	s_waitcnt vmcnt(0) lgkmcnt(0)
	v_or_b32_e32 v46, v4, v3
	s_mov_b32 m0, s17
	s_nop 0
	global_load_lds_dwordx4 v46, s[0:1]
	s_or_b32 s0, s13, s11
	s_mul_hi_i32 s1, s0, 0x1800
	s_mulk_i32 s0, 0x1800
	s_add_u32 s0, s30, s0
	s_addc_u32 s1, s33, s1
	v_bitop3_b32 v47, v4, 32, v3 bitop3:0x36
	s_mov_b32 m0, s16
	s_nop 0
	global_load_lds_dwordx4 v47, s[0:1]
	s_or_b32 s0, s13, s18
	s_mul_hi_i32 s1, s0, 0x1800
	s_mulk_i32 s0, 0x1800
	s_add_u32 s0, s30, s0
	v_writelane_b32 v255, s10, 23
	s_addc_u32 s1, s33, s1
	v_bitop3_b32 v48, v4, 64, v3 bitop3:0x36
	s_mov_b32 m0, s15
	s_nop 0
	global_load_lds_dwordx4 v48, s[0:1]
	s_or_b32 s0, s13, s19
	v_writelane_b32 v255, s11, 27
	s_mul_hi_i32 s1, s0, 0x1800
	s_mulk_i32 s0, 0x1800
	v_writelane_b32 v255, s18, 25
	s_add_u32 s0, s30, s0
	s_movk_i32 s15, 0x60
	v_writelane_b32 v255, s19, 29
	s_addc_u32 s1, s33, s1
	v_bitop3_b32 v49, v4, s15, v3 bitop3:0x36
	s_mov_b32 m0, s14
	s_nop 0
	global_load_lds_dwordx4 v49, s[0:1]
	v_writelane_b32 v255, s20, 8
	v_lshlrev_b32_e32 v4, 4, v2
	s_mov_b64 s[0:1], -1
	v_writelane_b32 v255, s21, 9
	s_and_b64 vcc, exec, s[20:21]
	v_lshlrev_b32_e32 v3, 5, v2
	v_and_b32_e32 v4, 48, v4
	s_cbranch_vccnz .LBB0_390
	s_movk_i32 s0, 0xff80
	v_and_or_b32 v50, v3, s0, v4
	s_mov_b64 s[0:1], 0
.LBB0_390:
	v_readlane_b32 s8, v255, 5
	s_add_i32 s14, s8, 0
	s_andn2_b64 vcc, exec, s[0:1]
	s_add_i32 s0, s14, 0x16000
	v_writelane_b32 v255, s0, 19
	s_nop 0
	v_readlane_b32 s10, v255, 15
	s_cbranch_vccnz .LBB0_392
	v_readlane_b32 s0, v255, 14
	s_add_i32 s0, s13, s0
	s_ashr_i32 s1, s0, 31
	s_lshl_b64 s[0:1], s[0:1], 7
	v_readlane_b32 s8, v255, 16
	s_add_u32 s0, s8, s0
	v_readlane_b32 s8, v255, 17
	s_addc_u32 s1, s8, s1
	s_lshl_b32 s12, s12, 6
	s_add_u32 s0, s0, s12
	s_movk_i32 s8, 0xff80
	s_addc_u32 s1, s1, 0
	v_and_or_b32 v50, v3, s8, v4
	v_readlane_b32 s8, v255, 19
	s_nop 4
	s_mov_b32 m0, s8
	s_nop 0
	global_load_lds_dwordx4 v50, s[0:1]

.LBB0_404:
	s_andn2_b32 s3, 1, s85
	s_mul_i32 s3, s3, 0x9000
	s_add_i32 s16, s3, 0
	v_readlane_b32 s10, v254, 41
	s_bfe_u32 s2, s30, 0x30005
	s_add_i32 s73, s16, 0xe000
	s_add_i32 s16, s10, s79
	s_mulk_i32 s2, 0x1100
	s_and_b32 s16, s16, 0x180
	s_add_i32 s2, s97, s2
	s_lshl_b32 s16, s16, 1
	v_readlane_b32 s10, v255, 21
	s_add_u32 s97, s10, s16
	v_readlane_b32 s10, v255, 12
	s_addc_u32 vcc_lo, s10, 0
	v_readlane_b32 s10, v255, 23
	s_add_i32 s16, s2, s10
	s_mul_hi_i32 s17, s16, 0x1800
	s_mulk_i32 s16, 0x1800
	s_add_u32 s16, s97, s16
	s_addc_u32 s17, vcc_lo, s17
	s_add_i32 vcc_hi, s73, s78
	s_nop 4
	s_mov_b32 s10, m0
	s_mov_b32 m0, vcc_hi
	s_nop 0
	global_load_lds_dwordx4 v46, s[16:17]
	s_mov_b32 m0, s10
	s_nop 0
	v_readlane_b32 s10, v255, 27
	s_add_i32 s10, s2, s10
	s_mul_hi_i32 s11, s10, 0x1800
	s_mulk_i32 s10, 0x1800
	s_add_u32 s16, s97, s10
	s_addc_u32 s17, vcc_lo, s11
	s_add_i32 s10, s73, s80
	s_nop 4
	s_mov_b32 m0, s10
	s_nop 0
	global_load_lds_dwordx4 v47, s[16:17]
	v_readlane_b32 s10, v255, 25
	s_add_i32 s10, s2, s10
	s_mul_hi_i32 s11, s10, 0x1800
	s_mulk_i32 s10, 0x1800
	s_add_u32 s16, s97, s10
	s_addc_u32 s17, vcc_lo, s11
	s_add_i32 s10, s73, s83
	s_nop 4
	s_mov_b32 m0, s10
	s_nop 0
	global_load_lds_dwordx4 v48, s[16:17]
	v_readlane_b32 s10, v255, 29
	s_add_i32 s10, s2, s10
	s_mul_hi_i32 s11, s10, 0x1800
	s_mulk_i32 s10, 0x1800
	s_add_u32 s16, s97, s10
	s_addc_u32 s17, vcc_lo, s11
	s_add_i32 s73, s73, s84
	s_mov_b32 m0, s73
	s_nop 0
	global_load_lds_dwordx4 v49, s[16:17]
	s_nop 0
	v_readlane_b32 s10, v255, 8
	v_readlane_b32 s11, v255, 9
	s_andn2_b64 vcc, exec, s[10:11]
	s_cbranch_vccnz .LBB0_406
	v_readlane_b32 s10, v255, 19
	s_add_i32 s10, s10, s3
	v_readlane_b32 s3, v255, 14
	s_add_i32 s2, s2, s3
	s_ashr_i32 s3, s2, 31
	s_lshl_b64 s[2:3], s[2:3], 7
	v_readlane_b32 s11, v255, 16
	s_add_u32 s2, s11, s2
	v_readlane_b32 s11, v255, 17
	s_addc_u32 s3, s11, s3
	s_lshl_b32 s11, s72, 6
	s_add_u32 s2, s2, s11
	s_addc_u32 s3, s3, 0
	s_nop 4
	s_mov_b32 m0, s10
	s_nop 0
	global_load_lds_dwordx4 v50, s[2:3]

.LBB0_467:
	s_or_b64 exec, exec, s[12:13]
	s_ashr_i32 s9, s56, 5
	s_bfe_u32 s66, s56, 0x20003
	s_lshl_b32 s12, s9, 3
	s_lshl_b32 s13, s66, 1
	s_bfe_u32 s19, s56, 0x10002
	s_or_b32 s12, s13, s12
	s_or_b32 s12, s12, s19
	s_mul_i32 s14, s12, 0x44
	s_ashr_i32 s15, s14, 31
	s_lshl_b64 s[12:13], s[14:15], 14
	s_add_u32 s16, s52, s12
	s_addc_u32 s17, s53, s13
	s_add_u32 s58, s16, 0x400
	s_addc_u32 s59, s17, 0
	s_add_u32 s60, s54, s12
	s_addc_u32 s61, s55, s13
	s_add_u32 s62, s60, 0x400
	s_addc_u32 s63, s61, 0
	s_lshl_b64 s[12:13], s[14:15], 13
	s_add_u32 s64, s35, s12
	s_mov_b32 m0, s25
	s_nop 0
	global_load_lds_dwordx4 v65, s[16:17]
	s_addc_u32 s65, s36, s13
	s_mov_b32 m0, s27
	s_nop 0
	global_load_lds_dwordx4 v65, s[58:59]
	s_cmp_eq_u32 s19, 0
	s_mov_b32 m0, s33
	s_nop 0
	global_load_lds_dwordx4 v65, s[60:61]
	s_cselect_b64 s[12:13], -1, 0
	s_mov_b32 m0, s34
	s_nop 0
	global_load_lds_dwordx4 v65, s[62:63]
	s_and_b64 s[16:17], s[12:13], exec
	s_mov_b32 m0, s37
	s_nop 0
	global_load_lds_dwordx4 v65, s[64:65]
	s_movk_i32 s16, 0x10c0
	s_mul_i32 s18, s9, 0x1100
	s_cselect_b32 s16, 0x1000, s16
	s_add_i32 s57, s18, s38
	s_add_i32 s16, s16, s57
	s_mul_hi_i32 s17, s16, 0x1800
	s_mulk_i32 s16, 0x1800
	s_add_u32 s16, s20, s16
	s_addc_u32 s17, s21, s17
	s_lshl_b32 s59, s66, 8
	s_lshl_b32 s58, s66, 9
	s_add_u32 s16, s16, s58
	s_addc_u32 s17, s17, 0
	s_lshl_b32 s58, s56, 6
	s_and_b32 s58, s58, 0xc0
	s_lshl_b32 s58, s58, 1
	s_add_u32 s16, s16, s58
	s_addc_u32 s17, s17, 0
	s_add_u32 s16, s16, 0x800
	s_addc_u32 s17, s17, 0
	s_mov_b32 m0, s39
	s_nop 0
	global_load_lds_dwordx4 v114, s[16:17]
	s_and_saveexec_b64 s[16:17], s[4:5]
	s_cbranch_execz .LBB0_469
	s_lshl_b64 s[60:61], s[14:15], 9
	s_add_u32 s60, s40, s60
	s_addc_u32 s61, s41, s61
	s_add_i32 s15, 0, 0xc000
	s_mov_b32 m0, s15
	s_nop 0
	global_load_lds_dwordx4 v65, s[60:61]
.LBB0_469:
	s_or_b64 exec, exec, s[16:17]
	s_or_b32 s14, s14, 1
	s_ashr_i32 s15, s14, 31
	s_lshl_b64 s[16:17], s[14:15], 14
	s_add_u32 s60, s52, s16
	s_addc_u32 s61, s53, s17
	s_nop 4
	s_mov_b32 m0, s42
	s_nop 0
	global_load_lds_dwordx4 v65, s[60:61]
	s_add_u32 s60, s60, 0x400
	s_addc_u32 s61, s61, 0
	s_add_u32 s16, s54, s16
	s_mov_b32 m0, s43
	s_nop 0
	global_load_lds_dwordx4 v65, s[60:61]
	s_addc_u32 s17, s55, s17
	s_mov_b32 m0, s44
	s_nop 0
	global_load_lds_dwordx4 v65, s[16:17]
	s_add_u32 s16, s16, 0x400
	s_addc_u32 s17, s17, 0
	s_mov_b32 m0, s45
	s_nop 0
	global_load_lds_dwordx4 v65, s[16:17]
	s_lshl_b64 s[16:17], s[14:15], 13
	s_add_u32 s16, s35, s16
	s_addc_u32 s17, s36, s17
	s_mov_b32 m0, s46
	s_nop 0
	global_load_lds_dwordx4 v65, s[16:17]
	s_lshl_b32 s16, s19, 6
	s_add_i32 s16, s57, s16
	s_addk_i32 s16, 0x1040
	s_mul_hi_i32 s17, s16, 0x1800
	s_mulk_i32 s16, 0x1800
	s_add_u32 s16, s20, s16
	s_addc_u32 s17, s21, s17
	s_lshl_b32 s19, s59, 1
	s_add_u32 s16, s16, s19
	s_addc_u32 s17, s17, 0
	s_add_u32 s16, s16, s58
	s_addc_u32 s17, s17, 0
	s_add_u32 s16, s16, 0x800
	s_addc_u32 s17, s17, 0
	s_mov_b32 m0, s47
	s_nop 0
	global_load_lds_dwordx4 v114, s[16:17]
	s_and_saveexec_b64 s[16:17], s[4:5]
	s_cbranch_execz .LBB0_471
	s_lshl_b64 s[14:15], s[14:15], 9
	s_add_u32 s14, s40, s14
	s_addc_u32 s15, s41, s15
	v_readlane_b32 s11, v254, 51
	s_nop 4
	s_mov_b32 m0, s11
	s_nop 0
	global_load_lds_dwordx4 v65, s[14:15]

.LBB0_482:
	s_bitcmp1_b32 s63, 0
	s_cselect_b64 s[14:15], -1, 0
	s_and_b64 s[16:17], s[14:15], exec
	s_cselect_b32 s16, 0xc400, 0
	s_add_i32 s16, s16, 0
	v_add_u32_e32 v16, s16, v132
	v_add_u32_e32 v17, s16, v136
	v_add_u32_e32 v18, s16, v137
	v_add3_u32 v16, v16, v133, v134
	v_add_u32_e32 v19, v17, v141
	v_add_u32_e32 v20, v18, v142
	s_barrier
	ds_read_b128 v[56:59], v19 offset:32768
	ds_read_b128 v[24:27], v20 offset:16384
	v_add_u32_e32 v20, v16, v140
	v_add_u32_e32 v21, v16, v143
	v_add_u32_e32 v22, v16, v144
	v_add_u32_e32 v23, v16, v145
	v_add_u32_e32 v16, v17, v146
	v_add_u32_e32 v17, v18, v147
	ds_read_b128 v[60:63], v16 offset:32768
	ds_read_b128 v[16:19], v17 offset:16384
	ds_read_b64_tr_b16 v[52:53], v20 offset:40960
	ds_read_b64_tr_b16 v[54:55], v20 offset:41472
	ds_read_b64_tr_b16 v[36:37], v20 offset:45056
	ds_read_b64_tr_b16 v[38:39], v20 offset:45568
	ds_read_b64_tr_b16 v[48:49], v21 offset:40960
	ds_read_b64_tr_b16 v[50:51], v21 offset:41472
	ds_read_b64_tr_b16 v[32:33], v21 offset:45056
	ds_read_b64_tr_b16 v[34:35], v21 offset:45568
	ds_read_b64_tr_b16 v[44:45], v22 offset:40960
	ds_read_b64_tr_b16 v[46:47], v22 offset:41472
	ds_read_b64_tr_b16 v[28:29], v22 offset:45056
	ds_read_b64_tr_b16 v[30:31], v22 offset:45568
	ds_read_b64_tr_b16 v[40:41], v23 offset:40960
	ds_read_b64_tr_b16 v[42:43], v23 offset:41472
	ds_read_b64_tr_b16 v[20:21], v23 offset:45056
	ds_read_b64_tr_b16 v[22:23], v23 offset:45568
	s_add_i32 s17, s16, s29
	v_add_u32_e32 v66, s17, v138
	v_add_u32_e32 v67, v66, v148
	v_add_u32_e32 v68, s50, v149
	ds_read_b128 v[74:77], v67
	ds_read_b128 v[78:81], v68
	v_add_u32_e32 v67, s51, v149
	v_add_u32_e32 v68, v66, v150
	ds_read_b128 v[90:93], v67
	ds_read_b128 v[82:85], v68
	v_add_u32_e32 v67, s50, v151
	v_add_u32_e32 v68, s51, v151
	ds_read_b128 v[98:101], v67
	ds_read_b128 v[102:105], v68
	v_add_u32_e32 v67, v66, v152
	v_add_u32_e32 v68, s50, v153
	ds_read_b128 v[86:89], v67
	ds_read_b128 v[110:113], v68
	v_add_u32_e32 v67, s51, v153
	v_add_u32_e32 v66, v66, v154
	v_add_u32_e32 v70, s50, v155
	v_add_u32_e32 v71, s51, v155
	v_add_u32_e32 v116, s16, v139
	ds_read_b128 v[106:109], v67
	ds_read_b128 v[66:69], v66
	ds_read_b128 v[94:97], v70
	ds_read_b128 v[70:73], v71
	ds_read_b128 v[116:119], v116 offset:49152
	s_waitcnt lgkmcnt(0)
	s_cmpk_gt_u32 s63, 0x41
	s_waitcnt lgkmcnt(0)
	s_barrier
	s_cbranch_scc1 .LBB0_490
	s_and_b64 s[14:15], s[14:15], exec
	v_readlane_b32 s11, v254, 48
	s_cselect_b32 s18, s11, 0
	s_add_i32 s14, s60, s62
	s_ashr_i32 s15, s14, 31
	s_lshl_b64 s[16:17], s[14:15], 14
	s_add_u32 s64, s52, s16
	s_addc_u32 s65, s53, s17
	s_add_i32 s19, s18, s24
	s_mov_b32 m0, s19
	s_nop 0
	global_load_lds_dwordx4 v65, s[64:65]
	s_add_u32 s64, s64, 0x400
	s_addc_u32 s65, s65, 0
	s_add_i32 s19, s18, s26
	s_add_u32 s16, s54, s16
	s_mov_b32 m0, s19
	s_nop 0
	global_load_lds_dwordx4 v65, s[64:65]
	s_addc_u32 s17, s55, s17
	s_add_i32 s19, s18, 0x4000
	s_add_i32 s64, s19, s24
	s_mov_b32 m0, s64
	s_nop 0
	global_load_lds_dwordx4 v65, s[16:17]
	s_add_u32 s16, s16, 0x400
	s_addc_u32 s17, s17, 0
	s_add_i32 s19, s19, s26
	s_mov_b32 m0, s19
	s_nop 0
	global_load_lds_dwordx4 v65, s[16:17]
	s_lshl_b64 s[16:17], s[14:15], 13
	s_add_u32 s16, s35, s16
	s_addc_u32 s17, s36, s17
	s_add_i32 s19, s48, s18
	s_mov_b32 m0, s19
	s_nop 0
	global_load_lds_dwordx4 v65, s[16:17]
	s_cmp_gt_u32 s63, 1
	s_mov_b64 s[16:17], -1
	s_cbranch_scc0 .LBB0_485
	s_add_i32 s19, s62, -4
	s_and_b64 s[16:17], s[12:13], exec
	s_cselect_b32 s16, s19, s61
	s_lshl_b32 s19, s16, 6
	s_mov_b64 s[16:17], 0

.LBB0_487:
	s_add_i32 s16, s19, s57
	s_mul_hi_i32 s17, s16, 0x1800
	s_mulk_i32 s16, 0x1800
	s_add_u32 s16, s58, s16
	s_addc_u32 s17, s59, s17
	s_add_u32 s16, s16, 0x800
	s_addc_u32 s17, s17, 0
	s_add_i32 s19, s49, s18
	s_nop 4
	s_mov_b32 m0, s19
	s_nop 0
	global_load_lds_dwordx4 v114, s[16:17]
	s_and_saveexec_b64 s[16:17], s[4:5]
	s_cbranch_execz .LBB0_489
	s_lshl_b64 s[14:15], s[14:15], 9
	s_add_u32 s14, s40, s14
	s_addc_u32 s15, s41, s15
	s_add_i32 s18, s18, 0xc000
	s_mov_b32 m0, s18
	s_nop 0
	global_load_lds_dwordx4 v65, s[14:15]

.LBB0_618:
	s_andn2_b64 vcc, exec, s[0:1]
	s_cbranch_vccnz .LBB0_658
	v_readlane_b32 s2, v254, 62
	v_readlane_b32 s3, v254, 63
	s_add_u32 s42, s2, 0x2000000
	s_mul_i32 s30, s67, 0x240000
	s_addc_u32 s43, s3, 0
	s_lshl_b64 s[0:1], s[30:31], 1
	s_add_u32 s0, s2, s0
	s_addc_u32 s1, s3, s1
	s_add_u32 s44, s0, 0x1fc00000
	s_addc_u32 s45, s1, 0
	s_lshl_b32 s6, s56, 10
	v_lshl_or_b32 v1, v0, 4, s6
	v_ashrrev_i32_e32 v2, 31, v1
	v_lshrrev_b32_e32 v2, 22, v2
	v_add_u32_e32 v2, v1, v2
	v_ashrrev_i32_e32 v2, 10, v2
	v_mul_i32_i24_e32 v3, 0x400, v2
	v_sub_u32_e32 v3, v1, v3
	v_lshrrev_b32_e32 v4, 4, v3
	v_bitop3_b32 v3, v4, v3, 32 bitop3:0x6c
	v_ashrrev_i32_e32 v5, 31, v3
	v_lshrrev_b32_e32 v5, 26, v5
	v_lshlrev_b32_e32 v4, 3, v2
	v_add_u32_e32 v5, v3, v5
	v_and_b32_e32 v4, -16, v4
	s_waitcnt vmcnt(0)
	v_ashrrev_i32_e32 v6, 6, v5
	v_and_b32_e32 v5, 0xc0, v5
	v_add_u32_e32 v4, v6, v4
	v_sub_u32_e32 v3, v3, v5
	s_add_i32 s47, s6, 0
	v_lshlrev_b32_e32 v2, 5, v2
	v_ashrrev_i16_sdwa v3, v193, sext(v3) dst_sel:DWORD dst_unused:UNUSED_PAD src0_sel:DWORD src1_sel:BYTE_0
	v_lshlrev_b32_e32 v5, 1, v4
	v_lshrrev_b32_e32 v7, 2, v4
	v_and_b32_e32 v6, 3, v6
	s_mov_b32 s6, 0x1fffe0
	v_and_b32_e32 v2, 32, v2
	v_bfe_i32 v3, v3, 0, 16
	v_and_b32_e32 v5, 24, v5
	v_and_b32_e32 v7, 4, v7
	v_and_or_b32 v6, v4, s6, v6
	v_or3_b32 v5, v6, v7, v5
	v_add_lshl_u32 v2, v2, v3, 1
	v_add_u32_e32 v1, 0x2000, v1
	v_lshl_add_u32 v65, v4, 11, v2
	s_waitcnt vmcnt(0)
	v_lshl_add_u32 v140, v5, 11, v2
	v_ashrrev_i32_e32 v2, 31, v1
	v_lshrrev_b32_e32 v2, 22, v2
	v_add_u32_e32 v2, v1, v2
	v_ashrrev_i32_e32 v2, 10, v2
	v_mul_i32_i24_e32 v3, 0x400, v2
	v_sub_u32_e32 v1, v1, v3
	v_lshrrev_b32_e32 v3, 4, v1
	v_bitop3_b32 v1, v3, v1, 32 bitop3:0x6c
	v_ashrrev_i32_e32 v4, 31, v1
	v_lshrrev_b32_e32 v4, 26, v4
	v_add_u32_e32 v4, v1, v4
	v_ashrrev_i32_e32 v5, 6, v4
	v_and_b32_e32 v4, 0xffc0, v4
	v_sub_u32_e32 v1, v1, v4
	s_ashr_i32 s46, s56, 2
	s_add_i32 s48, s47, 0x10000
	s_add_i32 s49, s47, 0x12000
	s_add_i32 s50, s47, 0x14000
	s_add_i32 s51, s47, 0x16000
	s_add_i32 s52, s47, 0x2000
	s_add_i32 s53, s47, 0x4000
	s_add_i32 s54, s47, 0x6000
	v_lshlrev_b32_e32 v3, 3, v2
	v_lshrrev_b16_e32 v4, 7, v1
	s_cmp_eq_u32 s46, 1
	v_and_b32_e32 v3, -16, v3
	v_and_b32_e32 v4, 1, v4
	s_cselect_b64 s[0:1], -1, 0
	s_ashr_i32 s21, s20, 31
	s_ashr_i32 s23, s22, 31
	v_add_u32_e32 v3, v5, v3
	v_add_u16_e32 v1, v1, v4
	s_lshl_b64 s[2:3], s[20:21], 19
	s_lshl_b64 s[4:5], s[22:23], 19
	v_lshlrev_b32_e32 v2, 5, v2
	v_ashrrev_i16_sdwa v1, v193, sext(v1) dst_sel:DWORD dst_unused:UNUSED_PAD src0_sel:DWORD src1_sel:BYTE_0
	v_lshlrev_b32_e32 v4, 1, v3
	v_lshrrev_b32_e32 v6, 2, v3
	v_and_b32_e32 v5, 3, v5
	s_add_u32 s26, s44, s4
	v_and_b32_e32 v2, 32, v2
	v_bfe_i32 v1, v1, 0, 16
	v_and_b32_e32 v4, 24, v4
	v_and_b32_e32 v6, 4, v6
	v_and_or_b32 v5, v3, s6, v5
	s_addc_u32 s27, s45, s5
	v_or3_b32 v4, v5, v6, v4
	v_add_lshl_u32 v1, v2, v1, 1
	s_mov_b32 m0, s48
	s_nop 0
	global_load_lds_dwordx4 v140, s[26:27]
	s_add_u32 s4, s26, 0x40000
	v_lshl_add_u32 v142, v4, 11, v1
	s_mov_b32 m0, s49
	s_nop 0
	global_load_lds_dwordx4 v142, s[26:27]
	s_addc_u32 s5, s27, 0
	s_mov_b32 m0, s50
	s_nop 0
	global_load_lds_dwordx4 v140, s[4:5]
	s_add_u32 s24, s42, s2
	s_mov_b32 m0, s51
	s_nop 0
	global_load_lds_dwordx4 v142, s[4:5]
	s_addc_u32 s25, s43, s3
	s_mov_b32 m0, s47
	s_nop 0
	global_load_lds_dwordx4 v65, s[24:25]
	s_add_u32 s2, s24, 0x40000
	v_lshl_add_u32 v141, v3, 11, v1
	s_mov_b32 m0, s52
	s_nop 0
	global_load_lds_dwordx4 v141, s[24:25]
	s_addc_u32 s3, s25, 0
	s_mov_b32 m0, s53
	s_nop 0
	global_load_lds_dwordx4 v65, s[2:3]
	s_mov_b32 s64, 0x800000
	s_mov_b32 m0, s54
	s_nop 0
	global_load_lds_dwordx4 v141, s[2:3]
	s_cmp_lg_u32 s46, 1
	s_cbranch_scc1 .LBB0_621
	s_barrier
.LBB0_621:
	v_readlane_b32 s8, v254, 62
	v_readlane_b32 s9, v254, 63
	s_add_u32 s4, s8, 0x6400000
	s_addc_u32 s5, s9, 0
	s_add_u32 s6, s8, 0x300000
	s_addc_u32 s7, s9, 0
	s_lshl_b32 s30, s67, 8
	s_lshl_b64 s[2:3], s[30:31], 2
	s_add_u32 s2, s8, s2
	s_addc_u32 s3, s9, s3
	s_add_u32 s8, s2, 0x304000
	s_addc_u32 s9, s3, 0
	s_and_b32 s21, s56, 3
	s_lshl_b32 s29, s46, 6
	s_lshl_b32 s2, s46, 13
	s_lshl_b32 s3, s21, 12
	s_add_i32 s30, s47, 0x18000
	s_add_i32 s55, s47, 0x1a000
	s_mov_b32 s10, s56
	s_add_i32 s56, s47, 0x8000
	s_add_i32 s57, s47, 0xa000
	s_add_i32 s58, s47, 0x1c000
	s_add_i32 s59, s47, 0x1e000
	s_add_i32 s60, s47, 0xc000
	s_cmp_lt_u32 s10, 4
	v_readlane_b32 s12, v255, 0
	s_cselect_b64 s[10:11], -1, 0
	s_ashr_i32 s62, s12, 31
	v_and_b32_e32 v1, 48, v0
	v_lshlrev_b32_e32 v2, 6, v0
	s_movk_i32 s12, 0x3c0
	v_lshlrev_b32_e32 v0, 2, v0
	s_add_i32 s61, s47, 0xe000
	v_and_or_b32 v1, v2, s12, v1
	v_and_b32_e32 v0, 32, v0
	v_bitop3_b32 v2, v1, s2, v0 bitop3:0xde
	s_add_u32 s2, s26, 0x80
	v_bitop3_b32 v0, v1, s3, v0 bitop3:0xde
	s_waitcnt vmcnt(2)
	s_barrier
	s_addc_u32 s3, s27, 0
	s_mov_b32 m0, s30
	s_nop 0
	global_load_lds_dwordx4 v140, s[2:3]
	s_mov_b32 s63, 0
	s_mov_b32 m0, s55
	s_nop 0
	global_load_lds_dwordx4 v142, s[2:3]
	s_add_u32 s2, s24, 0x80
	s_addc_u32 s3, s25, 0
	s_mov_b32 m0, s56
	s_nop 0
	global_load_lds_dwordx4 v65, s[2:3]
	v_add_u32_e32 v143, 0, v0
	s_mov_b32 m0, s57
	s_nop 0
	global_load_lds_dwordx4 v141, s[2:3]
	s_add_u32 s2, s26, 0x40080
	s_addc_u32 s3, s27, 0
	s_mov_b32 m0, s58
	s_nop 0
	global_load_lds_dwordx4 v140, s[2:3]
	v_add_u32_e32 v144, 0, v2
	s_mov_b32 m0, s59
	s_nop 0
	global_load_lds_dwordx4 v142, s[2:3]
	s_waitcnt vmcnt(6)
	s_barrier
	s_branch .LBB0_624

.LBB0_627:
	s_add_u32 s33, s24, s2
	s_addc_u32 s40, s25, s3
	v_add_u32_e32 v114, 0x10000, v143
	v_add_u32_e32 v133, 0x14000, v143
	s_add_u32 s18, s33, 0x100
	ds_read_b128 v[134:137], v114
	ds_read_b128 v[146:149], v114 offset:1024
	ds_read_b128 v[150:153], v114 offset:2048
	ds_read_b128 v[154:157], v114 offset:3072
	ds_read_b128 v[158:161], v133
	ds_read_b128 v[162:165], v133 offset:1024
	ds_read_b128 v[166:169], v133 offset:2048
	ds_read_b128 v[170:173], v133 offset:3072
	s_addc_u32 s19, s40, 0
	s_add_u32 s16, s33, 0x180
	s_addc_u32 s17, s40, 0
	s_add_u32 s15, s26, s2
	s_addc_u32 s23, s27, s3
	s_add_u32 s36, s15, 0x100
	s_addc_u32 s37, s23, 0
	ds_read_b128 v[174:177], v144
	ds_read_b128 v[178:181], v144 offset:1024
	ds_read_b128 v[182:185], v144 offset:2048
	ds_read_b128 v[186:189], v144 offset:3072
	ds_read_b128 v[202:205], v144 offset:4096
	ds_read_b128 v[206:209], v144 offset:5120
	ds_read_b128 v[210:213], v144 offset:6144
	ds_read_b128 v[214:217], v144 offset:7168
	s_add_u32 s38, s33, 0x40080
	s_addc_u32 s39, s40, 0
	s_mov_b32 m0, s60
	s_nop 0
	global_load_lds_dwordx4 v65, s[38:39]
	s_nop 0
	s_mov_b32 m0, s61
	s_nop 0
	global_load_lds_dwordx4 v141, s[38:39]
	s_waitcnt vmcnt(8)
	s_waitcnt lgkmcnt(0)
	s_barrier
	s_setprio 1
	s_waitcnt lgkmcnt(0)
	v_mfma_f32_16x16x32_bf16 v[128:131], v[134:137], v[174:177], v[128:131]
	v_mfma_f32_16x16x32_bf16 v[124:127], v[150:153], v[174:177], v[124:127]
	v_mfma_f32_16x16x32_bf16 v[120:123], v[134:137], v[182:185], v[120:123]
	v_mfma_f32_16x16x32_bf16 v[116:119], v[150:153], v[182:185], v[116:119]
	v_mfma_f32_16x16x32_bf16 v[110:113], v[134:137], v[202:205], v[110:113]
	v_mfma_f32_16x16x32_bf16 v[106:109], v[150:153], v[202:205], v[106:109]
	v_mfma_f32_16x16x32_bf16 v[102:105], v[134:137], v[210:213], v[102:105]
	v_mfma_f32_16x16x32_bf16 v[98:101], v[150:153], v[210:213], v[98:101]
	v_mfma_f32_16x16x32_bf16 v[128:131], v[146:149], v[178:181], v[128:131]
	v_mfma_f32_16x16x32_bf16 v[124:127], v[154:157], v[178:181], v[124:127]
	v_mfma_f32_16x16x32_bf16 v[120:123], v[146:149], v[186:189], v[120:123]
	v_mfma_f32_16x16x32_bf16 v[116:119], v[154:157], v[186:189], v[116:119]
	v_mfma_f32_16x16x32_bf16 v[110:113], v[146:149], v[206:209], v[110:113]
	v_mfma_f32_16x16x32_bf16 v[106:109], v[154:157], v[206:209], v[106:109]
	v_mfma_f32_16x16x32_bf16 v[102:105], v[146:149], v[214:217], v[102:105]
	v_mfma_f32_16x16x32_bf16 v[98:101], v[154:157], v[214:217], v[98:101]
	s_setprio 0
	s_setprio 1
	v_mfma_f32_16x16x32_bf16 v[94:97], v[158:161], v[174:177], v[94:97]
	v_mfma_f32_16x16x32_bf16 v[90:93], v[166:169], v[174:177], v[90:93]
	v_mfma_f32_16x16x32_bf16 v[86:89], v[158:161], v[182:185], v[86:89]
	v_mfma_f32_16x16x32_bf16 v[82:85], v[166:169], v[182:185], v[82:85]
	v_mfma_f32_16x16x32_bf16 v[78:81], v[158:161], v[202:205], v[78:81]
	v_mfma_f32_16x16x32_bf16 v[74:77], v[166:169], v[202:205], v[74:77]
	v_mfma_f32_16x16x32_bf16 v[70:73], v[158:161], v[210:213], v[70:73]
	v_mfma_f32_16x16x32_bf16 v[66:69], v[166:169], v[210:213], v[66:69]
	v_mfma_f32_16x16x32_bf16 v[94:97], v[162:165], v[178:181], v[94:97]
	v_mfma_f32_16x16x32_bf16 v[90:93], v[170:173], v[178:181], v[90:93]
	v_mfma_f32_16x16x32_bf16 v[86:89], v[162:165], v[186:189], v[86:89]
	v_mfma_f32_16x16x32_bf16 v[82:85], v[170:173], v[186:189], v[82:85]
	v_mfma_f32_16x16x32_bf16 v[78:81], v[162:165], v[206:209], v[78:81]
	v_mfma_f32_16x16x32_bf16 v[74:77], v[170:173], v[206:209], v[74:77]
	v_mfma_f32_16x16x32_bf16 v[70:73], v[162:165], v[214:217], v[70:73]
	v_mfma_f32_16x16x32_bf16 v[66:69], v[170:173], v[214:217], v[66:69]
	s_setprio 0
	s_barrier
	ds_read_b128 v[174:177], v144 offset:16384
	ds_read_b128 v[178:181], v144 offset:17408
	ds_read_b128 v[182:185], v144 offset:18432
	ds_read_b128 v[186:189], v144 offset:19456
	ds_read_b128 v[202:205], v144 offset:20480
	ds_read_b128 v[206:209], v144 offset:21504
	ds_read_b128 v[210:213], v144 offset:22528
	ds_read_b128 v[214:217], v144 offset:23552
	s_mov_b32 m0, s48
	s_nop 0
	global_load_lds_dwordx4 v140, s[36:37]
	s_nop 0
	s_mov_b32 m0, s49
	s_nop 0
	global_load_lds_dwordx4 v142, s[36:37]
	s_add_u32 s36, s15, 0x40100
	s_addc_u32 s37, s23, 0
	s_mov_b32 m0, s50
	s_nop 0
	global_load_lds_dwordx4 v140, s[36:37]
	s_nop 0
	s_mov_b32 m0, s51
	s_nop 0
	global_load_lds_dwordx4 v142, s[36:37]
	s_mov_b32 m0, s47
	s_nop 0
	global_load_lds_dwordx4 v65, s[18:19]
	s_nop 0
	s_mov_b32 m0, s52
	s_nop 0
	global_load_lds_dwordx4 v141, s[18:19]
	s_waitcnt vmcnt(8)
	s_waitcnt lgkmcnt(0)
	s_barrier
	s_setprio 1
	s_waitcnt lgkmcnt(0)
	v_mfma_f32_16x16x32_bf16 v[60:63], v[134:137], v[174:177], v[60:63]
	v_mfma_f32_16x16x32_bf16 v[56:59], v[150:153], v[174:177], v[56:59]
	s_waitcnt lgkmcnt(5)
	v_mfma_f32_16x16x32_bf16 v[52:55], v[134:137], v[182:185], v[52:55]
	v_mfma_f32_16x16x32_bf16 v[48:51], v[150:153], v[182:185], v[48:51]
	s_waitcnt lgkmcnt(3)
	v_mfma_f32_16x16x32_bf16 v[44:47], v[134:137], v[202:205], v[44:47]
	v_mfma_f32_16x16x32_bf16 v[40:43], v[150:153], v[202:205], v[40:43]
	s_waitcnt lgkmcnt(1)
	v_mfma_f32_16x16x32_bf16 v[36:39], v[134:137], v[210:213], v[36:39]
	v_mfma_f32_16x16x32_bf16 v[32:35], v[150:153], v[210:213], v[32:35]
	v_mfma_f32_16x16x32_bf16 v[60:63], v[146:149], v[178:181], v[60:63]
	v_mfma_f32_16x16x32_bf16 v[56:59], v[154:157], v[178:181], v[56:59]
	v_mfma_f32_16x16x32_bf16 v[52:55], v[146:149], v[186:189], v[52:55]
	v_mfma_f32_16x16x32_bf16 v[48:51], v[154:157], v[186:189], v[48:51]
	v_mfma_f32_16x16x32_bf16 v[44:47], v[146:149], v[206:209], v[44:47]
	v_mfma_f32_16x16x32_bf16 v[40:43], v[154:157], v[206:209], v[40:43]
	s_waitcnt lgkmcnt(0)
	v_mfma_f32_16x16x32_bf16 v[36:39], v[146:149], v[214:217], v[36:39]
	v_mfma_f32_16x16x32_bf16 v[32:35], v[154:157], v[214:217], v[32:35]
	s_setprio 0
	s_setprio 1
	v_mfma_f32_16x16x32_bf16 v[28:31], v[158:161], v[174:177], v[28:31]
	v_mfma_f32_16x16x32_bf16 v[24:27], v[166:169], v[174:177], v[24:27]
	v_mfma_f32_16x16x32_bf16 v[20:23], v[158:161], v[182:185], v[20:23]
	v_mfma_f32_16x16x32_bf16 v[16:19], v[166:169], v[182:185], v[16:19]
	v_mfma_f32_16x16x32_bf16 v[12:15], v[158:161], v[202:205], v[12:15]
	v_mfma_f32_16x16x32_bf16 v[8:11], v[166:169], v[202:205], v[8:11]
	v_mfma_f32_16x16x32_bf16 v[4:7], v[158:161], v[210:213], v[4:7]
	v_mfma_f32_16x16x32_bf16 v[0:3], v[166:169], v[210:213], v[0:3]
	v_mfma_f32_16x16x32_bf16 v[28:31], v[162:165], v[178:181], v[28:31]
	v_mfma_f32_16x16x32_bf16 v[24:27], v[170:173], v[178:181], v[24:27]
	v_mfma_f32_16x16x32_bf16 v[20:23], v[162:165], v[186:189], v[20:23]
	v_mfma_f32_16x16x32_bf16 v[16:19], v[170:173], v[186:189], v[16:19]
	v_mfma_f32_16x16x32_bf16 v[12:15], v[162:165], v[206:209], v[12:15]
	v_mfma_f32_16x16x32_bf16 v[8:11], v[170:173], v[206:209], v[8:11]
	v_mfma_f32_16x16x32_bf16 v[4:7], v[162:165], v[214:217], v[4:7]
	v_mfma_f32_16x16x32_bf16 v[0:3], v[170:173], v[214:217], v[0:3]
	s_setprio 0
	s_barrier
	v_add_u32_e32 v132, 0x18000, v143
	v_add_u32_e32 v134, 0x1c000, v143
	ds_read_b128 v[136:139], v132
	ds_read_b128 v[146:149], v132 offset:1024
	ds_read_b128 v[150:153], v132 offset:2048
	ds_read_b128 v[154:157], v132 offset:3072
	ds_read_b128 v[158:161], v134
	ds_read_b128 v[162:165], v134 offset:1024
	ds_read_b128 v[166:169], v134 offset:2048
	ds_read_b128 v[170:173], v134 offset:3072
	ds_read_b128 v[174:177], v144 offset:32768
	ds_read_b128 v[178:181], v144 offset:33792
	ds_read_b128 v[182:185], v144 offset:34816
	ds_read_b128 v[186:189], v144 offset:35840
	ds_read_b128 v[202:205], v144 offset:36864
	ds_read_b128 v[206:209], v144 offset:37888
	ds_read_b128 v[210:213], v144 offset:38912
	ds_read_b128 v[214:217], v144 offset:39936
	s_add_u32 s18, s33, 0x40100
	s_addc_u32 s19, s40, 0
	s_mov_b32 m0, s53
	s_nop 0
	global_load_lds_dwordx4 v65, s[18:19]
	s_nop 0
	s_mov_b32 m0, s54
	s_nop 0
	global_load_lds_dwordx4 v141, s[18:19]
	s_waitcnt vmcnt(8)
	s_waitcnt lgkmcnt(0)
	s_barrier
	s_setprio 1
	s_waitcnt lgkmcnt(0)
	v_mfma_f32_16x16x32_bf16 v[128:131], v[136:139], v[174:177], v[128:131]
	v_mfma_f32_16x16x32_bf16 v[124:127], v[150:153], v[174:177], v[124:127]
	s_waitcnt lgkmcnt(5)
	v_mfma_f32_16x16x32_bf16 v[120:123], v[136:139], v[182:185], v[120:123]
	v_mfma_f32_16x16x32_bf16 v[116:119], v[150:153], v[182:185], v[116:119]
	s_waitcnt lgkmcnt(3)
	v_mfma_f32_16x16x32_bf16 v[110:113], v[136:139], v[202:205], v[110:113]
	v_mfma_f32_16x16x32_bf16 v[106:109], v[150:153], v[202:205], v[106:109]
	s_waitcnt lgkmcnt(1)
	v_mfma_f32_16x16x32_bf16 v[102:105], v[136:139], v[210:213], v[102:105]
	v_mfma_f32_16x16x32_bf16 v[98:101], v[150:153], v[210:213], v[98:101]
	v_mfma_f32_16x16x32_bf16 v[128:131], v[146:149], v[178:181], v[128:131]
	v_mfma_f32_16x16x32_bf16 v[124:127], v[154:157], v[178:181], v[124:127]
	v_mfma_f32_16x16x32_bf16 v[120:123], v[146:149], v[186:189], v[120:123]
	v_mfma_f32_16x16x32_bf16 v[116:119], v[154:157], v[186:189], v[116:119]
	v_mfma_f32_16x16x32_bf16 v[110:113], v[146:149], v[206:209], v[110:113]
	v_mfma_f32_16x16x32_bf16 v[106:109], v[154:157], v[206:209], v[106:109]
	s_waitcnt lgkmcnt(0)
	v_mfma_f32_16x16x32_bf16 v[102:105], v[146:149], v[214:217], v[102:105]
	v_mfma_f32_16x16x32_bf16 v[98:101], v[154:157], v[214:217], v[98:101]
	s_setprio 0
	s_setprio 1
	v_mfma_f32_16x16x32_bf16 v[94:97], v[158:161], v[174:177], v[94:97]
	v_mfma_f32_16x16x32_bf16 v[90:93], v[166:169], v[174:177], v[90:93]
	v_mfma_f32_16x16x32_bf16 v[86:89], v[158:161], v[182:185], v[86:89]
	v_mfma_f32_16x16x32_bf16 v[82:85], v[166:169], v[182:185], v[82:85]
	v_mfma_f32_16x16x32_bf16 v[78:81], v[158:161], v[202:205], v[78:81]
	v_mfma_f32_16x16x32_bf16 v[74:77], v[166:169], v[202:205], v[74:77]
	v_mfma_f32_16x16x32_bf16 v[70:73], v[158:161], v[210:213], v[70:73]
	v_mfma_f32_16x16x32_bf16 v[66:69], v[166:169], v[210:213], v[66:69]
	v_mfma_f32_16x16x32_bf16 v[94:97], v[162:165], v[178:181], v[94:97]
	v_mfma_f32_16x16x32_bf16 v[90:93], v[170:173], v[178:181], v[90:93]
	v_mfma_f32_16x16x32_bf16 v[86:89], v[162:165], v[186:189], v[86:89]
	v_mfma_f32_16x16x32_bf16 v[82:85], v[170:173], v[186:189], v[82:85]
	v_mfma_f32_16x16x32_bf16 v[78:81], v[162:165], v[206:209], v[78:81]
	v_mfma_f32_16x16x32_bf16 v[74:77], v[170:173], v[206:209], v[74:77]
	v_mfma_f32_16x16x32_bf16 v[70:73], v[162:165], v[214:217], v[70:73]
	v_mfma_f32_16x16x32_bf16 v[66:69], v[170:173], v[214:217], v[66:69]
	s_setprio 0
	s_barrier
	ds_read_b128 v[174:177], v144 offset:49152
	ds_read_b128 v[178:181], v144 offset:50176
	ds_read_b128 v[182:185], v144 offset:51200
	ds_read_b128 v[186:189], v144 offset:52224
	ds_read_b128 v[202:205], v144 offset:53248
	ds_read_b128 v[206:209], v144 offset:54272
	ds_read_b128 v[210:213], v144 offset:55296
	ds_read_b128 v[214:217], v144 offset:56320
	s_add_u32 s18, s15, 0x180
	s_addc_u32 s19, s23, 0
	s_mov_b32 m0, s30
	s_nop 0
	global_load_lds_dwordx4 v140, s[18:19]
	s_nop 0
	s_mov_b32 m0, s55
	s_nop 0
	global_load_lds_dwordx4 v142, s[18:19]
	s_add_u32 s18, s15, 0x40180
	s_addc_u32 s19, s23, 0
	s_mov_b32 m0, s58
	s_nop 0
	global_load_lds_dwordx4 v140, s[18:19]
	s_nop 0
	s_mov_b32 m0, s59
	s_nop 0
	global_load_lds_dwordx4 v142, s[18:19]
	s_nop 0
	s_mov_b32 m0, s56
	s_nop 0
	global_load_lds_dwordx4 v65, s[16:17]
	s_nop 0
	s_mov_b32 m0, s57
	s_nop 0
	global_load_lds_dwordx4 v141, s[16:17]
	s_waitcnt vmcnt(8)
	s_waitcnt lgkmcnt(0)
	s_barrier
	s_setprio 1
	s_waitcnt lgkmcnt(0)
	v_mfma_f32_16x16x32_bf16 v[60:63], v[136:139], v[174:177], v[60:63]
	v_mfma_f32_16x16x32_bf16 v[56:59], v[150:153], v[174:177], v[56:59]
	s_waitcnt lgkmcnt(5)
	v_mfma_f32_16x16x32_bf16 v[52:55], v[136:139], v[182:185], v[52:55]
	v_mfma_f32_16x16x32_bf16 v[48:51], v[150:153], v[182:185], v[48:51]
	s_waitcnt lgkmcnt(3)
	v_mfma_f32_16x16x32_bf16 v[44:47], v[136:139], v[202:205], v[44:47]
	v_mfma_f32_16x16x32_bf16 v[40:43], v[150:153], v[202:205], v[40:43]
	s_waitcnt lgkmcnt(1)
	v_mfma_f32_16x16x32_bf16 v[36:39], v[136:139], v[210:213], v[36:39]
	v_mfma_f32_16x16x32_bf16 v[32:35], v[150:153], v[210:213], v[32:35]
	v_mfma_f32_16x16x32_bf16 v[60:63], v[146:149], v[178:181], v[60:63]
	v_mfma_f32_16x16x32_bf16 v[56:59], v[154:157], v[178:181], v[56:59]
	v_mfma_f32_16x16x32_bf16 v[52:55], v[146:149], v[186:189], v[52:55]
	v_mfma_f32_16x16x32_bf16 v[48:51], v[154:157], v[186:189], v[48:51]
	v_mfma_f32_16x16x32_bf16 v[44:47], v[146:149], v[206:209], v[44:47]
	v_mfma_f32_16x16x32_bf16 v[40:43], v[154:157], v[206:209], v[40:43]
	s_waitcnt lgkmcnt(0)
	v_mfma_f32_16x16x32_bf16 v[36:39], v[146:149], v[214:217], v[36:39]
	v_mfma_f32_16x16x32_bf16 v[32:35], v[154:157], v[214:217], v[32:35]
	s_setprio 0
	s_setprio 1
	v_mfma_f32_16x16x32_bf16 v[28:31], v[158:161], v[174:177], v[28:31]
	v_mfma_f32_16x16x32_bf16 v[24:27], v[166:169], v[174:177], v[24:27]
	v_mfma_f32_16x16x32_bf16 v[20:23], v[158:161], v[182:185], v[20:23]
	v_mfma_f32_16x16x32_bf16 v[16:19], v[166:169], v[182:185], v[16:19]
	v_mfma_f32_16x16x32_bf16 v[12:15], v[158:161], v[202:205], v[12:15]
	v_mfma_f32_16x16x32_bf16 v[8:11], v[166:169], v[202:205], v[8:11]
	v_mfma_f32_16x16x32_bf16 v[4:7], v[158:161], v[210:213], v[4:7]
	v_mfma_f32_16x16x32_bf16 v[0:3], v[166:169], v[210:213], v[0:3]
	v_mfma_f32_16x16x32_bf16 v[28:31], v[162:165], v[178:181], v[28:31]
	v_mfma_f32_16x16x32_bf16 v[24:27], v[170:173], v[178:181], v[24:27]
	v_mfma_f32_16x16x32_bf16 v[20:23], v[162:165], v[186:189], v[20:23]
	v_mfma_f32_16x16x32_bf16 v[16:19], v[170:173], v[186:189], v[16:19]
	v_mfma_f32_16x16x32_bf16 v[12:15], v[162:165], v[206:209], v[12:15]
	v_mfma_f32_16x16x32_bf16 v[8:11], v[170:173], v[206:209], v[8:11]
	v_mfma_f32_16x16x32_bf16 v[4:7], v[162:165], v[214:217], v[4:7]
	v_mfma_f32_16x16x32_bf16 v[0:3], v[170:173], v[214:217], v[0:3]
	s_setprio 0
	s_barrier
	s_add_i32 s13, s13, 2
	s_add_u32 s2, s2, 0x100
	s_addc_u32 s3, s3, 0
	s_cmp_lt_u32 s13, 12
	s_cbranch_scc1 .LBB0_627
	s_ashr_i32 s15, s14, 31
	s_ashr_i32 s13, s12, 31
	ds_read_b128 v[136:139], v114
	ds_read_b128 v[146:149], v114 offset:1024
	ds_read_b128 v[150:153], v114 offset:2048
	ds_read_b128 v[154:157], v114 offset:3072
	ds_read_b128 v[158:161], v133
	ds_read_b128 v[162:165], v133 offset:1024
	ds_read_b128 v[166:169], v133 offset:2048
	ds_read_b128 v[170:173], v133 offset:3072
	s_lshl_b64 s[2:3], s[14:15], 19
	s_lshl_b64 s[18:19], s[12:13], 19
	s_add_u32 s16, s42, s2
	s_addc_u32 s17, s43, s3
	s_add_u32 s18, s44, s18
	s_addc_u32 s19, s45, s19
	s_and_b64 s[2:3], s[34:35], exec
	s_cselect_b32 s36, s16, s24
	s_cselect_b32 s37, s17, s25
	s_add_u32 s2, s36, 0x80
	s_addc_u32 s3, s37, 0
	s_and_b64 s[38:39], s[34:35], exec
	s_cselect_b32 s27, s19, s27
	s_cselect_b32 s26, s18, s26
	ds_read_b128 v[174:177], v144
	ds_read_b128 v[178:181], v144 offset:1024
	ds_read_b128 v[182:185], v144 offset:2048
	ds_read_b128 v[186:189], v144 offset:3072
	ds_read_b128 v[202:205], v144 offset:4096
	ds_read_b128 v[206:209], v144 offset:5120
	ds_read_b128 v[210:213], v144 offset:6144
	ds_read_b128 v[214:217], v144 offset:7168
	s_add_u32 s24, s24, 0x40780
	s_addc_u32 s25, s25, 0
	s_mov_b32 m0, s60
	s_nop 0
	global_load_lds_dwordx4 v65, s[24:25]
	s_nop 0
	s_mov_b32 m0, s61
	s_nop 0
	global_load_lds_dwordx4 v141, s[24:25]
	s_waitcnt vmcnt(8)
	s_waitcnt lgkmcnt(0)
	s_barrier
	s_setprio 1
	s_waitcnt lgkmcnt(0)
	v_mfma_f32_16x16x32_bf16 v[128:131], v[136:139], v[174:177], v[128:131]
	v_mfma_f32_16x16x32_bf16 v[124:127], v[150:153], v[174:177], v[124:127]
	s_waitcnt lgkmcnt(3)
	v_mfma_f32_16x16x32_bf16 v[110:113], v[136:139], v[202:205], v[110:113]
	v_mfma_f32_16x16x32_bf16 v[106:109], v[150:153], v[202:205], v[106:109]
	v_mfma_f32_16x16x32_bf16 v[128:131], v[146:149], v[178:181], v[128:131]
	v_mfma_f32_16x16x32_bf16 v[124:127], v[154:157], v[178:181], v[124:127]
	v_mfma_f32_16x16x32_bf16 v[120:123], v[136:139], v[182:185], v[120:123]
	v_mfma_f32_16x16x32_bf16 v[116:119], v[150:153], v[182:185], v[116:119]
	s_waitcnt lgkmcnt(2)
	v_mfma_f32_16x16x32_bf16 v[110:113], v[146:149], v[206:209], v[110:113]
	v_mfma_f32_16x16x32_bf16 v[106:109], v[154:157], v[206:209], v[106:109]
	s_waitcnt lgkmcnt(1)
	v_mfma_f32_16x16x32_bf16 v[102:105], v[136:139], v[210:213], v[102:105]
	v_mfma_f32_16x16x32_bf16 v[98:101], v[150:153], v[210:213], v[98:101]
	v_mfma_f32_16x16x32_bf16 v[218:221], v[146:149], v[186:189], v[120:123]
	v_mfma_f32_16x16x32_bf16 v[222:225], v[154:157], v[186:189], v[116:119]
	s_waitcnt lgkmcnt(0)
	v_mfma_f32_16x16x32_bf16 v[226:229], v[146:149], v[214:217], v[102:105]
	v_mfma_f32_16x16x32_bf16 v[230:233], v[154:157], v[214:217], v[98:101]
	s_setprio 0
	s_setprio 1
	v_mfma_f32_16x16x32_bf16 v[94:97], v[158:161], v[174:177], v[94:97]
	v_mfma_f32_16x16x32_bf16 v[90:93], v[166:169], v[174:177], v[90:93]
	v_mfma_f32_16x16x32_bf16 v[78:81], v[158:161], v[202:205], v[78:81]
	v_mfma_f32_16x16x32_bf16 v[74:77], v[166:169], v[202:205], v[74:77]
	v_mfma_f32_16x16x32_bf16 v[94:97], v[162:165], v[178:181], v[94:97]
	v_mfma_f32_16x16x32_bf16 v[90:93], v[170:173], v[178:181], v[90:93]
	v_mfma_f32_16x16x32_bf16 v[86:89], v[158:161], v[182:185], v[86:89]
	v_mfma_f32_16x16x32_bf16 v[82:85], v[166:169], v[182:185], v[82:85]
	v_mfma_f32_16x16x32_bf16 v[78:81], v[162:165], v[206:209], v[78:81]
	v_mfma_f32_16x16x32_bf16 v[74:77], v[170:173], v[206:209], v[74:77]
	v_mfma_f32_16x16x32_bf16 v[70:73], v[158:161], v[210:213], v[70:73]
	v_mfma_f32_16x16x32_bf16 v[66:69], v[166:169], v[210:213], v[66:69]
	v_mfma_f32_16x16x32_bf16 v[174:177], v[162:165], v[186:189], v[86:89]
	v_mfma_f32_16x16x32_bf16 v[178:181], v[170:173], v[186:189], v[82:85]
	v_mfma_f32_16x16x32_bf16 v[182:185], v[162:165], v[214:217], v[70:73]
	v_mfma_f32_16x16x32_bf16 v[186:189], v[170:173], v[214:217], v[66:69]
	s_setprio 0
	s_barrier
	s_nop 1
	ds_read_b128 v[66:69], v144 offset:16384
	ds_read_b128 v[70:73], v144 offset:17408
	ds_read_b128 v[82:85], v144 offset:18432
	ds_read_b128 v[86:89], v144 offset:19456
	ds_read_b128 v[98:101], v144 offset:20480
	ds_read_b128 v[102:105], v144 offset:21504
	ds_read_b128 v[116:119], v144 offset:22528
	ds_read_b128 v[120:123], v144 offset:23552
	s_mov_b32 m0, s48
	s_nop 0
	global_load_lds_dwordx4 v140, s[26:27]
	s_add_u32 s24, s26, 0x40000
	s_mov_b32 m0, s49
	s_nop 0
	global_load_lds_dwordx4 v142, s[26:27]
	s_addc_u32 s25, s27, 0
	s_mov_b32 m0, s50
	s_nop 0
	global_load_lds_dwordx4 v140, s[24:25]
	s_nop 0
	s_mov_b32 m0, s51
	s_nop 0
	global_load_lds_dwordx4 v142, s[24:25]
	s_nop 0
	s_mov_b32 m0, s47
	s_nop 0
	global_load_lds_dwordx4 v65, s[36:37]
	s_nop 0
	s_mov_b32 m0, s52
	s_nop 0
	global_load_lds_dwordx4 v141, s[36:37]
	s_waitcnt vmcnt(8)
	s_waitcnt lgkmcnt(0)
	s_barrier
	s_setprio 1
	s_waitcnt lgkmcnt(0)
	v_mfma_f32_16x16x32_bf16 v[60:63], v[136:139], v[66:69], v[60:63]
	v_mfma_f32_16x16x32_bf16 v[56:59], v[150:153], v[66:69], v[56:59]
	s_waitcnt lgkmcnt(3)
	v_mfma_f32_16x16x32_bf16 v[44:47], v[136:139], v[98:101], v[44:47]
	v_mfma_f32_16x16x32_bf16 v[40:43], v[150:153], v[98:101], v[40:43]
	v_mfma_f32_16x16x32_bf16 v[60:63], v[146:149], v[70:73], v[60:63]
	v_mfma_f32_16x16x32_bf16 v[56:59], v[154:157], v[70:73], v[56:59]
	v_mfma_f32_16x16x32_bf16 v[52:55], v[136:139], v[82:85], v[52:55]
	v_mfma_f32_16x16x32_bf16 v[48:51], v[150:153], v[82:85], v[48:51]
	s_waitcnt lgkmcnt(2)
	v_mfma_f32_16x16x32_bf16 v[44:47], v[146:149], v[102:105], v[44:47]
	v_mfma_f32_16x16x32_bf16 v[40:43], v[154:157], v[102:105], v[40:43]
	s_waitcnt lgkmcnt(1)
	v_mfma_f32_16x16x32_bf16 v[36:39], v[136:139], v[116:119], v[36:39]
	v_mfma_f32_16x16x32_bf16 v[32:35], v[150:153], v[116:119], v[32:35]
	v_mfma_f32_16x16x32_bf16 v[202:205], v[146:149], v[86:89], v[52:55]
	v_mfma_f32_16x16x32_bf16 v[206:209], v[154:157], v[86:89], v[48:51]
	s_waitcnt lgkmcnt(0)
	v_mfma_f32_16x16x32_bf16 v[136:139], v[146:149], v[120:123], v[36:39]
	v_mfma_f32_16x16x32_bf16 v[146:149], v[154:157], v[120:123], v[32:35]
	s_setprio 0
	s_setprio 1
	v_mfma_f32_16x16x32_bf16 v[28:31], v[158:161], v[66:69], v[28:31]
	v_mfma_f32_16x16x32_bf16 v[24:27], v[166:169], v[66:69], v[24:27]
	v_mfma_f32_16x16x32_bf16 v[12:15], v[158:161], v[98:101], v[12:15]
	v_mfma_f32_16x16x32_bf16 v[8:11], v[166:169], v[98:101], v[8:11]
	v_mfma_f32_16x16x32_bf16 v[28:31], v[162:165], v[70:73], v[28:31]
	v_mfma_f32_16x16x32_bf16 v[24:27], v[170:173], v[70:73], v[24:27]
	v_mfma_f32_16x16x32_bf16 v[20:23], v[158:161], v[82:85], v[20:23]
	v_mfma_f32_16x16x32_bf16 v[16:19], v[166:169], v[82:85], v[16:19]
	v_mfma_f32_16x16x32_bf16 v[12:15], v[162:165], v[102:105], v[12:15]
	v_mfma_f32_16x16x32_bf16 v[8:11], v[170:173], v[102:105], v[8:11]
	v_mfma_f32_16x16x32_bf16 v[4:7], v[158:161], v[116:119], v[4:7]
	v_mfma_f32_16x16x32_bf16 v[0:3], v[166:169], v[116:119], v[0:3]
	v_mfma_f32_16x16x32_bf16 v[150:153], v[162:165], v[86:89], v[20:23]
	v_mfma_f32_16x16x32_bf16 v[154:157], v[170:173], v[86:89], v[16:19]
	v_mfma_f32_16x16x32_bf16 v[158:161], v[162:165], v[120:123], v[4:7]
	v_mfma_f32_16x16x32_bf16 v[162:165], v[170:173], v[120:123], v[0:3]
	s_setprio 0
	s_barrier
	s_nop 1
	ds_read_b128 v[0:3], v132
	ds_read_b128 v[4:7], v132 offset:1024
	ds_read_b128 v[166:169], v132 offset:2048
	ds_read_b128 v[170:173], v132 offset:3072
	ds_read_b128 v[210:213], v134
	ds_read_b128 v[214:217], v134 offset:1024
	ds_read_b128 v[244:247], v134 offset:2048
	ds_read_b128 v[132:135], v134 offset:3072
	ds_read_b128 v[16:19], v144 offset:32768
	ds_read_b128 v[20:23], v144 offset:33792
	ds_read_b128 v[32:35], v144 offset:34816
	ds_read_b128 v[36:39], v144 offset:35840
	ds_read_b128 v[48:51], v144 offset:36864
	ds_read_b128 v[52:55], v144 offset:37888
	ds_read_b128 v[248:251], v144 offset:38912
	ds_read_b128 v[194:197], v144 offset:39936
	s_add_u32 s24, s36, 0x40000
	s_addc_u32 s25, s37, 0
	s_mov_b32 m0, s53
	s_nop 0
	global_load_lds_dwordx4 v65, s[24:25]
	s_nop 0
	s_mov_b32 m0, s54
	s_nop 0
	global_load_lds_dwordx4 v141, s[24:25]
	s_waitcnt vmcnt(8)
	s_waitcnt lgkmcnt(0)
	s_barrier
	s_setprio 1
	s_waitcnt lgkmcnt(0)
	v_mfma_f32_16x16x32_bf16 v[66:69], v[0:3], v[16:19], v[128:131]
	s_waitcnt lgkmcnt(6)
	v_mfma_f32_16x16x32_bf16 v[116:119], v[4:7], v[20:23], v[66:69]
	v_mfma_f32_16x16x32_bf16 v[66:69], v[166:169], v[16:19], v[124:127]
	v_mfma_f32_16x16x32_bf16 v[120:123], v[170:173], v[20:23], v[66:69]
	s_waitcnt lgkmcnt(5)
	v_mfma_f32_16x16x32_bf16 v[66:69], v[0:3], v[32:35], v[218:221]
	s_waitcnt lgkmcnt(4)
	v_mfma_f32_16x16x32_bf16 v[98:101], v[4:7], v[36:39], v[66:69]
	v_mfma_f32_16x16x32_bf16 v[66:69], v[166:169], v[32:35], v[222:225]
	v_mfma_f32_16x16x32_bf16 v[102:105], v[170:173], v[36:39], v[66:69]
	s_waitcnt lgkmcnt(3)
	v_mfma_f32_16x16x32_bf16 v[66:69], v[0:3], v[48:51], v[110:113]
	s_waitcnt lgkmcnt(2)
	v_mfma_f32_16x16x32_bf16 v[82:85], v[4:7], v[52:55], v[66:69]
	v_mfma_f32_16x16x32_bf16 v[66:69], v[166:169], v[48:51], v[106:109]
	v_mfma_f32_16x16x32_bf16 v[86:89], v[170:173], v[52:55], v[66:69]
	s_waitcnt lgkmcnt(1)
	v_mfma_f32_16x16x32_bf16 v[66:69], v[0:3], v[248:251], v[226:229]
	v_mfma_f32_16x16x32_bf16 v[70:73], v[166:169], v[248:251], v[230:233]
	s_waitcnt lgkmcnt(0)
	v_mfma_f32_16x16x32_bf16 v[66:69], v[4:7], v[194:197], v[66:69]
	v_mfma_f32_16x16x32_bf16 v[70:73], v[170:173], v[194:197], v[70:73]
	s_setprio 0
	s_setprio 1
	v_mfma_f32_16x16x32_bf16 v[94:97], v[210:213], v[16:19], v[94:97]
	v_mfma_f32_16x16x32_bf16 v[16:19], v[244:247], v[16:19], v[90:93]
	v_mfma_f32_16x16x32_bf16 v[128:131], v[132:135], v[20:23], v[16:19]
	v_mfma_f32_16x16x32_bf16 v[16:19], v[210:213], v[32:35], v[174:177]
	v_mfma_f32_16x16x32_bf16 v[106:109], v[214:217], v[36:39], v[16:19]
	v_mfma_f32_16x16x32_bf16 v[16:19], v[244:247], v[32:35], v[178:181]
	v_mfma_f32_16x16x32_bf16 v[110:113], v[132:135], v[36:39], v[16:19]
	v_mfma_f32_16x16x32_bf16 v[16:19], v[210:213], v[48:51], v[78:81]
	v_mfma_f32_16x16x32_bf16 v[90:93], v[214:217], v[52:55], v[16:19]
	v_mfma_f32_16x16x32_bf16 v[16:19], v[244:247], v[48:51], v[74:77]
	v_mfma_f32_16x16x32_bf16 v[124:127], v[214:217], v[20:23], v[94:97]
	v_mfma_f32_16x16x32_bf16 v[94:97], v[132:135], v[52:55], v[16:19]
	v_mfma_f32_16x16x32_bf16 v[16:19], v[210:213], v[248:251], v[182:185]
	v_mfma_f32_16x16x32_bf16 v[74:77], v[214:217], v[194:197], v[16:19]
	v_mfma_f32_16x16x32_bf16 v[16:19], v[244:247], v[248:251], v[186:189]
	v_mfma_f32_16x16x32_bf16 v[78:81], v[132:135], v[194:197], v[16:19]
	s_setprio 0
	s_barrier
	ds_read_b128 v[174:177], v144 offset:49152
	ds_read_b128 v[178:181], v144 offset:50176
	ds_read_b128 v[182:185], v144 offset:51200
	ds_read_b128 v[186:189], v144 offset:52224
	ds_read_b128 v[194:197], v144 offset:53248
	ds_read_b128 v[218:221], v144 offset:54272
	ds_read_b128 v[222:225], v144 offset:55296
	ds_read_b128 v[226:229], v144 offset:56320
	s_add_u32 s24, s26, 0x80
	s_addc_u32 s25, s27, 0
	s_mov_b32 m0, s30
	s_nop 0
	global_load_lds_dwordx4 v140, s[24:25]
	s_nop 0
	s_mov_b32 m0, s55
	s_nop 0
	global_load_lds_dwordx4 v142, s[24:25]
	s_add_u32 s24, s26, 0x40080
	s_addc_u32 s25, s27, 0
	s_mov_b32 m0, s58
	s_nop 0
	global_load_lds_dwordx4 v140, s[24:25]
	s_nop 0
	s_mov_b32 m0, s59
	s_nop 0
	global_load_lds_dwordx4 v142, s[24:25]
	s_nop 0
	s_mov_b32 m0, s56
	s_nop 0
	global_load_lds_dwordx4 v65, s[2:3]
	s_nop 0
	s_mov_b32 m0, s57
	s_nop 0
	global_load_lds_dwordx4 v141, s[2:3]
	s_waitcnt vmcnt(8)
	s_waitcnt lgkmcnt(0)
	s_barrier
	s_setprio 1
	s_waitcnt lgkmcnt(0)
	v_mfma_f32_16x16x32_bf16 v[16:19], v[0:3], v[174:177], v[60:63]
	s_waitcnt lgkmcnt(6)
	v_mfma_f32_16x16x32_bf16 v[48:51], v[4:7], v[178:181], v[16:19]
	v_mfma_f32_16x16x32_bf16 v[16:19], v[166:169], v[174:177], v[56:59]
	v_mfma_f32_16x16x32_bf16 v[52:55], v[170:173], v[178:181], v[16:19]
	s_waitcnt lgkmcnt(5)
	v_mfma_f32_16x16x32_bf16 v[16:19], v[0:3], v[182:185], v[202:205]
	s_waitcnt lgkmcnt(4)
	v_mfma_f32_16x16x32_bf16 v[32:35], v[4:7], v[186:189], v[16:19]
	v_mfma_f32_16x16x32_bf16 v[16:19], v[166:169], v[182:185], v[206:209]
	v_mfma_f32_16x16x32_bf16 v[36:39], v[170:173], v[186:189], v[16:19]
	s_waitcnt lgkmcnt(3)
	v_mfma_f32_16x16x32_bf16 v[16:19], v[0:3], v[194:197], v[44:47]
	s_waitcnt lgkmcnt(1)
	v_mfma_f32_16x16x32_bf16 v[0:3], v[0:3], v[222:225], v[136:139]
	v_mfma_f32_16x16x32_bf16 v[16:19], v[4:7], v[218:221], v[16:19]
	v_mfma_f32_16x16x32_bf16 v[20:23], v[166:169], v[194:197], v[40:43]
	s_waitcnt lgkmcnt(0)
	v_mfma_f32_16x16x32_bf16 v[0:3], v[4:7], v[226:229], v[0:3]
	v_mfma_f32_16x16x32_bf16 v[4:7], v[166:169], v[222:225], v[146:149]
	v_mfma_f32_16x16x32_bf16 v[20:23], v[170:173], v[218:221], v[20:23]
	v_mfma_f32_16x16x32_bf16 v[4:7], v[170:173], v[226:229], v[4:7]
	s_setprio 0
	s_setprio 1
	v_mfma_f32_16x16x32_bf16 v[24:27], v[244:247], v[174:177], v[24:27]
	v_mfma_f32_16x16x32_bf16 v[60:63], v[132:135], v[178:181], v[24:27]
	v_mfma_f32_16x16x32_bf16 v[24:27], v[210:213], v[182:185], v[150:153]
	v_mfma_f32_16x16x32_bf16 v[28:31], v[210:213], v[174:177], v[28:31]
	v_mfma_f32_16x16x32_bf16 v[40:43], v[214:217], v[186:189], v[24:27]
	v_mfma_f32_16x16x32_bf16 v[24:27], v[244:247], v[182:185], v[154:157]
	v_mfma_f32_16x16x32_bf16 v[12:15], v[210:213], v[194:197], v[12:15]
	v_mfma_f32_16x16x32_bf16 v[8:11], v[244:247], v[194:197], v[8:11]
	v_mfma_f32_16x16x32_bf16 v[56:59], v[214:217], v[178:181], v[28:31]
	v_mfma_f32_16x16x32_bf16 v[44:47], v[132:135], v[186:189], v[24:27]
	v_mfma_f32_16x16x32_bf16 v[24:27], v[214:217], v[218:221], v[12:15]
	v_mfma_f32_16x16x32_bf16 v[28:31], v[132:135], v[218:221], v[8:11]
	v_mfma_f32_16x16x32_bf16 v[8:11], v[210:213], v[222:225], v[158:161]
	v_mfma_f32_16x16x32_bf16 v[12:15], v[244:247], v[222:225], v[162:165]
	v_mfma_f32_16x16x32_bf16 v[8:11], v[214:217], v[226:229], v[8:11]
	v_mfma_f32_16x16x32_bf16 v[12:15], v[132:135], v[226:229], v[12:15]
	s_setprio 0
	s_barrier
	s_andn2_b64 vcc, exec, s[10:11]
	s_cbranch_vccnz .LBB0_630
	s_barrier

.LBB0_818:
	s_andn2_b64 vcc, exec, s[2:3]
	s_cbranch_vccnz .LBB0_854
	s_add_i32 s2, s7, s11
	s_add_i32 s2, s2, -4
	s_cmp_gt_u32 s2, 7
	s_cbranch_scc1 .LBB0_853
	ds_read_b32 v32, v217
	ds_read_b32 v33, v217 offset:4
	ds_read_b32 v34, v217 offset:8
	ds_read_b32 v35, v217 offset:12
	ds_read_b32 v36, v217 offset:32
	ds_read_b32 v37, v217 offset:36
	ds_read_b32 v38, v217 offset:40
	ds_read_b32 v39, v217 offset:44
	ds_read_b32 v40, v217 offset:64
	ds_read_b32 v41, v217 offset:68
	ds_read_b32 v42, v217 offset:72
	ds_read_b32 v43, v217 offset:76
	ds_read_b32 v44, v217 offset:96
	ds_read_b32 v45, v217 offset:100
	ds_read_b32 v46, v217 offset:104
	ds_read_b32 v47, v217 offset:108
	ds_read_b32 v48, v217 offset:128
	ds_read_b32 v49, v217 offset:132
	ds_read_b32 v50, v217 offset:136
	ds_read_b32 v51, v217 offset:140
	ds_read_b32 v52, v217 offset:160
	ds_read_b32 v53, v217 offset:164
	ds_read_b32 v54, v217 offset:168
	ds_read_b32 v55, v217 offset:172
	ds_read_b32 v56, v217 offset:192
	ds_read_b32 v57, v217 offset:196
	ds_read_b32 v58, v217 offset:200
	ds_read_b32 v59, v217 offset:204
	ds_read_b32 v60, v217 offset:224
	ds_read_b32 v61, v217 offset:228
	ds_read_b32 v62, v217 offset:232
	ds_read_b32 v63, v217 offset:236
	s_waitcnt lgkmcnt(0)
	v_sub_f32_e32 v32, v32, v209
	v_sub_f32_e32 v33, v33, v209
	v_sub_f32_e32 v34, v34, v209
	v_sub_f32_e32 v35, v35, v209
	v_sub_f32_e32 v36, v36, v209
	v_sub_f32_e32 v37, v37, v209
	v_sub_f32_e32 v38, v38, v209
	v_sub_f32_e32 v39, v39, v209
	v_sub_f32_e32 v40, v40, v209
	v_sub_f32_e32 v41, v41, v209
	v_sub_f32_e32 v42, v42, v209
	v_sub_f32_e32 v43, v43, v209
	v_sub_f32_e32 v44, v44, v209
	v_sub_f32_e32 v45, v45, v209
	v_sub_f32_e32 v46, v46, v209
	v_sub_f32_e32 v47, v47, v209
	v_add_f32_e32 v32, v82, v32
	v_add_f32_e32 v33, v83, v33
	v_add_f32_e32 v34, v84, v34
	v_add_f32_e32 v35, v85, v35
	v_add_f32_e32 v36, v86, v36
	v_add_f32_e32 v37, v87, v37
	v_add_f32_e32 v38, v88, v38
	v_add_f32_e32 v39, v89, v39
	v_add_f32_e32 v40, v90, v40
	v_add_f32_e32 v41, v91, v41
	v_add_f32_e32 v42, v92, v42
	v_add_f32_e32 v43, v93, v43
	v_add_f32_e32 v44, v94, v44
	v_add_f32_e32 v45, v95, v45
	v_add_f32_e32 v46, v96, v46
	v_add_f32_e32 v47, v97, v47
	v_sub_f32_e32 v48, v48, v209
	v_sub_f32_e32 v49, v49, v209
	v_sub_f32_e32 v50, v50, v209
	v_sub_f32_e32 v51, v51, v209
	v_sub_f32_e32 v52, v52, v209
	v_sub_f32_e32 v53, v53, v209
	v_sub_f32_e32 v54, v54, v209
	v_sub_f32_e32 v55, v55, v209
	v_sub_f32_e32 v56, v56, v209
	v_sub_f32_e32 v57, v57, v209
	v_sub_f32_e32 v58, v58, v209
	v_sub_f32_e32 v59, v59, v209
	v_sub_f32_e32 v60, v60, v209
	v_sub_f32_e32 v61, v61, v209
	v_sub_f32_e32 v62, v62, v209
	v_sub_f32_e32 v63, v63, v209
	v_add_f32_e32 v48, v66, v48
	v_add_f32_e32 v49, v67, v49
	v_add_f32_e32 v50, v68, v50
	v_add_f32_e32 v51, v69, v51
	v_add_f32_e32 v52, v70, v52
	v_add_f32_e32 v53, v71, v53
	v_add_f32_e32 v54, v72, v54
	v_add_f32_e32 v55, v73, v55
	v_add_f32_e32 v56, v74, v56
	v_add_f32_e32 v57, v75, v57
	v_add_f32_e32 v58, v76, v58
	v_add_f32_e32 v59, v77, v59
	v_add_f32_e32 v60, v78, v60
	v_add_f32_e32 v61, v79, v61
	v_add_f32_e32 v62, v80, v62
	v_add_f32_e32 v63, v81, v63
	v_cndmask_b32_e64 v32, v64, v32, s[36:37]
	v_cndmask_b32_e64 v33, v64, v33, s[40:41]
	v_cndmask_b32_e64 v34, v64, v34, s[44:45]
	v_cndmask_b32_e64 v35, v64, v35, s[48:49]
	v_cndmask_b32_e64 v36, v64, v36, s[52:53]
	v_cndmask_b32_e64 v37, v64, v37, s[56:57]
	v_cndmask_b32_e64 v38, v64, v38, s[60:61]
	v_cndmask_b32_e64 v39, v64, v39, s[64:65]
	v_cndmask_b32_e64 v40, v64, v40, s[68:69]
	v_cndmask_b32_e64 v41, v64, v41, s[72:73]
	v_cndmask_b32_e64 v42, v64, v42, s[76:77]
	v_cndmask_b32_e64 v43, v64, v43, s[80:81]
	v_cndmask_b32_e64 v44, v64, v44, s[84:85]
	v_cndmask_b32_e64 v45, v64, v45, s[88:89]
	v_cndmask_b32_e64 v46, v64, v46, s[92:93]
	v_cndmask_b32_e64 v47, v64, v47, s[96:97]
	v_cndmask_b32_e64 v48, v64, v48, s[38:39]
	v_cndmask_b32_e64 v49, v64, v49, s[42:43]
	v_cndmask_b32_e64 v50, v64, v50, s[46:47]
	v_cndmask_b32_e64 v51, v64, v51, s[50:51]
	v_cndmask_b32_e64 v52, v64, v52, s[54:55]
	v_cndmask_b32_e64 v53, v64, v53, s[58:59]
	v_cndmask_b32_e64 v54, v64, v54, s[62:63]
	v_cndmask_b32_e64 v55, v64, v55, s[66:67]
	v_cndmask_b32_e64 v56, v64, v56, s[70:71]
	v_cndmask_b32_e64 v57, v64, v57, s[74:75]
	v_cndmask_b32_e64 v58, v64, v58, s[78:79]
	v_cndmask_b32_e64 v59, v64, v59, s[82:83]
	v_cndmask_b32_e64 v60, v64, v60, s[86:87]
	v_cndmask_b32_e64 v61, v64, v61, s[90:91]
	v_cndmask_b32_e64 v62, v64, v62, s[94:95]
	v_cndmask_b32_e64 v63, v64, v63, s[0:1]
	s_branch .LBB0_854

.LBB0_861:
	s_andn2_b64 vcc, exec, s[2:3]
	s_cbranch_vccnz .LBB0_897
	s_add_i32 s2, s7, s11
	s_add_i32 s2, s2, -11
	s_cmp_lt_u32 s2, -8
	s_cbranch_scc1 .LBB0_896
	ds_read_b32 v32, v217 offset:512
	ds_read_b32 v33, v217 offset:516
	ds_read_b32 v34, v217 offset:520
	ds_read_b32 v35, v217 offset:524
	ds_read_b32 v36, v217 offset:544
	ds_read_b32 v37, v217 offset:548
	ds_read_b32 v38, v217 offset:552
	ds_read_b32 v39, v217 offset:556
	ds_read_b32 v40, v217 offset:576
	ds_read_b32 v41, v217 offset:580
	ds_read_b32 v42, v217 offset:584
	ds_read_b32 v43, v217 offset:588
	ds_read_b32 v44, v217 offset:608
	ds_read_b32 v45, v217 offset:612
	ds_read_b32 v46, v217 offset:616
	ds_read_b32 v47, v217 offset:620
	ds_read_b32 v48, v217 offset:640
	ds_read_b32 v49, v217 offset:644
	ds_read_b32 v50, v217 offset:648
	ds_read_b32 v51, v217 offset:652
	ds_read_b32 v52, v217 offset:672
	ds_read_b32 v53, v217 offset:676
	ds_read_b32 v54, v217 offset:680
	ds_read_b32 v55, v217 offset:684
	ds_read_b32 v56, v217 offset:704
	ds_read_b32 v57, v217 offset:708
	ds_read_b32 v58, v217 offset:712
	ds_read_b32 v59, v217 offset:716
	ds_read_b32 v60, v217 offset:736
	ds_read_b32 v61, v217 offset:740
	ds_read_b32 v62, v217 offset:744
	ds_read_b32 v63, v217 offset:748
	s_waitcnt lgkmcnt(0)
	v_sub_f32_e32 v32, v32, v209
	v_sub_f32_e32 v33, v33, v209
	v_sub_f32_e32 v34, v34, v209
	v_sub_f32_e32 v35, v35, v209
	v_sub_f32_e32 v36, v36, v209
	v_sub_f32_e32 v37, v37, v209
	v_sub_f32_e32 v38, v38, v209
	v_sub_f32_e32 v39, v39, v209
	v_sub_f32_e32 v40, v40, v209
	v_sub_f32_e32 v41, v41, v209
	v_sub_f32_e32 v42, v42, v209
	v_sub_f32_e32 v43, v43, v209
	v_sub_f32_e32 v44, v44, v209
	v_sub_f32_e32 v45, v45, v209
	v_sub_f32_e32 v46, v46, v209
	v_sub_f32_e32 v47, v47, v209
	v_add_f32_e32 v32, v82, v32
	v_add_f32_e32 v33, v83, v33
	v_add_f32_e32 v34, v84, v34
	v_add_f32_e32 v35, v85, v35
	v_add_f32_e32 v36, v86, v36
	v_add_f32_e32 v37, v87, v37
	v_add_f32_e32 v38, v88, v38
	v_add_f32_e32 v39, v89, v39
	v_add_f32_e32 v40, v90, v40
	v_add_f32_e32 v41, v91, v41
	v_add_f32_e32 v42, v92, v42
	v_add_f32_e32 v43, v93, v43
	v_add_f32_e32 v44, v94, v44
	v_add_f32_e32 v45, v95, v45
	v_add_f32_e32 v46, v96, v46
	v_add_f32_e32 v47, v97, v47
	v_sub_f32_e32 v48, v48, v209
	v_sub_f32_e32 v49, v49, v209
	v_sub_f32_e32 v50, v50, v209
	v_sub_f32_e32 v51, v51, v209
	v_sub_f32_e32 v52, v52, v209
	v_sub_f32_e32 v53, v53, v209
	v_sub_f32_e32 v54, v54, v209
	v_sub_f32_e32 v55, v55, v209
	v_sub_f32_e32 v56, v56, v209
	v_sub_f32_e32 v57, v57, v209
	v_sub_f32_e32 v58, v58, v209
	v_sub_f32_e32 v59, v59, v209
	v_sub_f32_e32 v60, v60, v209
	v_sub_f32_e32 v61, v61, v209
	v_sub_f32_e32 v62, v62, v209
	v_sub_f32_e32 v63, v63, v209
	v_add_f32_e32 v48, v66, v48
	v_add_f32_e32 v49, v67, v49
	v_add_f32_e32 v50, v68, v50
	v_add_f32_e32 v51, v69, v51
	v_add_f32_e32 v52, v70, v52
	v_add_f32_e32 v53, v71, v53
	v_add_f32_e32 v54, v72, v54
	v_add_f32_e32 v55, v73, v55
	v_add_f32_e32 v56, v74, v56
	v_add_f32_e32 v57, v75, v57
	v_add_f32_e32 v58, v76, v58
	v_add_f32_e32 v59, v77, v59
	v_add_f32_e32 v60, v78, v60
	v_add_f32_e32 v61, v79, v61
	v_add_f32_e32 v62, v80, v62
	v_add_f32_e32 v63, v81, v63
	v_cndmask_b32_e64 v32, v64, v32, s[36:37]
	v_cndmask_b32_e64 v33, v64, v33, s[40:41]
	v_cndmask_b32_e64 v34, v64, v34, s[44:45]
	v_cndmask_b32_e64 v35, v64, v35, s[48:49]
	v_cndmask_b32_e64 v36, v64, v36, s[52:53]
	v_cndmask_b32_e64 v37, v64, v37, s[56:57]
	v_cndmask_b32_e64 v38, v64, v38, s[60:61]
	v_cndmask_b32_e64 v39, v64, v39, s[64:65]
	v_cndmask_b32_e64 v40, v64, v40, s[68:69]
	v_cndmask_b32_e64 v41, v64, v41, s[72:73]
	v_cndmask_b32_e64 v42, v64, v42, s[76:77]
	v_cndmask_b32_e64 v43, v64, v43, s[80:81]
	v_cndmask_b32_e64 v44, v64, v44, s[84:85]
	v_cndmask_b32_e64 v45, v64, v45, s[88:89]
	v_cndmask_b32_e64 v46, v64, v46, s[92:93]
	v_cndmask_b32_e64 v47, v64, v47, s[96:97]
	v_cndmask_b32_e64 v48, v64, v48, s[38:39]
	v_cndmask_b32_e64 v49, v64, v49, s[42:43]
	v_cndmask_b32_e64 v50, v64, v50, s[46:47]
	v_cndmask_b32_e64 v51, v64, v51, s[50:51]
	v_cndmask_b32_e64 v52, v64, v52, s[54:55]
	v_cndmask_b32_e64 v53, v64, v53, s[58:59]
	v_cndmask_b32_e64 v54, v64, v54, s[62:63]
	v_cndmask_b32_e64 v55, v64, v55, s[66:67]
	v_cndmask_b32_e64 v56, v64, v56, s[70:71]
	v_cndmask_b32_e64 v57, v64, v57, s[74:75]
	v_cndmask_b32_e64 v58, v64, v58, s[78:79]
	v_cndmask_b32_e64 v59, v64, v59, s[82:83]
	v_cndmask_b32_e64 v60, v64, v60, s[86:87]
	v_cndmask_b32_e64 v61, v64, v61, s[90:91]
	v_cndmask_b32_e64 v62, v64, v62, s[94:95]
	v_cndmask_b32_e64 v63, v64, v63, s[0:1]
	s_branch .LBB0_897

.LBB0_911:
	v_lshl_add_u64 v[32:33], v[216:217], 0, s[20:21]
	s_add_i32 s2, s6, s35
	s_mov_b32 s3, m0
	s_mov_b32 m0, s2
	s_nop 0
	global_load_lds_dwordx4 v[32:33], off
	s_mov_b32 m0, s3
	s_add_i32 s13, s7, s10
	s_add_i32 s2, s13, -4
	s_cmp_gt_u32 s2, 7
	s_cbranch_scc1 .LBB0_945
	ds_read_b32 v32, v234
	ds_read_b32 v33, v234 offset:4
	ds_read_b32 v34, v234 offset:8
	ds_read_b32 v35, v234 offset:12
	ds_read_b32 v36, v234 offset:32
	ds_read_b32 v37, v234 offset:36
	ds_read_b32 v38, v234 offset:40
	ds_read_b32 v39, v234 offset:44
	ds_read_b32 v40, v234 offset:64
	ds_read_b32 v41, v234 offset:68
	ds_read_b32 v42, v234 offset:72
	ds_read_b32 v43, v234 offset:76
	ds_read_b32 v44, v234 offset:96
	ds_read_b32 v45, v234 offset:100
	ds_read_b32 v46, v234 offset:104
	ds_read_b32 v47, v234 offset:108
	ds_read_b32 v48, v234 offset:128
	ds_read_b32 v49, v234 offset:132
	ds_read_b32 v50, v234 offset:136
	ds_read_b32 v51, v234 offset:140
	ds_read_b32 v52, v234 offset:160
	ds_read_b32 v53, v234 offset:164
	ds_read_b32 v54, v234 offset:168
	ds_read_b32 v55, v234 offset:172
	ds_read_b32 v56, v234 offset:192
	ds_read_b32 v57, v234 offset:196
	ds_read_b32 v58, v234 offset:200
	ds_read_b32 v59, v234 offset:204
	ds_read_b32 v60, v234 offset:224
	ds_read_b32 v61, v234 offset:228
	ds_read_b32 v62, v234 offset:232
	ds_read_b32 v63, v234 offset:236
	s_waitcnt lgkmcnt(0)
	v_sub_f32_e32 v32, v32, v209
	v_sub_f32_e32 v33, v33, v209
	v_sub_f32_e32 v34, v34, v209
	v_sub_f32_e32 v35, v35, v209
	v_sub_f32_e32 v36, v36, v209
	v_sub_f32_e32 v37, v37, v209
	v_sub_f32_e32 v38, v38, v209
	v_sub_f32_e32 v39, v39, v209
	v_sub_f32_e32 v40, v40, v209
	v_sub_f32_e32 v41, v41, v209
	v_sub_f32_e32 v42, v42, v209
	v_sub_f32_e32 v43, v43, v209
	v_sub_f32_e32 v44, v44, v209
	v_sub_f32_e32 v45, v45, v209
	v_sub_f32_e32 v46, v46, v209
	v_sub_f32_e32 v47, v47, v209
	v_add_f32_e32 v32, v82, v32
	v_add_f32_e32 v33, v83, v33
	v_add_f32_e32 v34, v84, v34
	v_add_f32_e32 v35, v85, v35
	v_add_f32_e32 v36, v86, v36
	v_add_f32_e32 v37, v87, v37
	v_add_f32_e32 v38, v88, v38
	v_add_f32_e32 v39, v89, v39
	v_add_f32_e32 v40, v90, v40
	v_add_f32_e32 v41, v91, v41
	v_add_f32_e32 v42, v92, v42
	v_add_f32_e32 v43, v93, v43
	v_add_f32_e32 v44, v94, v44
	v_add_f32_e32 v45, v95, v45
	v_add_f32_e32 v46, v96, v46
	v_add_f32_e32 v47, v97, v47
	v_sub_f32_e32 v48, v48, v209
	v_sub_f32_e32 v49, v49, v209
	v_sub_f32_e32 v50, v50, v209
	v_sub_f32_e32 v51, v51, v209
	v_sub_f32_e32 v52, v52, v209
	v_sub_f32_e32 v53, v53, v209
	v_sub_f32_e32 v54, v54, v209
	v_sub_f32_e32 v55, v55, v209
	v_sub_f32_e32 v56, v56, v209
	v_sub_f32_e32 v57, v57, v209
	v_sub_f32_e32 v58, v58, v209
	v_sub_f32_e32 v59, v59, v209
	v_sub_f32_e32 v60, v60, v209
	v_sub_f32_e32 v61, v61, v209
	v_sub_f32_e32 v62, v62, v209
	v_sub_f32_e32 v63, v63, v209
	v_add_f32_e32 v48, v66, v48
	v_add_f32_e32 v49, v67, v49
	v_add_f32_e32 v50, v68, v50
	v_add_f32_e32 v51, v69, v51
	v_add_f32_e32 v52, v70, v52
	v_add_f32_e32 v53, v71, v53
	v_add_f32_e32 v54, v72, v54
	v_add_f32_e32 v55, v73, v55
	v_add_f32_e32 v56, v74, v56
	v_add_f32_e32 v57, v75, v57
	v_add_f32_e32 v58, v76, v58
	v_add_f32_e32 v59, v77, v59
	v_add_f32_e32 v60, v78, v60
	v_add_f32_e32 v61, v79, v61
	v_add_f32_e32 v62, v80, v62
	v_add_f32_e32 v63, v81, v63
	v_cndmask_b32_e64 v32, v64, v32, s[36:37]
	v_cndmask_b32_e64 v33, v64, v33, s[40:41]
	v_cndmask_b32_e64 v34, v64, v34, s[44:45]
	v_cndmask_b32_e64 v35, v64, v35, s[48:49]
	v_cndmask_b32_e64 v36, v64, v36, s[52:53]
	v_cndmask_b32_e64 v37, v64, v37, s[56:57]
	v_cndmask_b32_e64 v38, v64, v38, s[60:61]
	v_cndmask_b32_e64 v39, v64, v39, s[64:65]
	v_cndmask_b32_e64 v40, v64, v40, s[68:69]
	v_cndmask_b32_e64 v41, v64, v41, s[72:73]
	v_cndmask_b32_e64 v42, v64, v42, s[76:77]
	v_cndmask_b32_e64 v43, v64, v43, s[80:81]
	v_cndmask_b32_e64 v44, v64, v44, s[84:85]
	v_cndmask_b32_e64 v45, v64, v45, s[88:89]
	v_cndmask_b32_e64 v46, v64, v46, s[92:93]
	v_cndmask_b32_e64 v47, v64, v47, s[96:97]
	v_cndmask_b32_e64 v48, v64, v48, s[38:39]
	v_cndmask_b32_e64 v49, v64, v49, s[42:43]
	v_cndmask_b32_e64 v50, v64, v50, s[46:47]
	v_cndmask_b32_e64 v51, v64, v51, s[50:51]
	v_cndmask_b32_e64 v52, v64, v52, s[54:55]
	v_cndmask_b32_e64 v53, v64, v53, s[58:59]
	v_cndmask_b32_e64 v54, v64, v54, s[62:63]
	v_cndmask_b32_e64 v55, v64, v55, s[66:67]
	v_cndmask_b32_e64 v56, v64, v56, s[70:71]
	v_cndmask_b32_e64 v57, v64, v57, s[74:75]
	v_cndmask_b32_e64 v58, v64, v58, s[78:79]
	v_cndmask_b32_e64 v59, v64, v59, s[82:83]
	v_cndmask_b32_e64 v60, v64, v60, s[86:87]
	v_cndmask_b32_e64 v61, v64, v61, s[90:91]
	v_cndmask_b32_e64 v62, v64, v62, s[94:95]
	v_cndmask_b32_e64 v63, v64, v63, s[0:1]
	s_branch .LBB0_946

.LBB0_953:
	s_add_i32 s11, s6, 0x2000
	s_cmpk_lg_i32 s6, 0x4000
	s_cselect_b32 s11, s11, 0
	s_add_i32 s14, s11, s35
	s_add_i32 s13, s13, -11
	v_lshl_add_u64 v[32:33], v[218:219], 0, s[20:21]
	s_cmp_lt_u32 s13, -8
	s_mov_b32 s13, m0
	s_mov_b32 m0, s14
	s_nop 0
	global_load_lds_dwordx4 v[32:33], off
	s_mov_b32 m0, s13
	s_cbranch_scc1 .LBB0_989
	ds_read_b32 v32, v234 offset:512
	ds_read_b32 v33, v234 offset:516
	ds_read_b32 v34, v234 offset:520
	ds_read_b32 v35, v234 offset:524
	ds_read_b32 v36, v234 offset:544
	ds_read_b32 v37, v234 offset:548
	ds_read_b32 v38, v234 offset:552
	ds_read_b32 v39, v234 offset:556
	ds_read_b32 v40, v234 offset:576
	ds_read_b32 v41, v234 offset:580
	ds_read_b32 v42, v234 offset:584
	ds_read_b32 v43, v234 offset:588
	ds_read_b32 v44, v234 offset:608
	ds_read_b32 v45, v234 offset:612
	ds_read_b32 v46, v234 offset:616
	ds_read_b32 v47, v234 offset:620
	ds_read_b32 v48, v234 offset:640
	ds_read_b32 v49, v234 offset:644
	ds_read_b32 v50, v234 offset:648
	ds_read_b32 v51, v234 offset:652
	ds_read_b32 v52, v234 offset:672
	ds_read_b32 v53, v234 offset:676
	ds_read_b32 v54, v234 offset:680
	ds_read_b32 v55, v234 offset:684
	ds_read_b32 v56, v234 offset:704
	ds_read_b32 v57, v234 offset:708
	ds_read_b32 v58, v234 offset:712
	ds_read_b32 v59, v234 offset:716
	ds_read_b32 v60, v234 offset:736
	ds_read_b32 v61, v234 offset:740
	ds_read_b32 v62, v234 offset:744
	ds_read_b32 v63, v234 offset:748
	s_waitcnt lgkmcnt(0)
	v_sub_f32_e32 v32, v32, v209
	v_sub_f32_e32 v33, v33, v209
	v_sub_f32_e32 v34, v34, v209
	v_sub_f32_e32 v35, v35, v209
	v_sub_f32_e32 v36, v36, v209
	v_sub_f32_e32 v37, v37, v209
	v_sub_f32_e32 v38, v38, v209
	v_sub_f32_e32 v39, v39, v209
	v_sub_f32_e32 v40, v40, v209
	v_sub_f32_e32 v41, v41, v209
	v_sub_f32_e32 v42, v42, v209
	v_sub_f32_e32 v43, v43, v209
	v_sub_f32_e32 v44, v44, v209
	v_sub_f32_e32 v45, v45, v209
	v_sub_f32_e32 v46, v46, v209
	v_sub_f32_e32 v47, v47, v209
	v_add_f32_e32 v32, v82, v32
	v_add_f32_e32 v33, v83, v33
	v_add_f32_e32 v34, v84, v34
	v_add_f32_e32 v35, v85, v35
	v_add_f32_e32 v36, v86, v36
	v_add_f32_e32 v37, v87, v37
	v_add_f32_e32 v38, v88, v38
	v_add_f32_e32 v39, v89, v39
	v_add_f32_e32 v40, v90, v40
	v_add_f32_e32 v41, v91, v41
	v_add_f32_e32 v42, v92, v42
	v_add_f32_e32 v43, v93, v43
	v_add_f32_e32 v44, v94, v44
	v_add_f32_e32 v45, v95, v45
	v_add_f32_e32 v46, v96, v46
	v_add_f32_e32 v47, v97, v47
	v_sub_f32_e32 v48, v48, v209
	v_sub_f32_e32 v49, v49, v209
	v_sub_f32_e32 v50, v50, v209
	v_sub_f32_e32 v51, v51, v209
	v_sub_f32_e32 v52, v52, v209
	v_sub_f32_e32 v53, v53, v209
	v_sub_f32_e32 v54, v54, v209
	v_sub_f32_e32 v55, v55, v209
	v_sub_f32_e32 v56, v56, v209
	v_sub_f32_e32 v57, v57, v209
	v_sub_f32_e32 v58, v58, v209
	v_sub_f32_e32 v59, v59, v209
	v_sub_f32_e32 v60, v60, v209
	v_sub_f32_e32 v61, v61, v209
	v_sub_f32_e32 v62, v62, v209
	v_sub_f32_e32 v63, v63, v209
	v_add_f32_e32 v48, v66, v48
	v_add_f32_e32 v49, v67, v49
	v_add_f32_e32 v50, v68, v50
	v_add_f32_e32 v51, v69, v51
	v_add_f32_e32 v52, v70, v52
	v_add_f32_e32 v53, v71, v53
	v_add_f32_e32 v54, v72, v54
	v_add_f32_e32 v55, v73, v55
	v_add_f32_e32 v56, v74, v56
	v_add_f32_e32 v57, v75, v57
	v_add_f32_e32 v58, v76, v58
	v_add_f32_e32 v59, v77, v59
	v_add_f32_e32 v60, v78, v60
	v_add_f32_e32 v61, v79, v61
	v_add_f32_e32 v62, v80, v62
	v_add_f32_e32 v63, v81, v63
	v_cndmask_b32_e64 v32, v64, v32, s[36:37]
	v_cndmask_b32_e64 v33, v64, v33, s[40:41]
	v_cndmask_b32_e64 v34, v64, v34, s[44:45]
	v_cndmask_b32_e64 v35, v64, v35, s[48:49]
	v_cndmask_b32_e64 v36, v64, v36, s[52:53]
	v_cndmask_b32_e64 v37, v64, v37, s[56:57]
	v_cndmask_b32_e64 v38, v64, v38, s[60:61]
	v_cndmask_b32_e64 v39, v64, v39, s[64:65]
	v_cndmask_b32_e64 v40, v64, v40, s[68:69]
	v_cndmask_b32_e64 v41, v64, v41, s[72:73]
	v_cndmask_b32_e64 v42, v64, v42, s[76:77]
	v_cndmask_b32_e64 v43, v64, v43, s[80:81]
	v_cndmask_b32_e64 v44, v64, v44, s[84:85]
	v_cndmask_b32_e64 v45, v64, v45, s[88:89]
	v_cndmask_b32_e64 v46, v64, v46, s[92:93]
	v_cndmask_b32_e64 v47, v64, v47, s[96:97]
	v_cndmask_b32_e64 v48, v64, v48, s[38:39]
	v_cndmask_b32_e64 v49, v64, v49, s[42:43]
	v_cndmask_b32_e64 v50, v64, v50, s[46:47]
	v_cndmask_b32_e64 v51, v64, v51, s[50:51]
	v_cndmask_b32_e64 v52, v64, v52, s[54:55]
	v_cndmask_b32_e64 v53, v64, v53, s[58:59]
	v_cndmask_b32_e64 v54, v64, v54, s[62:63]
	v_cndmask_b32_e64 v55, v64, v55, s[66:67]
	v_cndmask_b32_e64 v56, v64, v56, s[70:71]
	v_cndmask_b32_e64 v57, v64, v57, s[74:75]
	v_cndmask_b32_e64 v58, v64, v58, s[78:79]
	v_cndmask_b32_e64 v59, v64, v59, s[82:83]
	v_cndmask_b32_e64 v60, v64, v60, s[86:87]
	v_cndmask_b32_e64 v61, v64, v61, s[90:91]
	v_cndmask_b32_e64 v62, v64, v62, s[94:95]
	v_cndmask_b32_e64 v63, v64, v63, s[0:1]
	s_branch .LBB0_990

.LBB0_1005:
	v_readlane_b32 s2, v255, 25
	s_add_i32 s29, s29, s2
	v_med3_i32 v65, s29, 4, 60
	ds_read_b64_tr_b16 v[160:161], v223 offset:40960
	ds_read_b64_tr_b16 v[162:163], v223 offset:41472
	s_waitcnt lgkmcnt(9)
	v_mfma_f32_32x32x16_bf16 v[82:97], v[70:73], v[128:131], 0
	v_add_f32_e32 v74, v32, v33
	v_add_f32_e32 v74, v34, v74
	v_add_f32_e32 v74, v35, v74
	v_add_f32_e32 v74, v36, v74
	v_add_f32_e32 v74, v37, v74
	v_cvt_pk_bf16_f32 v110, v32, v33
	v_cvt_pk_bf16_f32 v111, v34, v35
	ds_read_b64_tr_b16 v[156:157], v223 offset:45056
	ds_read_b64_tr_b16 v[158:159], v223 offset:45568
	v_add_f32_e32 v32, v38, v74
	s_waitcnt lgkmcnt(10)
	v_mfma_f32_32x32x16_bf16 v[66:81], v[66:69], v[128:131], 0
	v_add_f32_e32 v32, v39, v32
	v_add_f32_e32 v32, v40, v32
	v_add_f32_e32 v32, v41, v32
	v_cvt_pk_bf16_f32 v112, v36, v37
	v_cvt_pk_bf16_f32 v113, v38, v39
	ds_read_b64_tr_b16 v[128:129], v223 offset:41984
	ds_read_b64_tr_b16 v[130:131], v223 offset:42496
	s_waitcnt lgkmcnt(11)
	v_mfma_f32_32x32x16_bf16 v[82:97], v[152:155], v[124:127], v[82:97]
	v_add_f32_e32 v32, v42, v32
	v_add_f32_e32 v32, v43, v32
	v_add_f32_e32 v32, v44, v32
	v_add_f32_e32 v32, v45, v32
	v_cvt_pk_bf16_f32 v106, v40, v41
	v_cvt_pk_bf16_f32 v107, v42, v43
	ds_read_b64_tr_b16 v[152:153], v223 offset:46080
	ds_read_b64_tr_b16 v[154:155], v223 offset:46592
	s_waitcnt lgkmcnt(12)
	v_mfma_f32_32x32x16_bf16 v[66:81], v[148:151], v[124:127], v[66:81]
	v_add_f32_e32 v32, v46, v32
	v_add_f32_e32 v32, v47, v32
	v_add_f32_e32 v32, v48, v32
	v_add_f32_e32 v32, v49, v32
	v_cvt_pk_bf16_f32 v108, v44, v45
	v_cvt_pk_bf16_f32 v109, v46, v47
	ds_read_b64_tr_b16 v[124:125], v223 offset:43008
	ds_read_b64_tr_b16 v[126:127], v223 offset:43520
	s_waitcnt lgkmcnt(13)
	v_mfma_f32_32x32x16_bf16 v[82:97], v[144:147], v[120:123], v[82:97]
	v_add_f32_e32 v32, v50, v32
	v_add_f32_e32 v32, v51, v32
	v_add_f32_e32 v32, v52, v32
	v_add_f32_e32 v32, v53, v32
	v_cvt_pk_bf16_f32 v102, v48, v49
	v_cvt_pk_bf16_f32 v103, v50, v51
	ds_read_b64_tr_b16 v[144:145], v223 offset:47104
	ds_read_b64_tr_b16 v[146:147], v223 offset:47616
	s_waitcnt lgkmcnt(14)
	v_mfma_f32_32x32x16_bf16 v[66:81], v[140:143], v[120:123], v[66:81]
	v_add_f32_e32 v32, v54, v32
	v_add_f32_e32 v32, v55, v32
	v_add_f32_e32 v32, v56, v32
	v_add_f32_e32 v32, v57, v32
	v_cvt_pk_bf16_f32 v104, v52, v53
	v_cvt_pk_bf16_f32 v105, v54, v55
	ds_read_b64_tr_b16 v[120:121], v223 offset:44032
	ds_read_b64_tr_b16 v[122:123], v223 offset:44544
	s_waitcnt lgkmcnt(14)
	v_mfma_f32_32x32x16_bf16 v[82:97], v[136:139], v[116:119], v[82:97]
	v_add_f32_e32 v32, v58, v32
	v_add_f32_e32 v32, v59, v32
	v_add_f32_e32 v32, v60, v32
	v_add_f32_e32 v32, v61, v32
	v_cvt_pk_bf16_f32 v98, v56, v57
	v_cvt_pk_bf16_f32 v99, v58, v59
	ds_read_b64_tr_b16 v[136:137], v223 offset:48128
	ds_read_b64_tr_b16 v[138:139], v223 offset:48640
	v_mfma_f32_32x32x16_bf16 v[66:81], v[132:135], v[116:119], v[66:81]
	v_add_f32_e32 v32, v62, v32
	v_add_f32_e32 v32, v63, v32
	v_add_f32_e32 v116, 0, v32
	v_cvt_pk_bf16_f32 v100, v60, v61
	v_cvt_pk_bf16_f32 v101, v62, v63
	v_sub_u32_e32 v32, v246, v65
	v_add_u32_e32 v32, 11, v32
	v_cmp_lt_u32_e32 vcc, 7, v32
	v_readlane_b32 s8, v255, 27
	s_cbranch_vccnz .LBB0_1039
	v_subrev_u32_e32 v32, s29, v246
	v_lshlrev_b32_e32 v32, 9, v32
	v_add_u32_e32 v49, v228, v32
	ds_read_b32 v32, v49 offset:3836
	ds_read_b32 v33, v49 offset:3840
	ds_read_b32 v34, v49 offset:3844
	ds_read_b32 v35, v49 offset:3848
	ds_read_b32 v36, v49 offset:3868
	ds_read_b32 v37, v49 offset:3872
	ds_read_b32 v38, v49 offset:3876
	ds_read_b32 v39, v49 offset:3880
	ds_read_b32 v40, v49 offset:3900
	ds_read_b32 v41, v49 offset:3904
	ds_read_b32 v42, v49 offset:3908
	ds_read_b32 v43, v49 offset:3912
	ds_read_b32 v44, v49 offset:3932
	ds_read_b32 v45, v49 offset:3936
	ds_read_b32 v46, v49 offset:3940
	ds_read_b32 v47, v49 offset:3944
	ds_read_b32 v48, v49 offset:3964
	ds_read_b32 v50, v49 offset:3968
	ds_read_b32 v51, v49 offset:3972
	ds_read_b32 v52, v49 offset:3976
	ds_read_b32 v53, v49 offset:3996
	ds_read_b32 v54, v49 offset:4000
	ds_read_b32 v55, v49 offset:4004
	ds_read_b32 v56, v49 offset:4008
	ds_read_b32 v57, v49 offset:4028
	ds_read_b32 v58, v49 offset:4032
	ds_read_b32 v59, v49 offset:4036
	ds_read_b32 v60, v49 offset:4040
	ds_read_b32 v61, v49 offset:4060
	ds_read_b32 v62, v49 offset:4064
	ds_read_b32 v65, v49 offset:4068
	ds_read_b32 v63, v49 offset:4072
	s_waitcnt lgkmcnt(0)
	v_sub_f32_e32 v32, v32, v209
	v_sub_f32_e32 v33, v33, v209
	v_sub_f32_e32 v34, v34, v209
	v_sub_f32_e32 v35, v35, v209
	v_sub_f32_e32 v36, v36, v209
	v_sub_f32_e32 v37, v37, v209
	v_sub_f32_e32 v38, v38, v209
	v_sub_f32_e32 v39, v39, v209
	v_sub_f32_e32 v40, v40, v209
	v_sub_f32_e32 v41, v41, v209
	v_sub_f32_e32 v42, v42, v209
	v_sub_f32_e32 v43, v43, v209
	v_sub_f32_e32 v44, v44, v209
	v_sub_f32_e32 v45, v45, v209
	v_sub_f32_e32 v46, v46, v209
	v_sub_f32_e32 v47, v47, v209
	v_add_f32_e32 v32, v82, v32
	v_add_f32_e32 v33, v83, v33
	v_add_f32_e32 v34, v84, v34
	v_add_f32_e32 v35, v85, v35
	v_add_f32_e32 v36, v86, v36
	v_add_f32_e32 v37, v87, v37
	v_add_f32_e32 v38, v88, v38
	v_add_f32_e32 v39, v89, v39
	v_add_f32_e32 v40, v90, v40
	v_add_f32_e32 v41, v91, v41
	v_add_f32_e32 v42, v92, v42
	v_add_f32_e32 v43, v93, v43
	v_add_f32_e32 v44, v94, v44
	v_add_f32_e32 v45, v95, v45
	v_add_f32_e32 v46, v96, v46
	v_add_f32_e32 v47, v97, v47
	v_sub_f32_e32 v48, v48, v209
	v_sub_f32_e32 v49, v50, v209
	v_sub_f32_e32 v50, v51, v209
	v_sub_f32_e32 v51, v52, v209
	v_sub_f32_e32 v52, v53, v209
	v_sub_f32_e32 v53, v54, v209
	v_sub_f32_e32 v54, v55, v209
	v_sub_f32_e32 v55, v56, v209
	v_sub_f32_e32 v56, v57, v209
	v_sub_f32_e32 v57, v58, v209
	v_sub_f32_e32 v58, v59, v209
	v_sub_f32_e32 v59, v60, v209
	v_sub_f32_e32 v60, v61, v209
	v_sub_f32_e32 v61, v62, v209
	v_sub_f32_e32 v62, v65, v209
	v_sub_f32_e32 v63, v63, v209
	v_add_f32_e32 v48, v66, v48
	v_add_f32_e32 v49, v67, v49
	v_add_f32_e32 v50, v68, v50
	v_add_f32_e32 v51, v69, v51
	v_add_f32_e32 v52, v70, v52
	v_add_f32_e32 v53, v71, v53
	v_add_f32_e32 v54, v72, v54
	v_add_f32_e32 v55, v73, v55
	v_add_f32_e32 v56, v74, v56
	v_add_f32_e32 v57, v75, v57
	v_add_f32_e32 v58, v76, v58
	v_add_f32_e32 v59, v77, v59
	v_add_f32_e32 v60, v78, v60
	v_add_f32_e32 v61, v79, v61
	v_add_f32_e32 v62, v80, v62
	v_add_f32_e32 v63, v81, v63
	v_cndmask_b32_e64 v32, v64, v32, s[36:37]
	v_cndmask_b32_e64 v33, v64, v33, s[40:41]
	v_cndmask_b32_e64 v34, v64, v34, s[44:45]
	v_cndmask_b32_e64 v35, v64, v35, s[48:49]
	v_cndmask_b32_e64 v36, v64, v36, s[52:53]
	v_cndmask_b32_e64 v37, v64, v37, s[56:57]
	v_cndmask_b32_e64 v38, v64, v38, s[60:61]
	v_cndmask_b32_e64 v39, v64, v39, s[64:65]
	v_cndmask_b32_e64 v40, v64, v40, s[68:69]
	v_cndmask_b32_e64 v41, v64, v41, s[72:73]
	v_cndmask_b32_e64 v42, v64, v42, s[76:77]
	v_cndmask_b32_e64 v43, v64, v43, s[80:81]
	v_cndmask_b32_e64 v44, v64, v44, s[84:85]
	v_cndmask_b32_e64 v45, v64, v45, s[88:89]
	v_cndmask_b32_e64 v46, v64, v46, s[92:93]
	v_cndmask_b32_e64 v47, v64, v47, s[96:97]
	v_cndmask_b32_e64 v48, v64, v48, s[38:39]
	v_cndmask_b32_e64 v49, v64, v49, s[42:43]
	v_cndmask_b32_e64 v50, v64, v50, s[46:47]
	v_cndmask_b32_e64 v51, v64, v51, s[50:51]
	v_cndmask_b32_e64 v52, v64, v52, s[54:55]
	v_cndmask_b32_e64 v53, v64, v53, s[58:59]
	v_cndmask_b32_e64 v54, v64, v54, s[62:63]
	v_cndmask_b32_e64 v55, v64, v55, s[66:67]
	v_cndmask_b32_e64 v56, v64, v56, s[70:71]
	v_cndmask_b32_e64 v57, v64, v57, s[74:75]
	v_cndmask_b32_e64 v58, v64, v58, s[78:79]
	v_cndmask_b32_e64 v59, v64, v59, s[82:83]
	v_cndmask_b32_e64 v60, v64, v60, s[86:87]
	v_cndmask_b32_e64 v61, v64, v61, s[90:91]
	v_cndmask_b32_e64 v62, v64, v62, s[94:95]
	v_cndmask_b32_e64 v63, v64, v63, s[0:1]
	s_branch .LBB0_1040

.LBB0_1101:
	s_andn2_b64 vcc, exec, s[0:1]
	s_cbranch_vccnz .LBB0_1184
	v_readlane_b32 s0, v254, 59
	s_cmp_eq_u32 s0, 3
	s_cselect_b64 s[4:5], -1, 0
	s_and_b64 s[0:1], s[4:5], exec
	s_movk_i32 s0, 0x220
	s_cselect_b32 s30, 0x200, s0
	v_readlane_b32 s6, v255, 0
	s_cmp_ge_i32 s6, s30
	v_mbcnt_lo_u32_b32 v0, -1, 0
	v_mbcnt_hi_u32_b32 v0, -1, v0
	s_cbranch_scc1 .LBB0_1122
	v_readlane_b32 s2, v254, 62
	v_readlane_b32 s3, v254, 63
	s_add_u32 s29, s2, 0x13000000
	v_readlane_b32 s0, v255, 1
	s_addc_u32 s36, s3, 0
	v_readlane_b32 s1, v255, 2
	s_and_b64 s[0:1], s[0:1], exec
	s_mov_b32 s0, 0x20500000
	s_cselect_b32 s0, s0, 0x21600000
	s_add_u32 s0, s2, s0
	s_addc_u32 s1, s3, 0
	s_lshl_b32 s2, s67, 21
	s_add_u32 s37, s0, s2
	s_addc_u32 s38, s1, 0
	s_and_b64 s[0:1], s[4:5], exec
	s_movk_i32 s0, 0x88
	s_cselect_b32 s39, 0x80, s0
	s_lshl_b32 s8, s56, 10
	v_lshl_or_b32 v1, v0, 4, s8
	v_ashrrev_i32_e32 v2, 31, v1
	v_lshrrev_b32_e32 v2, 22, v2
	v_add_u32_e32 v2, v1, v2
	v_ashrrev_i32_e32 v2, 10, v2
	v_mul_i32_i24_e32 v3, 0x400, v2
	v_sub_u32_e32 v3, v1, v3
	v_lshrrev_b32_e32 v4, 4, v3
	v_bitop3_b32 v3, v4, v3, 32 bitop3:0x6c
	v_ashrrev_i32_e32 v5, 31, v3
	v_lshrrev_b32_e32 v5, 26, v5
	v_lshlrev_b32_e32 v4, 3, v2
	v_add_u32_e32 v5, v3, v5
	v_and_b32_e32 v4, -16, v4
	s_waitcnt vmcnt(0)
	v_ashrrev_i32_e32 v6, 6, v5
	v_and_b32_e32 v5, 0xc0, v5
	v_add_u32_e32 v4, v6, v4
	v_sub_u32_e32 v3, v3, v5
	v_lshlrev_b32_e32 v2, 5, v2
	v_ashrrev_i16_sdwa v3, v193, sext(v3) dst_sel:DWORD dst_unused:UNUSED_PAD src0_sel:DWORD src1_sel:BYTE_0
	v_lshlrev_b32_e32 v5, 1, v4
	v_lshrrev_b32_e32 v7, 2, v4
	v_and_b32_e32 v6, 3, v6
	s_mov_b32 s0, 0x1fffe0
	v_and_b32_e32 v2, 32, v2
	v_bfe_i32 v3, v3, 0, 16
	v_and_b32_e32 v5, 24, v5
	v_and_b32_e32 v7, 4, v7
	v_and_or_b32 v6, v4, s0, v6
	v_or3_b32 v5, v6, v7, v5
	v_add_lshl_u32 v2, v2, v3, 1
	v_add_u32_e32 v1, 0x2000, v1
	v_lshl_add_u32 v65, v4, 11, v2
	v_lshl_add_u32 v114, v5, 11, v2
	v_ashrrev_i32_e32 v2, 31, v1
	v_lshrrev_b32_e32 v2, 22, v2
	v_add_u32_e32 v2, v1, v2
	v_ashrrev_i32_e32 v2, 10, v2
	v_mul_i32_i24_e32 v3, 0x400, v2
	v_sub_u32_e32 v1, v1, v3
	v_lshrrev_b32_e32 v3, 4, v1
	v_bitop3_b32 v1, v3, v1, 32 bitop3:0x6c
	v_ashrrev_i32_e32 v4, 31, v1
	v_lshrrev_b32_e32 v4, 26, v4
	v_lshlrev_b32_e32 v3, 3, v2
	v_add_u32_e32 v4, v1, v4
	v_and_b32_e32 v3, -16, v3
	v_ashrrev_i32_e32 v5, 6, v4
	v_add_u32_e32 v3, v5, v3
	v_and_b32_e32 v5, 3, v5
	s_ashr_i32 s41, s6, 31
	v_and_or_b32 v5, v3, s0, v5
	s_lshr_b32 s0, s41, 29
	s_add_i32 s0, s6, s0
	s_lshr_b32 s40, s30, 3
	s_ashr_i32 s2, s0, 3
	s_and_b32 s0, s0, -8
	s_ashr_i32 s1, s56, 2
	s_sub_i32 s0, s6, s0
	s_or_b32 s42, s40, 1
	s_cmp_lt_i32 s0, 0
	s_cselect_b32 s3, s42, s40
	s_mul_i32 s0, s0, s3
	s_add_i32 s0, s0, s2
	v_and_b32_e32 v4, 0xffc0, v4
	s_ashr_i32 s2, s0, 31
	v_sub_u32_e32 v1, v1, v4
	s_lshr_b32 s2, s2, 27
	v_lshrrev_b16_e32 v4, 7, v1
	s_add_i32 s2, s0, s2
	v_and_b32_e32 v4, 1, v4
	s_ashr_i32 s3, s2, 5
	v_add_u16_e32 v1, v1, v4
	s_lshl_b32 s6, s3, 3
	v_lshlrev_b32_e32 v2, 5, v2
	v_ashrrev_i16_sdwa v1, v193, sext(v1) dst_sel:DWORD dst_unused:UNUSED_PAD src0_sel:DWORD src1_sel:BYTE_0
	v_lshlrev_b32_e32 v4, 1, v3
	v_lshrrev_b32_e32 v6, 2, v3
	s_sub_i32 s3, s39, s6
	v_and_b32_e32 v2, 32, v2
	v_bfe_i32 v1, v1, 0, 16
	v_and_b32_e32 v4, 24, v4
	v_and_b32_e32 v6, 4, v6
	s_min_u32 s7, s3, 8
	s_andn2_b32 s2, s2, 31
	v_or3_b32 v4, v5, v6, v4
	v_add_lshl_u32 v1, v2, v1, 1
	s_sub_i32 s9, s0, s2
	v_cvt_f32_ubyte0_e32 v2, s7
	v_lshl_add_u32 v202, v3, 11, v1
	v_lshl_add_u32 v203, v4, 11, v1
	v_cvt_f32_i32_e32 v1, s9
	v_rcp_iflag_f32_e32 v3, v2
	s_ashr_i32 s0, s9, 30
	s_or_b32 s0, s0, 1
	v_mul_f32_e32 v3, v1, v3
	v_trunc_f32_e32 v3, v3
	v_fma_f32 v1, -v3, v2, v1
	v_cvt_i32_f32_e32 v3, v3
	v_cmp_ge_f32_e64 s[2:3], |v1|, v2
	s_and_b64 s[2:3], s[2:3], exec
	s_cselect_b32 s0, s0, 0
	v_readfirstlane_b32 s2, v3
	s_add_i32 s0, s2, s0
	s_mul_i32 s2, s0, s7
	s_sub_i32 s2, s9, s2
	s_sext_i32_i8 s2, s2
	s_add_i32 s6, s6, s2
	s_ashr_i32 s7, s6, 4
	s_and_b64 s[2:3], s[4:5], exec
	s_cselect_b32 s2, s7, 0
	s_add_i32 s22, s2, s6
	s_ashr_i32 s23, s22, 31
	s_bfe_i64 s[6:7], s[0:1], 0x80000
	s_lshl_b64 s[2:3], s[22:23], 19
	s_lshl_b64 s[6:7], s[6:7], 19
	s_add_u32 s24, s37, s6
	s_addc_u32 s25, s38, s7
	s_add_i32 s43, s8, 0
	s_add_i32 s44, s43, 0x10000
	s_mov_b32 m0, s44
	s_nop 0
	global_load_lds_dwordx4 v114, s[24:25]
	s_add_i32 s45, s43, 0x12000
	s_mov_b32 m0, s45
	s_nop 0
	global_load_lds_dwordx4 v203, s[24:25]
	s_add_u32 s6, s24, 0x40000
	s_addc_u32 s7, s25, 0
	s_add_i32 s46, s43, 0x14000
	s_mov_b32 m0, s46
	s_nop 0
	global_load_lds_dwordx4 v114, s[6:7]
	s_add_i32 s47, s43, 0x16000
	s_mov_b32 m0, s47
	s_nop 0
	global_load_lds_dwordx4 v203, s[6:7]
	s_add_u32 s26, s29, s2
	s_addc_u32 s27, s36, s3
	s_mov_b32 m0, s43
	s_nop 0
	global_load_lds_dwordx4 v65, s[26:27]
	s_add_i32 s48, s43, 0x2000
	s_mov_b32 m0, s48
	s_nop 0
	global_load_lds_dwordx4 v202, s[26:27]
	s_add_u32 s2, s26, 0x40000
	s_addc_u32 s3, s27, 0
	s_add_i32 s49, s43, 0x4000
	s_mov_b32 m0, s49
	s_nop 0
	global_load_lds_dwordx4 v65, s[2:3]
	s_add_i32 s50, s43, 0x6000
	s_mov_b32 m0, s50
	s_nop 0
	global_load_lds_dwordx4 v202, s[2:3]
	s_cmp_eq_u32 s1, 1
	s_cselect_b64 s[6:7], -1, 0
	s_cmp_lg_u32 s1, 1
	s_cbranch_scc1 .LBB0_1105
	s_barrier
.LBB0_1105:
	s_sext_i32_i8 s23, s0
	v_readlane_b32 s10, v254, 62
	v_readlane_b32 s0, v254, 59
	v_readlane_b32 s11, v254, 63
	s_add_u32 s8, s10, 0x1b800000
	s_mul_i32 s2, s0, 0xd800
	s_mov_b32 s3, s31
	s_addc_u32 s9, s11, 0
	s_lshl_b64 s[2:3], s[2:3], 2
	s_add_u32 s51, s10, s2
	s_addc_u32 s52, s11, s3
	s_cmp_eq_u32 s0, 0
	s_cselect_b64 s[2:3], -1, 0
	s_lshl_b32 s54, s1, 6
	v_and_b32_e32 v1, 48, v0
	s_lshl_b32 s0, s1, 13
	v_lshlrev_b32_e32 v2, 6, v0
	s_movk_i32 s1, 0x3c0
	v_lshlrev_b32_e32 v0, 2, v0
	v_and_or_b32 v1, v2, s1, v1
	v_and_b32_e32 v0, 32, v0
	v_bitop3_b32 v2, v1, s0, v0 bitop3:0xde
	s_lshl_b32 s0, s56, 5
	s_and_b32 s55, s0, 0x60
	s_lshl_b32 s0, s55, 7
	v_bitop3_b32 v0, v1, s0, v0 bitop3:0xde
	s_add_u32 s0, s24, 0x80
	s_waitcnt vmcnt(2)
	s_barrier
	s_addc_u32 s1, s25, 0
	s_mov_b32 s11, s56
	s_add_i32 s56, s43, 0x18000
	s_mov_b32 m0, s56
	s_nop 0
	global_load_lds_dwordx4 v114, s[0:1]
	s_add_i32 s57, s43, 0x1a000
	s_mov_b32 m0, s57
	s_nop 0
	global_load_lds_dwordx4 v203, s[0:1]
	s_add_u32 s0, s26, 0x80
	s_addc_u32 s1, s27, 0
	s_add_i32 s58, s43, 0x8000
	s_mov_b32 m0, s58
	s_nop 0
	global_load_lds_dwordx4 v65, s[0:1]
	s_add_i32 s59, s43, 0xa000
	s_mov_b32 m0, s59
	s_nop 0
	global_load_lds_dwordx4 v202, s[0:1]
	s_add_u32 s0, s24, 0x40080
	s_addc_u32 s1, s25, 0
	s_add_i32 s60, s43, 0x1c000
	s_mov_b32 m0, s60
	s_nop 0
	global_load_lds_dwordx4 v114, s[0:1]
	s_add_i32 s61, s43, 0x1e000
	s_mov_b32 m0, s61
	s_nop 0
	global_load_lds_dwordx4 v203, s[0:1]
	s_waitcnt vmcnt(6)
	s_add_i32 s62, s43, 0xc000
	v_readlane_b32 s0, v254, 45
	s_cmp_lt_u32 s11, 4
	v_readlane_b32 s1, v254, 46
	s_mov_b32 s53, 0
	s_cselect_b64 s[10:11], -1, 0
	s_add_i32 s63, s43, 0xe000
	s_and_b64 s[12:13], s[2:3], s[0:1]
	v_add_u32_e32 v204, 0, v0
	v_add_u32_e32 v205, 0, v2
	s_barrier
	s_branch .LBB0_1108

.LBB0_1111:
	s_add_u32 s66, s26, s2
	s_addc_u32 s67, s27, s3
	s_nop 0
	v_add_u32_e32 v132, 0x10000, v204
	v_add_u32_e32 v134, 0x14000, v204
	s_add_u32 s20, s66, 0x100
	ds_read_b128 v[136:139], v132
	ds_read_b128 v[140:143], v132 offset:1024
	ds_read_b128 v[144:147], v132 offset:2048
	ds_read_b128 v[148:151], v132 offset:3072
	ds_read_b128 v[152:155], v134
	ds_read_b128 v[156:159], v134 offset:1024
	ds_read_b128 v[160:163], v134 offset:2048
	ds_read_b128 v[164:167], v134 offset:3072
	s_addc_u32 s21, s67, 0
	s_add_u32 s18, s66, 0x180
	s_addc_u32 s19, s67, 0
	s_add_u32 s17, s24, s2
	s_addc_u32 s33, s25, s3
	s_add_u32 s34, s17, 0x100
	s_addc_u32 s35, s33, 0
	ds_read_b128 v[168:171], v205
	ds_read_b128 v[172:175], v205 offset:1024
	ds_read_b128 v[176:179], v205 offset:2048
	ds_read_b128 v[180:183], v205 offset:3072
	ds_read_b128 v[184:187], v205 offset:4096
	ds_read_b128 v[188:191], v205 offset:5120
	ds_read_b128 v[194:197], v205 offset:6144
	ds_read_b128 v[198:201], v205 offset:7168
	s_add_u32 s64, s66, 0x40080
	s_addc_u32 s65, s67, 0
	s_mov_b32 m0, s62
	s_nop 0
	global_load_lds_dwordx4 v65, s[64:65]
	s_nop 0
	s_mov_b32 m0, s63
	s_nop 0
	global_load_lds_dwordx4 v202, s[64:65]
	s_waitcnt vmcnt(8)
	s_waitcnt lgkmcnt(0)
	s_barrier
	s_setprio 1
	s_waitcnt lgkmcnt(0)
	v_mfma_f32_16x16x32_bf16 v[128:131], v[136:139], v[168:171], v[128:131]
	v_mfma_f32_16x16x32_bf16 v[124:127], v[144:147], v[168:171], v[124:127]
	v_mfma_f32_16x16x32_bf16 v[120:123], v[136:139], v[176:179], v[120:123]
	v_mfma_f32_16x16x32_bf16 v[116:119], v[144:147], v[176:179], v[116:119]
	v_mfma_f32_16x16x32_bf16 v[110:113], v[136:139], v[184:187], v[110:113]
	v_mfma_f32_16x16x32_bf16 v[106:109], v[144:147], v[184:187], v[106:109]
	v_mfma_f32_16x16x32_bf16 v[102:105], v[136:139], v[194:197], v[102:105]
	v_mfma_f32_16x16x32_bf16 v[98:101], v[144:147], v[194:197], v[98:101]
	v_mfma_f32_16x16x32_bf16 v[128:131], v[140:143], v[172:175], v[128:131]
	v_mfma_f32_16x16x32_bf16 v[124:127], v[148:151], v[172:175], v[124:127]
	v_mfma_f32_16x16x32_bf16 v[120:123], v[140:143], v[180:183], v[120:123]
	v_mfma_f32_16x16x32_bf16 v[116:119], v[148:151], v[180:183], v[116:119]
	v_mfma_f32_16x16x32_bf16 v[110:113], v[140:143], v[188:191], v[110:113]
	v_mfma_f32_16x16x32_bf16 v[106:109], v[148:151], v[188:191], v[106:109]
	v_mfma_f32_16x16x32_bf16 v[102:105], v[140:143], v[198:201], v[102:105]
	v_mfma_f32_16x16x32_bf16 v[98:101], v[148:151], v[198:201], v[98:101]
	s_setprio 0
	s_setprio 1
	v_mfma_f32_16x16x32_bf16 v[94:97], v[152:155], v[168:171], v[94:97]
	v_mfma_f32_16x16x32_bf16 v[90:93], v[160:163], v[168:171], v[90:93]
	v_mfma_f32_16x16x32_bf16 v[86:89], v[152:155], v[176:179], v[86:89]
	v_mfma_f32_16x16x32_bf16 v[82:85], v[160:163], v[176:179], v[82:85]
	v_mfma_f32_16x16x32_bf16 v[78:81], v[152:155], v[184:187], v[78:81]
	v_mfma_f32_16x16x32_bf16 v[74:77], v[160:163], v[184:187], v[74:77]
	v_mfma_f32_16x16x32_bf16 v[70:73], v[152:155], v[194:197], v[70:73]
	v_mfma_f32_16x16x32_bf16 v[66:69], v[160:163], v[194:197], v[66:69]
	v_mfma_f32_16x16x32_bf16 v[94:97], v[156:159], v[172:175], v[94:97]
	v_mfma_f32_16x16x32_bf16 v[90:93], v[164:167], v[172:175], v[90:93]
	v_mfma_f32_16x16x32_bf16 v[86:89], v[156:159], v[180:183], v[86:89]
	v_mfma_f32_16x16x32_bf16 v[82:85], v[164:167], v[180:183], v[82:85]
	v_mfma_f32_16x16x32_bf16 v[78:81], v[156:159], v[188:191], v[78:81]
	v_mfma_f32_16x16x32_bf16 v[74:77], v[164:167], v[188:191], v[74:77]
	v_mfma_f32_16x16x32_bf16 v[70:73], v[156:159], v[198:201], v[70:73]
	v_mfma_f32_16x16x32_bf16 v[66:69], v[164:167], v[198:201], v[66:69]
	s_setprio 0
	s_barrier
	ds_read_b128 v[168:171], v205 offset:16384
	ds_read_b128 v[172:175], v205 offset:17408
	ds_read_b128 v[176:179], v205 offset:18432
	ds_read_b128 v[180:183], v205 offset:19456
	ds_read_b128 v[184:187], v205 offset:20480
	ds_read_b128 v[188:191], v205 offset:21504
	ds_read_b128 v[194:197], v205 offset:22528
	ds_read_b128 v[198:201], v205 offset:23552
	s_mov_b32 m0, s44
	s_nop 0
	global_load_lds_dwordx4 v114, s[34:35]
	s_nop 0
	s_mov_b32 m0, s45
	s_nop 0
	global_load_lds_dwordx4 v203, s[34:35]
	s_add_u32 s34, s17, 0x40100
	s_addc_u32 s35, s33, 0
	s_mov_b32 m0, s46
	s_nop 0
	global_load_lds_dwordx4 v114, s[34:35]
	s_nop 0
	s_mov_b32 m0, s47
	s_nop 0
	global_load_lds_dwordx4 v203, s[34:35]
	s_mov_b32 m0, s43
	s_nop 0
	global_load_lds_dwordx4 v65, s[20:21]
	s_nop 0
	s_mov_b32 m0, s48
	s_nop 0
	global_load_lds_dwordx4 v202, s[20:21]
	s_waitcnt vmcnt(8)
	s_waitcnt lgkmcnt(0)
	s_barrier
	s_setprio 1
	s_waitcnt lgkmcnt(7)
	v_mfma_f32_16x16x32_bf16 v[60:63], v[136:139], v[168:171], v[60:63]
	v_mfma_f32_16x16x32_bf16 v[56:59], v[144:147], v[168:171], v[56:59]
	s_waitcnt lgkmcnt(5)
	v_mfma_f32_16x16x32_bf16 v[52:55], v[136:139], v[176:179], v[52:55]
	v_mfma_f32_16x16x32_bf16 v[48:51], v[144:147], v[176:179], v[48:51]
	s_waitcnt lgkmcnt(3)
	v_mfma_f32_16x16x32_bf16 v[44:47], v[136:139], v[184:187], v[44:47]
	v_mfma_f32_16x16x32_bf16 v[40:43], v[144:147], v[184:187], v[40:43]
	s_waitcnt lgkmcnt(1)
	v_mfma_f32_16x16x32_bf16 v[36:39], v[136:139], v[194:197], v[36:39]
	v_mfma_f32_16x16x32_bf16 v[32:35], v[144:147], v[194:197], v[32:35]
	v_mfma_f32_16x16x32_bf16 v[60:63], v[140:143], v[172:175], v[60:63]
	v_mfma_f32_16x16x32_bf16 v[56:59], v[148:151], v[172:175], v[56:59]
	v_mfma_f32_16x16x32_bf16 v[52:55], v[140:143], v[180:183], v[52:55]
	v_mfma_f32_16x16x32_bf16 v[48:51], v[148:151], v[180:183], v[48:51]
	v_mfma_f32_16x16x32_bf16 v[44:47], v[140:143], v[188:191], v[44:47]
	v_mfma_f32_16x16x32_bf16 v[40:43], v[148:151], v[188:191], v[40:43]
	s_waitcnt lgkmcnt(0)
	v_mfma_f32_16x16x32_bf16 v[36:39], v[140:143], v[198:201], v[36:39]
	v_mfma_f32_16x16x32_bf16 v[32:35], v[148:151], v[198:201], v[32:35]
	s_setprio 0
	s_setprio 1
	v_mfma_f32_16x16x32_bf16 v[28:31], v[152:155], v[168:171], v[28:31]
	v_mfma_f32_16x16x32_bf16 v[24:27], v[160:163], v[168:171], v[24:27]
	v_mfma_f32_16x16x32_bf16 v[20:23], v[152:155], v[176:179], v[20:23]
	v_mfma_f32_16x16x32_bf16 v[16:19], v[160:163], v[176:179], v[16:19]
	v_mfma_f32_16x16x32_bf16 v[12:15], v[152:155], v[184:187], v[12:15]
	v_mfma_f32_16x16x32_bf16 v[8:11], v[160:163], v[184:187], v[8:11]
	v_mfma_f32_16x16x32_bf16 v[4:7], v[152:155], v[194:197], v[4:7]
	v_mfma_f32_16x16x32_bf16 v[0:3], v[160:163], v[194:197], v[0:3]
	v_mfma_f32_16x16x32_bf16 v[28:31], v[156:159], v[172:175], v[28:31]
	v_mfma_f32_16x16x32_bf16 v[24:27], v[164:167], v[172:175], v[24:27]
	v_mfma_f32_16x16x32_bf16 v[20:23], v[156:159], v[180:183], v[20:23]
	v_mfma_f32_16x16x32_bf16 v[16:19], v[164:167], v[180:183], v[16:19]
	v_mfma_f32_16x16x32_bf16 v[12:15], v[156:159], v[188:191], v[12:15]
	v_mfma_f32_16x16x32_bf16 v[8:11], v[164:167], v[188:191], v[8:11]
	v_mfma_f32_16x16x32_bf16 v[4:7], v[156:159], v[198:201], v[4:7]
	v_mfma_f32_16x16x32_bf16 v[0:3], v[164:167], v[198:201], v[0:3]
	s_setprio 0
	s_barrier
	v_add_u32_e32 v133, 0x18000, v204
	v_add_u32_e32 v135, 0x1c000, v204
	ds_read_b128 v[136:139], v133
	ds_read_b128 v[140:143], v133 offset:1024
	ds_read_b128 v[144:147], v133 offset:2048
	ds_read_b128 v[148:151], v133 offset:3072
	ds_read_b128 v[152:155], v135
	ds_read_b128 v[156:159], v135 offset:1024
	ds_read_b128 v[160:163], v135 offset:2048
	ds_read_b128 v[164:167], v135 offset:3072
	ds_read_b128 v[168:171], v205 offset:32768
	ds_read_b128 v[172:175], v205 offset:33792
	ds_read_b128 v[176:179], v205 offset:34816
	ds_read_b128 v[180:183], v205 offset:35840
	ds_read_b128 v[184:187], v205 offset:36864
	ds_read_b128 v[188:191], v205 offset:37888
	ds_read_b128 v[194:197], v205 offset:38912
	ds_read_b128 v[198:201], v205 offset:39936
	s_add_u32 s20, s66, 0x40100
	s_addc_u32 s21, s67, 0
	s_mov_b32 m0, s49
	s_nop 0
	global_load_lds_dwordx4 v65, s[20:21]
	s_nop 0
	s_mov_b32 m0, s50
	s_nop 0
	global_load_lds_dwordx4 v202, s[20:21]
	s_waitcnt vmcnt(8)
	s_waitcnt lgkmcnt(0)
	s_barrier
	s_setprio 1
	s_waitcnt lgkmcnt(7)
	v_mfma_f32_16x16x32_bf16 v[128:131], v[136:139], v[168:171], v[128:131]
	v_mfma_f32_16x16x32_bf16 v[124:127], v[144:147], v[168:171], v[124:127]
	s_waitcnt lgkmcnt(5)
	v_mfma_f32_16x16x32_bf16 v[120:123], v[136:139], v[176:179], v[120:123]
	v_mfma_f32_16x16x32_bf16 v[116:119], v[144:147], v[176:179], v[116:119]
	s_waitcnt lgkmcnt(3)
	v_mfma_f32_16x16x32_bf16 v[110:113], v[136:139], v[184:187], v[110:113]
	v_mfma_f32_16x16x32_bf16 v[106:109], v[144:147], v[184:187], v[106:109]
	s_waitcnt lgkmcnt(1)
	v_mfma_f32_16x16x32_bf16 v[102:105], v[136:139], v[194:197], v[102:105]
	v_mfma_f32_16x16x32_bf16 v[98:101], v[144:147], v[194:197], v[98:101]
	v_mfma_f32_16x16x32_bf16 v[128:131], v[140:143], v[172:175], v[128:131]
	v_mfma_f32_16x16x32_bf16 v[124:127], v[148:151], v[172:175], v[124:127]
	v_mfma_f32_16x16x32_bf16 v[120:123], v[140:143], v[180:183], v[120:123]
	v_mfma_f32_16x16x32_bf16 v[116:119], v[148:151], v[180:183], v[116:119]
	v_mfma_f32_16x16x32_bf16 v[110:113], v[140:143], v[188:191], v[110:113]
	v_mfma_f32_16x16x32_bf16 v[106:109], v[148:151], v[188:191], v[106:109]
	s_waitcnt lgkmcnt(0)
	v_mfma_f32_16x16x32_bf16 v[102:105], v[140:143], v[198:201], v[102:105]
	v_mfma_f32_16x16x32_bf16 v[98:101], v[148:151], v[198:201], v[98:101]
	s_setprio 0
	s_setprio 1
	v_mfma_f32_16x16x32_bf16 v[94:97], v[152:155], v[168:171], v[94:97]
	v_mfma_f32_16x16x32_bf16 v[90:93], v[160:163], v[168:171], v[90:93]
	v_mfma_f32_16x16x32_bf16 v[86:89], v[152:155], v[176:179], v[86:89]
	v_mfma_f32_16x16x32_bf16 v[82:85], v[160:163], v[176:179], v[82:85]
	v_mfma_f32_16x16x32_bf16 v[78:81], v[152:155], v[184:187], v[78:81]
	v_mfma_f32_16x16x32_bf16 v[74:77], v[160:163], v[184:187], v[74:77]
	v_mfma_f32_16x16x32_bf16 v[70:73], v[152:155], v[194:197], v[70:73]
	v_mfma_f32_16x16x32_bf16 v[66:69], v[160:163], v[194:197], v[66:69]
	v_mfma_f32_16x16x32_bf16 v[94:97], v[156:159], v[172:175], v[94:97]
	v_mfma_f32_16x16x32_bf16 v[90:93], v[164:167], v[172:175], v[90:93]
	v_mfma_f32_16x16x32_bf16 v[86:89], v[156:159], v[180:183], v[86:89]
	v_mfma_f32_16x16x32_bf16 v[82:85], v[164:167], v[180:183], v[82:85]
	v_mfma_f32_16x16x32_bf16 v[78:81], v[156:159], v[188:191], v[78:81]
	v_mfma_f32_16x16x32_bf16 v[74:77], v[164:167], v[188:191], v[74:77]
	v_mfma_f32_16x16x32_bf16 v[70:73], v[156:159], v[198:201], v[70:73]
	v_mfma_f32_16x16x32_bf16 v[66:69], v[164:167], v[198:201], v[66:69]
	s_setprio 0
	s_barrier
	ds_read_b128 v[168:171], v205 offset:49152
	ds_read_b128 v[172:175], v205 offset:50176
	ds_read_b128 v[176:179], v205 offset:51200
	ds_read_b128 v[180:183], v205 offset:52224
	ds_read_b128 v[184:187], v205 offset:53248
	ds_read_b128 v[188:191], v205 offset:54272
	ds_read_b128 v[194:197], v205 offset:55296
	ds_read_b128 v[198:201], v205 offset:56320
	s_add_u32 s20, s17, 0x180
	s_addc_u32 s21, s33, 0
	s_mov_b32 m0, s56
	s_nop 0
	global_load_lds_dwordx4 v114, s[20:21]
	s_nop 0
	s_mov_b32 m0, s57
	s_nop 0
	global_load_lds_dwordx4 v203, s[20:21]
	s_add_u32 s20, s17, 0x40180
	s_addc_u32 s21, s33, 0
	s_mov_b32 m0, s60
	s_nop 0
	global_load_lds_dwordx4 v114, s[20:21]
	s_nop 0
	s_mov_b32 m0, s61
	s_nop 0
	global_load_lds_dwordx4 v203, s[20:21]
	s_nop 0
	s_mov_b32 m0, s58
	s_nop 0
	global_load_lds_dwordx4 v65, s[18:19]
	s_nop 0
	s_mov_b32 m0, s59
	s_nop 0
	global_load_lds_dwordx4 v202, s[18:19]
	s_waitcnt vmcnt(8)
	s_waitcnt lgkmcnt(0)
	s_barrier
	s_setprio 1
	s_waitcnt lgkmcnt(7)
	v_mfma_f32_16x16x32_bf16 v[60:63], v[136:139], v[168:171], v[60:63]
	v_mfma_f32_16x16x32_bf16 v[56:59], v[144:147], v[168:171], v[56:59]
	s_waitcnt lgkmcnt(5)
	v_mfma_f32_16x16x32_bf16 v[52:55], v[136:139], v[176:179], v[52:55]
	v_mfma_f32_16x16x32_bf16 v[48:51], v[144:147], v[176:179], v[48:51]
	s_waitcnt lgkmcnt(3)
	v_mfma_f32_16x16x32_bf16 v[44:47], v[136:139], v[184:187], v[44:47]
	v_mfma_f32_16x16x32_bf16 v[40:43], v[144:147], v[184:187], v[40:43]
	s_waitcnt lgkmcnt(1)
	v_mfma_f32_16x16x32_bf16 v[36:39], v[136:139], v[194:197], v[36:39]
	v_mfma_f32_16x16x32_bf16 v[32:35], v[144:147], v[194:197], v[32:35]
	v_mfma_f32_16x16x32_bf16 v[60:63], v[140:143], v[172:175], v[60:63]
	v_mfma_f32_16x16x32_bf16 v[56:59], v[148:151], v[172:175], v[56:59]
	v_mfma_f32_16x16x32_bf16 v[52:55], v[140:143], v[180:183], v[52:55]
	v_mfma_f32_16x16x32_bf16 v[48:51], v[148:151], v[180:183], v[48:51]
	v_mfma_f32_16x16x32_bf16 v[44:47], v[140:143], v[188:191], v[44:47]
	v_mfma_f32_16x16x32_bf16 v[40:43], v[148:151], v[188:191], v[40:43]
	s_waitcnt lgkmcnt(0)
	v_mfma_f32_16x16x32_bf16 v[36:39], v[140:143], v[198:201], v[36:39]
	v_mfma_f32_16x16x32_bf16 v[32:35], v[148:151], v[198:201], v[32:35]
	s_setprio 0
	s_setprio 1
	v_mfma_f32_16x16x32_bf16 v[28:31], v[152:155], v[168:171], v[28:31]
	v_mfma_f32_16x16x32_bf16 v[24:27], v[160:163], v[168:171], v[24:27]
	v_mfma_f32_16x16x32_bf16 v[20:23], v[152:155], v[176:179], v[20:23]
	v_mfma_f32_16x16x32_bf16 v[16:19], v[160:163], v[176:179], v[16:19]
	v_mfma_f32_16x16x32_bf16 v[12:15], v[152:155], v[184:187], v[12:15]
	v_mfma_f32_16x16x32_bf16 v[8:11], v[160:163], v[184:187], v[8:11]
	v_mfma_f32_16x16x32_bf16 v[4:7], v[152:155], v[194:197], v[4:7]
	v_mfma_f32_16x16x32_bf16 v[0:3], v[160:163], v[194:197], v[0:3]
	v_mfma_f32_16x16x32_bf16 v[28:31], v[156:159], v[172:175], v[28:31]
	v_mfma_f32_16x16x32_bf16 v[24:27], v[164:167], v[172:175], v[24:27]
	v_mfma_f32_16x16x32_bf16 v[20:23], v[156:159], v[180:183], v[20:23]
	v_mfma_f32_16x16x32_bf16 v[16:19], v[164:167], v[180:183], v[16:19]
	v_mfma_f32_16x16x32_bf16 v[12:15], v[156:159], v[188:191], v[12:15]
	v_mfma_f32_16x16x32_bf16 v[8:11], v[164:167], v[188:191], v[8:11]
	v_mfma_f32_16x16x32_bf16 v[4:7], v[156:159], v[198:201], v[4:7]
	v_mfma_f32_16x16x32_bf16 v[0:3], v[164:167], v[198:201], v[0:3]
	s_setprio 0
	s_barrier
	s_add_i32 s15, s15, 2
	s_add_u32 s2, s2, 0x100
	s_addc_u32 s3, s3, 0
	s_cmp_lt_u32 s15, 12
	s_cbranch_scc1 .LBB0_1111
	s_ashr_i32 s17, s16, 31
	s_ashr_i32 s15, s14, 31
	ds_read_b128 v[136:139], v132
	ds_read_b128 v[140:143], v132 offset:1024
	ds_read_b128 v[144:147], v132 offset:2048
	ds_read_b128 v[148:151], v132 offset:3072
	ds_read_b128 v[152:155], v134
	ds_read_b128 v[156:159], v134 offset:1024
	ds_read_b128 v[160:163], v134 offset:2048
	ds_read_b128 v[164:167], v134 offset:3072
	s_lshl_b64 s[2:3], s[16:17], 19
	s_lshl_b64 s[20:21], s[14:15], 19
	s_add_u32 s18, s29, s2
	s_addc_u32 s19, s36, s3
	s_add_u32 s20, s37, s20
	s_addc_u32 s21, s38, s21
	s_and_b64 s[2:3], s[0:1], exec
	s_cselect_b32 s34, s18, s26
	s_cselect_b32 s35, s19, s27
	s_add_u32 s2, s34, 0x80
	s_addc_u32 s3, s35, 0
	s_and_b64 s[64:65], s[0:1], exec
	s_cselect_b32 s25, s21, s25
	s_cselect_b32 s24, s20, s24
	ds_read_b128 v[168:171], v205
	ds_read_b128 v[172:175], v205 offset:1024
	ds_read_b128 v[176:179], v205 offset:2048
	ds_read_b128 v[180:183], v205 offset:3072
	ds_read_b128 v[184:187], v205 offset:4096
	ds_read_b128 v[188:191], v205 offset:5120
	ds_read_b128 v[194:197], v205 offset:6144
	ds_read_b128 v[198:201], v205 offset:7168
	s_add_u32 s26, s26, 0x40780
	s_addc_u32 s27, s27, 0
	s_mov_b32 m0, s62
	s_nop 0
	global_load_lds_dwordx4 v65, s[26:27]
	s_nop 0
	s_mov_b32 m0, s63
	s_nop 0
	global_load_lds_dwordx4 v202, s[26:27]
	s_waitcnt vmcnt(8)
	s_waitcnt lgkmcnt(0)
	s_barrier
	s_setprio 1
	s_waitcnt lgkmcnt(7)
	v_mfma_f32_16x16x32_bf16 v[128:131], v[136:139], v[168:171], v[128:131]
	v_mfma_f32_16x16x32_bf16 v[124:127], v[144:147], v[168:171], v[124:127]
	s_waitcnt lgkmcnt(5)
	v_mfma_f32_16x16x32_bf16 v[120:123], v[136:139], v[176:179], v[120:123]
	v_mfma_f32_16x16x32_bf16 v[116:119], v[144:147], v[176:179], v[116:119]
	s_waitcnt lgkmcnt(3)
	v_mfma_f32_16x16x32_bf16 v[110:113], v[136:139], v[184:187], v[110:113]
	v_mfma_f32_16x16x32_bf16 v[106:109], v[144:147], v[184:187], v[106:109]
	v_mfma_f32_16x16x32_bf16 v[128:131], v[140:143], v[172:175], v[128:131]
	v_mfma_f32_16x16x32_bf16 v[124:127], v[148:151], v[172:175], v[124:127]
	v_mfma_f32_16x16x32_bf16 v[120:123], v[140:143], v[180:183], v[120:123]
	v_mfma_f32_16x16x32_bf16 v[116:119], v[148:151], v[180:183], v[116:119]
	s_waitcnt lgkmcnt(2)
	v_mfma_f32_16x16x32_bf16 v[110:113], v[140:143], v[188:191], v[110:113]
	v_mfma_f32_16x16x32_bf16 v[106:109], v[148:151], v[188:191], v[106:109]
	s_waitcnt lgkmcnt(1)
	v_mfma_f32_16x16x32_bf16 v[102:105], v[136:139], v[194:197], v[102:105]
	v_mfma_f32_16x16x32_bf16 v[98:101], v[144:147], v[194:197], v[98:101]
	s_waitcnt lgkmcnt(0)
	v_mfma_f32_16x16x32_bf16 v[206:209], v[140:143], v[198:201], v[102:105]
	v_mfma_f32_16x16x32_bf16 v[210:213], v[148:151], v[198:201], v[98:101]
	s_setprio 0
	s_setprio 1
	v_mfma_f32_16x16x32_bf16 v[94:97], v[152:155], v[168:171], v[94:97]
	v_mfma_f32_16x16x32_bf16 v[90:93], v[160:163], v[168:171], v[90:93]
	v_mfma_f32_16x16x32_bf16 v[78:81], v[152:155], v[184:187], v[78:81]
	v_mfma_f32_16x16x32_bf16 v[74:77], v[160:163], v[184:187], v[74:77]
	v_mfma_f32_16x16x32_bf16 v[70:73], v[152:155], v[194:197], v[70:73]
	v_mfma_f32_16x16x32_bf16 v[66:69], v[160:163], v[194:197], v[66:69]
	v_mfma_f32_16x16x32_bf16 v[94:97], v[156:159], v[172:175], v[94:97]
	v_mfma_f32_16x16x32_bf16 v[90:93], v[164:167], v[172:175], v[90:93]
	v_mfma_f32_16x16x32_bf16 v[86:89], v[152:155], v[176:179], v[86:89]
	v_mfma_f32_16x16x32_bf16 v[82:85], v[160:163], v[176:179], v[82:85]
	v_mfma_f32_16x16x32_bf16 v[78:81], v[156:159], v[188:191], v[78:81]
	v_mfma_f32_16x16x32_bf16 v[74:77], v[164:167], v[188:191], v[74:77]
	v_mfma_f32_16x16x32_bf16 v[70:73], v[156:159], v[198:201], v[70:73]
	v_mfma_f32_16x16x32_bf16 v[66:69], v[164:167], v[198:201], v[66:69]
	v_mfma_f32_16x16x32_bf16 v[168:171], v[156:159], v[180:183], v[86:89]
	v_mfma_f32_16x16x32_bf16 v[172:175], v[164:167], v[180:183], v[82:85]
	s_setprio 0
	s_barrier
	s_nop 0
	ds_read_b128 v[82:85], v205 offset:16384
	ds_read_b128 v[86:89], v205 offset:17408
	ds_read_b128 v[98:101], v205 offset:18432
	ds_read_b128 v[102:105], v205 offset:19456
	ds_read_b128 v[176:179], v205 offset:20480
	ds_read_b128 v[180:183], v205 offset:21504
	ds_read_b128 v[184:187], v205 offset:22528
	ds_read_b128 v[188:191], v205 offset:23552
	s_mov_b32 m0, s44
	s_nop 0
	global_load_lds_dwordx4 v114, s[24:25]
	s_add_u32 s26, s24, 0x40000
	s_mov_b32 m0, s45
	s_nop 0
	global_load_lds_dwordx4 v203, s[24:25]
	s_addc_u32 s27, s25, 0
	s_mov_b32 m0, s46
	s_nop 0
	global_load_lds_dwordx4 v114, s[26:27]
	s_nop 0
	s_mov_b32 m0, s47
	s_nop 0
	global_load_lds_dwordx4 v203, s[26:27]
	s_nop 0
	s_mov_b32 m0, s43
	s_nop 0
	global_load_lds_dwordx4 v65, s[34:35]
	s_nop 0
	s_mov_b32 m0, s48
	s_nop 0
	global_load_lds_dwordx4 v202, s[34:35]
	s_waitcnt vmcnt(8)
	s_waitcnt lgkmcnt(0)
	s_barrier
	s_setprio 1
	s_waitcnt lgkmcnt(7)
	v_mfma_f32_16x16x32_bf16 v[60:63], v[136:139], v[82:85], v[60:63]
	v_mfma_f32_16x16x32_bf16 v[56:59], v[144:147], v[82:85], v[56:59]
	s_waitcnt lgkmcnt(5)
	v_mfma_f32_16x16x32_bf16 v[52:55], v[136:139], v[98:101], v[52:55]
	v_mfma_f32_16x16x32_bf16 v[48:51], v[144:147], v[98:101], v[48:51]
	v_mfma_f32_16x16x32_bf16 v[60:63], v[140:143], v[86:89], v[60:63]
	v_mfma_f32_16x16x32_bf16 v[56:59], v[148:151], v[86:89], v[56:59]
	s_waitcnt lgkmcnt(4)
	v_mfma_f32_16x16x32_bf16 v[52:55], v[140:143], v[102:105], v[52:55]
	v_mfma_f32_16x16x32_bf16 v[48:51], v[148:151], v[102:105], v[48:51]
	s_waitcnt lgkmcnt(3)
	v_mfma_f32_16x16x32_bf16 v[44:47], v[136:139], v[176:179], v[44:47]
	v_mfma_f32_16x16x32_bf16 v[40:43], v[144:147], v[176:179], v[40:43]
	s_waitcnt lgkmcnt(1)
	v_mfma_f32_16x16x32_bf16 v[36:39], v[136:139], v[184:187], v[36:39]
	v_mfma_f32_16x16x32_bf16 v[32:35], v[144:147], v[184:187], v[32:35]
	v_mfma_f32_16x16x32_bf16 v[44:47], v[140:143], v[180:183], v[44:47]
	v_mfma_f32_16x16x32_bf16 v[40:43], v[148:151], v[180:183], v[40:43]
	s_waitcnt lgkmcnt(0)
	v_mfma_f32_16x16x32_bf16 v[36:39], v[140:143], v[188:191], v[36:39]
	v_mfma_f32_16x16x32_bf16 v[148:151], v[148:151], v[188:191], v[32:35]
	s_setprio 0
	s_setprio 1
	v_mfma_f32_16x16x32_bf16 v[20:23], v[152:155], v[98:101], v[20:23]
	v_mfma_f32_16x16x32_bf16 v[16:19], v[160:163], v[98:101], v[16:19]
	v_mfma_f32_16x16x32_bf16 v[4:7], v[152:155], v[184:187], v[4:7]
	v_mfma_f32_16x16x32_bf16 v[0:3], v[160:163], v[184:187], v[0:3]
	v_mfma_f32_16x16x32_bf16 v[28:31], v[152:155], v[82:85], v[28:31]
	v_mfma_f32_16x16x32_bf16 v[24:27], v[160:163], v[82:85], v[24:27]
	v_mfma_f32_16x16x32_bf16 v[20:23], v[156:159], v[102:105], v[20:23]
	v_mfma_f32_16x16x32_bf16 v[16:19], v[164:167], v[102:105], v[16:19]
	v_mfma_f32_16x16x32_bf16 v[12:15], v[152:155], v[176:179], v[12:15]
	v_mfma_f32_16x16x32_bf16 v[8:11], v[160:163], v[176:179], v[8:11]
	v_mfma_f32_16x16x32_bf16 v[4:7], v[156:159], v[188:191], v[4:7]
	v_mfma_f32_16x16x32_bf16 v[0:3], v[164:167], v[188:191], v[0:3]
	v_mfma_f32_16x16x32_bf16 v[28:31], v[156:159], v[86:89], v[28:31]
	v_mfma_f32_16x16x32_bf16 v[194:197], v[164:167], v[86:89], v[24:27]
	v_mfma_f32_16x16x32_bf16 v[198:201], v[156:159], v[180:183], v[12:15]
	v_mfma_f32_16x16x32_bf16 v[176:179], v[164:167], v[180:183], v[8:11]
	s_setprio 0
	s_barrier
	s_nop 0
	ds_read_b128 v[8:11], v133
	ds_read_b128 v[12:15], v133 offset:1024
	ds_read_b128 v[152:155], v133 offset:2048
	ds_read_b128 v[156:159], v133 offset:3072
	ds_read_b128 v[160:163], v135
	ds_read_b128 v[164:167], v135 offset:1024
	ds_read_b128 v[180:183], v135 offset:2048
	ds_read_b128 v[184:187], v135 offset:3072
	ds_read_b128 v[24:27], v205 offset:32768
	ds_read_b128 v[32:35], v205 offset:33792
	ds_read_b128 v[188:191], v205 offset:34816
	ds_read_b128 v[214:217], v205 offset:35840
	ds_read_b128 v[218:221], v205 offset:36864
	ds_read_b128 v[222:225], v205 offset:37888
	ds_read_b128 v[226:229], v205 offset:38912
	ds_read_b128 v[230:233], v205 offset:39936
	s_add_u32 s26, s34, 0x40000
	s_addc_u32 s27, s35, 0
	s_mov_b32 m0, s49
	s_nop 0
	global_load_lds_dwordx4 v65, s[26:27]
	s_nop 0
	s_mov_b32 m0, s50
	s_nop 0
	global_load_lds_dwordx4 v202, s[26:27]
	s_waitcnt vmcnt(8)
	s_waitcnt lgkmcnt(0)
	s_barrier
	s_setprio 1
	s_waitcnt lgkmcnt(7)
	v_mfma_f32_16x16x32_bf16 v[82:85], v[8:11], v[24:27], v[128:131]
	s_waitcnt lgkmcnt(6)
	v_mfma_f32_16x16x32_bf16 v[140:143], v[12:15], v[32:35], v[82:85]
	v_mfma_f32_16x16x32_bf16 v[82:85], v[152:155], v[24:27], v[124:127]
	v_mfma_f32_16x16x32_bf16 v[144:147], v[156:159], v[32:35], v[82:85]
	s_waitcnt lgkmcnt(5)
	v_mfma_f32_16x16x32_bf16 v[82:85], v[8:11], v[188:191], v[120:123]
	s_waitcnt lgkmcnt(4)
	v_mfma_f32_16x16x32_bf16 v[124:127], v[12:15], v[214:217], v[82:85]
	v_mfma_f32_16x16x32_bf16 v[82:85], v[152:155], v[188:191], v[116:119]
	v_mfma_f32_16x16x32_bf16 v[128:131], v[156:159], v[214:217], v[82:85]
	s_waitcnt lgkmcnt(3)
	v_mfma_f32_16x16x32_bf16 v[82:85], v[8:11], v[218:221], v[110:113]
	s_waitcnt lgkmcnt(2)
	v_mfma_f32_16x16x32_bf16 v[98:101], v[12:15], v[222:225], v[82:85]
	v_mfma_f32_16x16x32_bf16 v[82:85], v[152:155], v[218:221], v[106:109]
	v_mfma_f32_16x16x32_bf16 v[102:105], v[156:159], v[222:225], v[82:85]
	s_waitcnt lgkmcnt(1)
	v_mfma_f32_16x16x32_bf16 v[82:85], v[8:11], v[226:229], v[206:209]
	v_mfma_f32_16x16x32_bf16 v[86:89], v[152:155], v[226:229], v[210:213]
	s_waitcnt lgkmcnt(0)
	v_mfma_f32_16x16x32_bf16 v[82:85], v[12:15], v[230:233], v[82:85]
	v_mfma_f32_16x16x32_bf16 v[86:89], v[156:159], v[230:233], v[86:89]
	s_setprio 0
	s_setprio 1
	v_mfma_f32_16x16x32_bf16 v[94:97], v[160:163], v[24:27], v[94:97]
	v_mfma_f32_16x16x32_bf16 v[24:27], v[180:183], v[24:27], v[90:93]
	v_mfma_f32_16x16x32_bf16 v[132:135], v[184:187], v[32:35], v[24:27]
	v_mfma_f32_16x16x32_bf16 v[24:27], v[160:163], v[188:191], v[168:171]
	v_mfma_f32_16x16x32_bf16 v[120:123], v[164:167], v[214:217], v[24:27]
	v_mfma_f32_16x16x32_bf16 v[24:27], v[180:183], v[188:191], v[172:175]
	v_mfma_f32_16x16x32_bf16 v[116:119], v[184:187], v[214:217], v[24:27]
	v_mfma_f32_16x16x32_bf16 v[24:27], v[160:163], v[218:221], v[78:81]
	v_mfma_f32_16x16x32_bf16 v[106:109], v[164:167], v[222:225], v[24:27]
	v_mfma_f32_16x16x32_bf16 v[24:27], v[180:183], v[218:221], v[74:77]
	v_mfma_f32_16x16x32_bf16 v[110:113], v[184:187], v[222:225], v[24:27]
	v_mfma_f32_16x16x32_bf16 v[24:27], v[160:163], v[226:229], v[70:73]
	v_mfma_f32_16x16x32_bf16 v[90:93], v[164:167], v[230:233], v[24:27]
	v_mfma_f32_16x16x32_bf16 v[24:27], v[180:183], v[226:229], v[66:69]
	v_mfma_f32_16x16x32_bf16 v[136:139], v[164:167], v[32:35], v[94:97]
	v_mfma_f32_16x16x32_bf16 v[94:97], v[184:187], v[230:233], v[24:27]
	s_setprio 0
	s_barrier
	ds_read_b128 v[66:69], v205 offset:49152
	ds_read_b128 v[168:171], v205 offset:50176
	ds_read_b128 v[172:175], v205 offset:51200
	ds_read_b128 v[188:191], v205 offset:52224
	ds_read_b128 v[206:209], v205 offset:53248
	ds_read_b128 v[210:213], v205 offset:54272
	ds_read_b128 v[214:217], v205 offset:55296
	ds_read_b128 v[218:221], v205 offset:56320
	s_add_u32 s26, s24, 0x80
	s_addc_u32 s27, s25, 0
	s_mov_b32 m0, s56
	s_nop 0
	global_load_lds_dwordx4 v114, s[26:27]
	s_add_u32 s24, s24, 0x40080
	s_mov_b32 m0, s57
	s_nop 0
	global_load_lds_dwordx4 v203, s[26:27]
	s_addc_u32 s25, s25, 0
	s_mov_b32 m0, s60
	s_nop 0
	global_load_lds_dwordx4 v114, s[24:25]
	s_nop 0
	s_mov_b32 m0, s61
	s_nop 0
	global_load_lds_dwordx4 v203, s[24:25]
	s_nop 0
	s_mov_b32 m0, s58
	s_nop 0
	global_load_lds_dwordx4 v65, s[2:3]
	s_nop 0
	s_mov_b32 m0, s59
	s_nop 0
	global_load_lds_dwordx4 v202, s[2:3]
	s_waitcnt vmcnt(8)
	s_waitcnt lgkmcnt(0)
	s_barrier
	s_setprio 1
	s_waitcnt lgkmcnt(7)
	v_mfma_f32_16x16x32_bf16 v[24:27], v[8:11], v[66:69], v[60:63]
	s_waitcnt lgkmcnt(6)
	v_mfma_f32_16x16x32_bf16 v[78:81], v[12:15], v[168:171], v[24:27]
	v_mfma_f32_16x16x32_bf16 v[24:27], v[152:155], v[66:69], v[56:59]
	v_mfma_f32_16x16x32_bf16 v[74:77], v[156:159], v[168:171], v[24:27]
	s_waitcnt lgkmcnt(5)
	v_mfma_f32_16x16x32_bf16 v[24:27], v[8:11], v[172:175], v[52:55]
	s_waitcnt lgkmcnt(4)
	v_mfma_f32_16x16x32_bf16 v[60:63], v[12:15], v[188:191], v[24:27]
	v_mfma_f32_16x16x32_bf16 v[24:27], v[152:155], v[172:175], v[48:51]
	v_mfma_f32_16x16x32_bf16 v[56:59], v[156:159], v[188:191], v[24:27]
	s_waitcnt lgkmcnt(3)
	v_mfma_f32_16x16x32_bf16 v[24:27], v[8:11], v[206:209], v[44:47]
	s_waitcnt lgkmcnt(1)
	v_mfma_f32_16x16x32_bf16 v[8:11], v[8:11], v[214:217], v[36:39]
	v_mfma_f32_16x16x32_bf16 v[32:35], v[12:15], v[210:213], v[24:27]
	v_mfma_f32_16x16x32_bf16 v[24:27], v[152:155], v[206:209], v[40:43]
	s_waitcnt lgkmcnt(0)
	v_mfma_f32_16x16x32_bf16 v[12:15], v[12:15], v[218:221], v[8:11]
	v_mfma_f32_16x16x32_bf16 v[8:11], v[152:155], v[214:217], v[148:151]
	v_mfma_f32_16x16x32_bf16 v[24:27], v[156:159], v[210:213], v[24:27]
	v_mfma_f32_16x16x32_bf16 v[8:11], v[156:159], v[218:221], v[8:11]
	s_setprio 0
	s_setprio 1
	v_mfma_f32_16x16x32_bf16 v[16:19], v[180:183], v[172:175], v[16:19]
	v_mfma_f32_16x16x32_bf16 v[28:31], v[160:163], v[66:69], v[28:31]
	v_mfma_f32_16x16x32_bf16 v[20:23], v[160:163], v[172:175], v[20:23]
	v_mfma_f32_16x16x32_bf16 v[48:51], v[184:187], v[188:191], v[16:19]
	v_mfma_f32_16x16x32_bf16 v[16:19], v[160:163], v[206:209], v[198:201]
	v_mfma_f32_16x16x32_bf16 v[70:73], v[164:167], v[168:171], v[28:31]
	v_mfma_f32_16x16x32_bf16 v[28:31], v[180:183], v[66:69], v[194:197]
	v_mfma_f32_16x16x32_bf16 v[52:55], v[164:167], v[188:191], v[20:23]
	v_mfma_f32_16x16x32_bf16 v[20:23], v[164:167], v[210:213], v[16:19]
	v_mfma_f32_16x16x32_bf16 v[16:19], v[180:183], v[206:209], v[176:179]
	v_mfma_f32_16x16x32_bf16 v[4:7], v[160:163], v[214:217], v[4:7]
	v_mfma_f32_16x16x32_bf16 v[0:3], v[180:183], v[214:217], v[0:3]
	v_mfma_f32_16x16x32_bf16 v[66:69], v[184:187], v[168:171], v[28:31]
	v_mfma_f32_16x16x32_bf16 v[16:19], v[184:187], v[210:213], v[16:19]
	v_mfma_f32_16x16x32_bf16 v[4:7], v[164:167], v[218:221], v[4:7]
	v_mfma_f32_16x16x32_bf16 v[0:3], v[184:187], v[218:221], v[0:3]
	s_setprio 0
	s_barrier
	s_andn2_b64 vcc, exec, s[10:11]
	s_cbranch_vccnz .LBB0_1114
	s_barrier

.LBB0_1411:
	s_andn2_b64 vcc, exec, s[0:1]
	s_mov_b32 s46, 0xffff0000
	s_movk_i32 s48, 0x7fff
	s_cbranch_vccnz .LBB0_1494
	v_readlane_b32 s1, v254, 59
	s_cmp_eq_u32 s1, 3
	s_movk_i32 s0, 0x110
	s_cselect_b32 s29, 0x100, s0
	s_lshl_b32 s30, s29, 3
	v_readlane_b32 s4, v255, 0
	s_cmp_ge_i32 s4, s30
	v_mbcnt_lo_u32_b32 v0, -1, 0
	v_mbcnt_hi_u32_b32 v0, -1, v0
	s_cbranch_scc1 .LBB0_1432
	v_readlane_b32 s2, v254, 62
	v_readlane_b32 s3, v254, 63
	s_add_u32 s6, s2, 0x2000000
	s_addc_u32 s7, s3, 0
	s_lshl_b32 s0, s1, 26
	s_add_u32 s0, s2, s0
	s_addc_u32 s1, s3, 0
	s_add_u32 s36, s0, 0x21a00000
	s_addc_u32 s37, s1, 0
	s_add_u32 s8, s2, 0x1200000
	s_addc_u32 s9, s3, 0
	s_lshl_b32 s0, s56, 10
	s_add_i32 s40, s0, 0
	s_lshl_b32 s38, s56, 6
	s_ashr_i32 s1, s56, 2
	s_or_b32 s39, s29, 1
	s_add_i32 s41, s40, 0x10000
	s_add_i32 s42, s40, 0x12000
	s_add_i32 s43, s40, 0x14000
	s_add_i32 s44, s40, 0x16000
	s_add_i32 s45, s40, 0x2000
	s_add_i32 s46, s40, 0x4000
	s_add_i32 s47, s40, 0x6000
	s_cmp_eq_u32 s1, 1
	s_cselect_b64 s[10:11], -1, 0
	s_ashr_i32 s48, s4, 31
	s_lshr_b32 s0, s48, 29
	s_add_i32 s0, s4, s0
	s_ashr_i32 s2, s0, 3
	s_and_b32 s0, s0, -8
	s_sub_i32 s0, s4, s0
	s_cmp_lt_i32 s0, 0
	s_cselect_b32 s3, s39, s29
	s_mul_i32 s0, s0, s3
	s_add_i32 s0, s0, s2
	s_ashr_i32 s2, s0, 31
	s_lshr_b32 s2, s2, 26
	s_add_i32 s2, s0, s2
	s_ashr_i32 s3, s2, 6
	s_lshl_b32 s4, s3, 3
	s_sub_i32 s3, s29, s4
	s_min_i32 s5, s3, 8
	s_sext_i32_i8 s3, s5
	v_cvt_f32_i32_e32 v1, s3
	s_andn2_b32 s2, s2, 63
	s_sub_i32 s12, s0, s2
	v_cvt_f32_i32_e32 v2, s12
	v_rcp_iflag_f32_e32 v3, v1
	s_xor_b32 s0, s12, s3
	s_ashr_i32 s0, s0, 30
	s_or_b32 s0, s0, 1
	v_mul_f32_e32 v3, v2, v3
	v_trunc_f32_e32 v3, v3
	v_fma_f32 v2, -v3, v1, v2
	v_cvt_i32_f32_e32 v3, v3
	v_cmp_ge_f32_e64 s[2:3], |v2|, |v1|
	s_and_b64 s[2:3], s[2:3], exec
	v_or_b32_e32 v1, s38, v0
	v_readfirstlane_b32 s2, v3
	v_ashrrev_i32_e32 v3, 31, v1
	v_lshrrev_b32_e32 v3, 26, v3
	v_lshlrev_b32_e32 v2, 4, v1
	v_add_u32_e32 v3, v1, v3
	v_bfe_i32 v1, v1, 27, 1
	v_lshrrev_b32_e32 v1, 22, v1
	v_add_u32_e32 v1, v2, v1
	v_and_b32_e32 v1, 0xfffffc00, v1
	v_sub_u32_e32 v1, v2, v1
	v_lshrrev_b32_e32 v4, 4, v1
	v_bitop3_b32 v1, v4, v1, 32 bitop3:0x6c
	v_ashrrev_i32_e32 v5, 31, v1
	v_ashrrev_i32_e32 v3, 6, v3
	v_lshrrev_b32_e32 v5, 26, v5
	v_lshlrev_b32_e32 v4, 3, v3
	v_add_u32_e32 v5, v1, v5
	v_and_b32_e32 v4, -16, v4
	s_waitcnt vmcnt(0)
	v_ashrrev_i32_e32 v6, 6, v5
	v_add_u32_e32 v7, v6, v4
	v_and_b32_e32 v4, 0xc0, v5
	v_lshlrev_b32_e32 v3, 5, v3
	v_sub_u32_e32 v1, v1, v4
	v_and_b32_e32 v3, 32, v3
	v_ashrrev_i16_sdwa v1, v193, sext(v1) dst_sel:DWORD dst_unused:UNUSED_PAD src0_sel:DWORD src1_sel:BYTE_0
	v_add_u32_e32 v2, 0x2000, v2
	v_add_u32_sdwa v1, v3, sext(v1) dst_sel:DWORD dst_unused:UNUSED_PAD src0_sel:DWORD src1_sel:WORD_0
	v_ashrrev_i32_e32 v3, 31, v2
	v_lshrrev_b32_e32 v3, 22, v3
	v_add_u32_e32 v3, v2, v3
	v_ashrrev_i32_e32 v3, 10, v3
	v_mul_i32_i24_e32 v4, 0x400, v3
	v_sub_u32_e32 v2, v2, v4
	v_lshrrev_b32_e32 v4, 4, v2
	v_bitop3_b32 v2, v4, v2, 32 bitop3:0x6c
	v_ashrrev_i32_e32 v5, 31, v2
	v_lshrrev_b32_e32 v5, 26, v5
	v_lshlrev_b32_e32 v4, 3, v3
	v_add_u32_e32 v5, v2, v5
	s_cselect_b32 s0, s0, 0
	v_and_b32_e32 v4, -16, v4
	v_ashrrev_i32_e32 v8, 6, v5
	s_add_i32 s0, s2, s0
	v_add_u32_e32 v9, v8, v4
	v_and_b32_e32 v4, 0xc0, v5
	s_mul_i32 s2, s0, s5
	v_lshlrev_b32_e32 v3, 5, v3
	v_sub_u32_e32 v2, v2, v4
	s_sub_i32 s2, s12, s2
	v_and_b32_e32 v3, 32, v3
	v_ashrrev_i16_sdwa v2, v193, sext(v2) dst_sel:DWORD dst_unused:UNUSED_PAD src0_sel:DWORD src1_sel:BYTE_0
	s_sext_i32_i8 s2, s2
	v_add_u32_sdwa v10, v3, sext(v2) dst_sel:DWORD dst_unused:UNUSED_PAD src0_sel:DWORD src1_sel:WORD_0
	v_lshrrev_b32_e32 v2, 10, v1
	s_add_i32 s61, s4, s2
	v_add_u32_e32 v2, v2, v7
	s_lshl_b32 s2, s61, 8
	v_and_b32_e32 v4, 0x1fffff, v2
	v_add_u32_e32 v2, s2, v4
	v_ashrrev_i32_e32 v3, 31, v2
	v_lshl_add_u64 v[2:3], v[2:3], 2, s[8:9]
	flat_load_dword v11, v[2:3]
	v_lshrrev_b32_e32 v2, 10, v10
	v_add_u32_e32 v2, v2, v9
	s_or_b32 s3, s2, 0x80
	v_and_b32_e32 v12, 0x1fffff, v2
	v_add_u32_e32 v2, s2, v12
	v_add_u32_e32 v4, s3, v4
	v_ashrrev_i32_e32 v3, 31, v2
	v_ashrrev_i32_e32 v5, 31, v4
	v_lshl_add_u64 v[2:3], v[2:3], 2, s[8:9]
	v_lshl_add_u64 v[4:5], v[4:5], 2, s[8:9]
	flat_load_dword v13, v[2:3]
	s_nop 0
	flat_load_dword v4, v[4:5]
	v_add_u32_e32 v2, s3, v12
	v_ashrrev_i32_e32 v3, 31, v2
	v_lshl_add_u64 v[2:3], v[2:3], 2, s[8:9]
	flat_load_dword v2, v[2:3]
	s_ashr_i32 s2, s61, 4
	s_add_i32 s3, s61, 0xffffff00
	s_cmpk_lt_i32 s61, 0x100
	s_cselect_b32 s2, s2, s3
	s_ashr_i32 s3, s2, 31
	s_lshl_b64 s[2:3], s[2:3], 22
	s_add_u32 s4, s36, s2
	s_addc_u32 s5, s37, s3
	s_bfe_i64 s[2:3], s[0:1], 0x80000
	s_lshl_b64 s[2:3], s[2:3], 19
	s_add_u32 s24, s4, s2
	v_lshlrev_b32_e32 v3, 1, v7
	v_lshrrev_b32_e32 v5, 2, v7
	v_and_b32_e32 v6, 3, v6
	s_mov_b32 s4, 0x1fffe0
	v_and_b32_e32 v3, 24, v3
	v_and_b32_e32 v5, 4, v5
	v_and_or_b32 v6, v7, s4, v6
	v_or3_b32 v3, v6, v5, v3
	v_lshlrev_b32_e32 v1, 1, v1
	v_lshl_add_u32 v65, v3, 11, v1
	v_lshlrev_b32_e32 v3, 1, v9
	v_lshrrev_b32_e32 v5, 2, v9
	v_and_b32_e32 v6, 3, v8
	v_and_b32_e32 v3, 24, v3
	v_and_b32_e32 v5, 4, v5
	v_and_or_b32 v6, v9, s4, v6
	s_addc_u32 s25, s5, s3
	v_or3_b32 v3, v6, v5, v3
	v_lshlrev_b32_e32 v5, 1, v10
	s_mov_b32 m0, s41
	s_nop 0
	global_load_lds_dwordx4 v65, s[24:25]
	s_add_u32 s2, s24, 0x40000
	v_lshl_add_u32 v114, v3, 11, v5
	s_mov_b32 m0, s42
	s_nop 0
	global_load_lds_dwordx4 v114, s[24:25]
	s_addc_u32 s3, s25, 0
	s_mov_b32 m0, s43
	s_nop 0
	global_load_lds_dwordx4 v65, s[2:3]
	v_and_b32_e32 v1, 0x7fe, v1
	s_mov_b32 m0, s44
	s_nop 0
	global_load_lds_dwordx4 v114, s[2:3]
	v_and_b32_e32 v5, 0x7fe, v5
	s_cmp_lg_u32 s1, 1
	s_waitcnt vmcnt(0) lgkmcnt(0)
	v_med3_i32 v3, v11, 0, v243
	v_lshl_or_b32 v139, v3, 11, v1
	s_mov_b32 m0, s40
	s_nop 0
	global_load_lds_dwordx4 v139, s[6:7]
	v_med3_i32 v3, v13, 0, v243
	v_lshl_or_b32 v138, v3, 11, v5
	v_med3_i32 v3, v4, 0, v243
	s_mov_b32 m0, s45
	s_nop 0
	global_load_lds_dwordx4 v138, s[6:7]
	v_lshl_or_b32 v133, v3, 11, v1
	v_med3_i32 v1, v2, 0, v243
	s_mov_b32 m0, s46
	s_nop 0
	global_load_lds_dwordx4 v133, s[6:7]
	v_lshl_or_b32 v132, v1, 11, v5
	s_mov_b32 m0, s47
	s_nop 0
	global_load_lds_dwordx4 v132, s[6:7]
	s_cbranch_scc1 .LBB0_1415
	s_barrier
.LBB0_1415:
	v_readlane_b32 s4, v254, 62
	v_readlane_b32 s5, v254, 63
	s_add_u32 s12, s4, 0x6400000
	s_sext_i32_i8 s62, s0
	s_addc_u32 s13, s5, 0
	s_lshl_b32 s49, s1, 6
	s_lshl_b32 s0, s1, 13
	s_lshl_b32 s1, s56, 5
	s_and_b32 s50, s1, 0x60
	s_lshl_b32 s1, s50, 7
	s_add_i32 s51, s40, 0x18000
	s_add_i32 s52, s40, 0x1a000
	s_add_u32 s14, s4, 0x2000080
	s_addc_u32 s15, s5, 0
	s_add_i32 s53, s40, 0x8000
	s_add_i32 s54, s40, 0xa000
	s_add_i32 s55, s40, 0x1c000
	s_mov_b32 s2, s56
	s_add_i32 s56, s40, 0x1e000
	s_add_i32 s57, s40, 0xc000
	s_cmp_lt_u32 s2, 4
	s_cselect_b64 s[16:17], -1, 0
	s_add_i32 s58, s40, 0xe000
	s_add_u32 s18, s4, 0x2000780
	v_and_b32_e32 v1, 48, v0
	v_lshlrev_b32_e32 v2, 6, v0
	s_movk_i32 s2, 0x3c0
	v_lshlrev_b32_e32 v0, 2, v0
	s_addc_u32 s19, s5, 0
	v_and_or_b32 v1, v2, s2, v1
	v_and_b32_e32 v0, 32, v0
	v_bitop3_b32 v2, v1, s0, v0 bitop3:0xde
	s_add_u32 s0, s24, 0x80
	v_bitop3_b32 v0, v1, s1, v0 bitop3:0xde
	s_waitcnt vmcnt(2)
	s_barrier
	s_addc_u32 s1, s25, 0
	s_mov_b32 m0, s51
	s_nop 0
	global_load_lds_dwordx4 v65, s[0:1]
	v_mov_b32_e32 v136, 0
	s_mov_b32 m0, s52
	s_nop 0
	global_load_lds_dwordx4 v114, s[0:1]
	s_mov_b32 m0, s53
	s_nop 0
	global_load_lds_dwordx4 v139, s[14:15]
	s_mov_b32 s59, 0
	s_mov_b32 m0, s54
	s_nop 0
	global_load_lds_dwordx4 v138, s[14:15]
	s_add_u32 s0, s24, 0x40080
	s_addc_u32 s1, s25, 0
	s_mov_b32 m0, s55
	s_nop 0
	global_load_lds_dwordx4 v65, s[0:1]
	v_add_u32_e32 v134, 0, v0
	s_mov_b32 m0, s56
	s_nop 0
	global_load_lds_dwordx4 v114, s[0:1]
	s_waitcnt vmcnt(6)
	v_add_u32_e32 v135, 0, v2
	v_mov_b32_e32 v137, 0
	s_barrier
	s_branch .LBB0_1418

.LBB0_1425:
	s_add_u32 s66, s72, s2
	s_addc_u32 s67, s73, s3
	s_add_u32 s34, s66, 0x2000100
	s_addc_u32 s35, s67, 0
	v_add_u32_e32 v141, 0x10000, v134
	v_add_u32_e32 v142, 0x14000, v134
	s_add_u32 s26, s66, 0x2000180
	ds_read_b128 v[144:147], v141
	ds_read_b128 v[148:151], v141 offset:1024
	ds_read_b128 v[152:155], v141 offset:2048
	ds_read_b128 v[156:159], v141 offset:3072
	ds_read_b128 v[160:163], v142
	ds_read_b128 v[164:167], v142 offset:1024
	ds_read_b128 v[168:171], v142 offset:2048
	ds_read_b128 v[172:175], v142 offset:3072
	s_addc_u32 s27, s67, 0
	s_add_u32 s33, s24, s2
	s_addc_u32 s63, s25, s3
	s_add_u32 s64, s33, 0x100
	s_addc_u32 s65, s63, 0
	s_add_u32 s66, s66, 0x2000080
	s_addc_u32 s67, s67, 0
	ds_read_b128 v[176:179], v135
	ds_read_b128 v[180:183], v135 offset:1024
	ds_read_b128 v[184:187], v135 offset:2048
	ds_read_b128 v[188:191], v135 offset:3072
	ds_read_b128 v[194:197], v135 offset:4096
	ds_read_b128 v[198:201], v135 offset:5120
	ds_read_b128 v[202:205], v135 offset:6144
	ds_read_b128 v[206:209], v135 offset:7168
	s_mov_b32 m0, s57
	s_nop 0
	global_load_lds_dwordx4 v133, s[66:67]
	s_nop 0
	s_mov_b32 m0, s58
	s_nop 0
	global_load_lds_dwordx4 v132, s[66:67]
	s_waitcnt vmcnt(8)
	s_waitcnt lgkmcnt(0)
	s_barrier
	s_setprio 1
	s_waitcnt lgkmcnt(0)
	v_mfma_f32_16x16x32_bf16 v[128:131], v[144:147], v[176:179], v[128:131]
	v_mfma_f32_16x16x32_bf16 v[124:127], v[152:155], v[176:179], v[124:127]
	s_waitcnt lgkmcnt(5)
	v_mfma_f32_16x16x32_bf16 v[120:123], v[144:147], v[184:187], v[120:123]
	v_mfma_f32_16x16x32_bf16 v[116:119], v[152:155], v[184:187], v[116:119]
	s_waitcnt lgkmcnt(3)
	v_mfma_f32_16x16x32_bf16 v[110:113], v[144:147], v[194:197], v[110:113]
	v_mfma_f32_16x16x32_bf16 v[106:109], v[152:155], v[194:197], v[106:109]
	s_waitcnt lgkmcnt(1)
	v_mfma_f32_16x16x32_bf16 v[102:105], v[144:147], v[202:205], v[102:105]
	v_mfma_f32_16x16x32_bf16 v[98:101], v[152:155], v[202:205], v[98:101]
	v_mfma_f32_16x16x32_bf16 v[128:131], v[148:151], v[180:183], v[128:131]
	v_mfma_f32_16x16x32_bf16 v[124:127], v[156:159], v[180:183], v[124:127]
	v_mfma_f32_16x16x32_bf16 v[120:123], v[148:151], v[188:191], v[120:123]
	v_mfma_f32_16x16x32_bf16 v[116:119], v[156:159], v[188:191], v[116:119]
	v_mfma_f32_16x16x32_bf16 v[110:113], v[148:151], v[198:201], v[110:113]
	v_mfma_f32_16x16x32_bf16 v[106:109], v[156:159], v[198:201], v[106:109]
	s_waitcnt lgkmcnt(0)
	v_mfma_f32_16x16x32_bf16 v[102:105], v[148:151], v[206:209], v[102:105]
	v_mfma_f32_16x16x32_bf16 v[98:101], v[156:159], v[206:209], v[98:101]
	s_setprio 0
	s_setprio 1
	v_mfma_f32_16x16x32_bf16 v[94:97], v[160:163], v[176:179], v[94:97]
	v_mfma_f32_16x16x32_bf16 v[90:93], v[168:171], v[176:179], v[90:93]
	v_mfma_f32_16x16x32_bf16 v[86:89], v[160:163], v[184:187], v[86:89]
	v_mfma_f32_16x16x32_bf16 v[82:85], v[168:171], v[184:187], v[82:85]
	v_mfma_f32_16x16x32_bf16 v[78:81], v[160:163], v[194:197], v[78:81]
	v_mfma_f32_16x16x32_bf16 v[74:77], v[168:171], v[194:197], v[74:77]
	v_mfma_f32_16x16x32_bf16 v[70:73], v[160:163], v[202:205], v[70:73]
	v_mfma_f32_16x16x32_bf16 v[66:69], v[168:171], v[202:205], v[66:69]
	v_mfma_f32_16x16x32_bf16 v[94:97], v[164:167], v[180:183], v[94:97]
	v_mfma_f32_16x16x32_bf16 v[90:93], v[172:175], v[180:183], v[90:93]
	v_mfma_f32_16x16x32_bf16 v[86:89], v[164:167], v[188:191], v[86:89]
	v_mfma_f32_16x16x32_bf16 v[82:85], v[172:175], v[188:191], v[82:85]
	v_mfma_f32_16x16x32_bf16 v[78:81], v[164:167], v[198:201], v[78:81]
	v_mfma_f32_16x16x32_bf16 v[74:77], v[172:175], v[198:201], v[74:77]
	v_mfma_f32_16x16x32_bf16 v[70:73], v[164:167], v[206:209], v[70:73]
	v_mfma_f32_16x16x32_bf16 v[66:69], v[172:175], v[206:209], v[66:69]
	s_setprio 0
	s_barrier
	ds_read_b128 v[176:179], v135 offset:16384
	ds_read_b128 v[180:183], v135 offset:17408
	ds_read_b128 v[184:187], v135 offset:18432
	ds_read_b128 v[188:191], v135 offset:19456
	ds_read_b128 v[194:197], v135 offset:20480
	ds_read_b128 v[198:201], v135 offset:21504
	ds_read_b128 v[202:205], v135 offset:22528
	ds_read_b128 v[206:209], v135 offset:23552
	s_mov_b32 m0, s41
	s_nop 0
	global_load_lds_dwordx4 v65, s[64:65]
	s_nop 0
	s_mov_b32 m0, s42
	s_nop 0
	global_load_lds_dwordx4 v114, s[64:65]
	s_add_u32 s64, s33, 0x40100
	s_addc_u32 s65, s63, 0
	s_mov_b32 m0, s43
	s_nop 0
	global_load_lds_dwordx4 v65, s[64:65]
	s_nop 0
	s_mov_b32 m0, s44
	s_nop 0
	global_load_lds_dwordx4 v114, s[64:65]
	s_mov_b32 m0, s40
	s_nop 0
	global_load_lds_dwordx4 v139, s[34:35]
	s_nop 0
	s_mov_b32 m0, s45
	s_nop 0
	global_load_lds_dwordx4 v138, s[34:35]
	s_waitcnt vmcnt(8)
	s_waitcnt lgkmcnt(0)
	s_barrier
	s_setprio 1
	s_waitcnt lgkmcnt(0)
	v_mfma_f32_16x16x32_bf16 v[60:63], v[144:147], v[176:179], v[60:63]
	v_mfma_f32_16x16x32_bf16 v[56:59], v[152:155], v[176:179], v[56:59]
	s_waitcnt lgkmcnt(5)
	v_mfma_f32_16x16x32_bf16 v[52:55], v[144:147], v[184:187], v[52:55]
	v_mfma_f32_16x16x32_bf16 v[48:51], v[152:155], v[184:187], v[48:51]
	s_waitcnt lgkmcnt(3)
	v_mfma_f32_16x16x32_bf16 v[44:47], v[144:147], v[194:197], v[44:47]
	v_mfma_f32_16x16x32_bf16 v[40:43], v[152:155], v[194:197], v[40:43]
	s_waitcnt lgkmcnt(1)
	v_mfma_f32_16x16x32_bf16 v[36:39], v[144:147], v[202:205], v[36:39]
	v_mfma_f32_16x16x32_bf16 v[32:35], v[152:155], v[202:205], v[32:35]
	v_mfma_f32_16x16x32_bf16 v[60:63], v[148:151], v[180:183], v[60:63]
	v_mfma_f32_16x16x32_bf16 v[56:59], v[156:159], v[180:183], v[56:59]
	v_mfma_f32_16x16x32_bf16 v[52:55], v[148:151], v[188:191], v[52:55]
	v_mfma_f32_16x16x32_bf16 v[48:51], v[156:159], v[188:191], v[48:51]
	v_mfma_f32_16x16x32_bf16 v[44:47], v[148:151], v[198:201], v[44:47]
	v_mfma_f32_16x16x32_bf16 v[40:43], v[156:159], v[198:201], v[40:43]
	s_waitcnt lgkmcnt(0)
	v_mfma_f32_16x16x32_bf16 v[36:39], v[148:151], v[206:209], v[36:39]
	v_mfma_f32_16x16x32_bf16 v[32:35], v[156:159], v[206:209], v[32:35]
	s_setprio 0
	s_setprio 1
	v_mfma_f32_16x16x32_bf16 v[28:31], v[160:163], v[176:179], v[28:31]
	v_mfma_f32_16x16x32_bf16 v[24:27], v[168:171], v[176:179], v[24:27]
	v_mfma_f32_16x16x32_bf16 v[20:23], v[160:163], v[184:187], v[20:23]
	v_mfma_f32_16x16x32_bf16 v[16:19], v[168:171], v[184:187], v[16:19]
	v_mfma_f32_16x16x32_bf16 v[12:15], v[160:163], v[194:197], v[12:15]
	v_mfma_f32_16x16x32_bf16 v[8:11], v[168:171], v[194:197], v[8:11]
	v_mfma_f32_16x16x32_bf16 v[4:7], v[160:163], v[202:205], v[4:7]
	v_mfma_f32_16x16x32_bf16 v[0:3], v[168:171], v[202:205], v[0:3]
	v_mfma_f32_16x16x32_bf16 v[28:31], v[164:167], v[180:183], v[28:31]
	v_mfma_f32_16x16x32_bf16 v[24:27], v[172:175], v[180:183], v[24:27]
	v_mfma_f32_16x16x32_bf16 v[20:23], v[164:167], v[188:191], v[20:23]
	v_mfma_f32_16x16x32_bf16 v[16:19], v[172:175], v[188:191], v[16:19]
	v_mfma_f32_16x16x32_bf16 v[12:15], v[164:167], v[198:201], v[12:15]
	v_mfma_f32_16x16x32_bf16 v[8:11], v[172:175], v[198:201], v[8:11]
	v_mfma_f32_16x16x32_bf16 v[4:7], v[164:167], v[206:209], v[4:7]
	v_mfma_f32_16x16x32_bf16 v[0:3], v[172:175], v[206:209], v[0:3]
	s_setprio 0
	s_barrier
	v_add_u32_e32 v143, 0x18000, v134
	v_add_u32_e32 v144, 0x1c000, v134
	ds_read_b128 v[146:149], v143
	ds_read_b128 v[150:153], v143 offset:1024
	ds_read_b128 v[154:157], v143 offset:2048
	ds_read_b128 v[158:161], v143 offset:3072
	ds_read_b128 v[162:165], v144
	ds_read_b128 v[166:169], v144 offset:1024
	ds_read_b128 v[170:173], v144 offset:2048
	ds_read_b128 v[174:177], v144 offset:3072
	ds_read_b128 v[178:181], v135 offset:32768
	ds_read_b128 v[182:185], v135 offset:33792
	ds_read_b128 v[186:189], v135 offset:34816
	ds_read_b128 v[194:197], v135 offset:35840
	ds_read_b128 v[198:201], v135 offset:36864
	ds_read_b128 v[202:205], v135 offset:37888
	ds_read_b128 v[206:209], v135 offset:38912
	ds_read_b128 v[210:213], v135 offset:39936
	s_mov_b32 m0, s46
	s_nop 0
	global_load_lds_dwordx4 v133, s[34:35]
	s_nop 0
	s_mov_b32 m0, s47
	s_nop 0
	global_load_lds_dwordx4 v132, s[34:35]
	s_waitcnt vmcnt(8)
	s_waitcnt lgkmcnt(0)
	s_barrier
	s_setprio 1
	s_waitcnt lgkmcnt(0)
	v_mfma_f32_16x16x32_bf16 v[128:131], v[146:149], v[178:181], v[128:131]
	v_mfma_f32_16x16x32_bf16 v[124:127], v[154:157], v[178:181], v[124:127]
	s_waitcnt lgkmcnt(5)
	v_mfma_f32_16x16x32_bf16 v[120:123], v[146:149], v[186:189], v[120:123]
	v_mfma_f32_16x16x32_bf16 v[116:119], v[154:157], v[186:189], v[116:119]
	s_waitcnt lgkmcnt(3)
	v_mfma_f32_16x16x32_bf16 v[110:113], v[146:149], v[198:201], v[110:113]
	v_mfma_f32_16x16x32_bf16 v[106:109], v[154:157], v[198:201], v[106:109]
	s_waitcnt lgkmcnt(1)
	v_mfma_f32_16x16x32_bf16 v[102:105], v[146:149], v[206:209], v[102:105]
	v_mfma_f32_16x16x32_bf16 v[98:101], v[154:157], v[206:209], v[98:101]
	v_mfma_f32_16x16x32_bf16 v[128:131], v[150:153], v[182:185], v[128:131]
	v_mfma_f32_16x16x32_bf16 v[124:127], v[158:161], v[182:185], v[124:127]
	v_mfma_f32_16x16x32_bf16 v[120:123], v[150:153], v[194:197], v[120:123]
	v_mfma_f32_16x16x32_bf16 v[116:119], v[158:161], v[194:197], v[116:119]
	v_mfma_f32_16x16x32_bf16 v[110:113], v[150:153], v[202:205], v[110:113]
	v_mfma_f32_16x16x32_bf16 v[106:109], v[158:161], v[202:205], v[106:109]
	s_waitcnt lgkmcnt(0)
	v_mfma_f32_16x16x32_bf16 v[102:105], v[150:153], v[210:213], v[102:105]
	v_mfma_f32_16x16x32_bf16 v[98:101], v[158:161], v[210:213], v[98:101]
	s_setprio 0
	s_setprio 1
	v_mfma_f32_16x16x32_bf16 v[94:97], v[162:165], v[178:181], v[94:97]
	v_mfma_f32_16x16x32_bf16 v[90:93], v[170:173], v[178:181], v[90:93]
	v_mfma_f32_16x16x32_bf16 v[86:89], v[162:165], v[186:189], v[86:89]
	v_mfma_f32_16x16x32_bf16 v[82:85], v[170:173], v[186:189], v[82:85]
	v_mfma_f32_16x16x32_bf16 v[78:81], v[162:165], v[198:201], v[78:81]
	v_mfma_f32_16x16x32_bf16 v[74:77], v[170:173], v[198:201], v[74:77]
	v_mfma_f32_16x16x32_bf16 v[70:73], v[162:165], v[206:209], v[70:73]
	v_mfma_f32_16x16x32_bf16 v[66:69], v[170:173], v[206:209], v[66:69]
	v_mfma_f32_16x16x32_bf16 v[94:97], v[166:169], v[182:185], v[94:97]
	v_mfma_f32_16x16x32_bf16 v[90:93], v[174:177], v[182:185], v[90:93]
	v_mfma_f32_16x16x32_bf16 v[86:89], v[166:169], v[194:197], v[86:89]
	v_mfma_f32_16x16x32_bf16 v[82:85], v[174:177], v[194:197], v[82:85]
	v_mfma_f32_16x16x32_bf16 v[78:81], v[166:169], v[202:205], v[78:81]
	v_mfma_f32_16x16x32_bf16 v[74:77], v[174:177], v[202:205], v[74:77]
	v_mfma_f32_16x16x32_bf16 v[70:73], v[166:169], v[210:213], v[70:73]
	v_mfma_f32_16x16x32_bf16 v[66:69], v[174:177], v[210:213], v[66:69]
	s_setprio 0
	s_barrier
	ds_read_b128 v[178:181], v135 offset:49152
	ds_read_b128 v[182:185], v135 offset:50176
	ds_read_b128 v[186:189], v135 offset:51200
	ds_read_b128 v[194:197], v135 offset:52224
	ds_read_b128 v[198:201], v135 offset:53248
	ds_read_b128 v[202:205], v135 offset:54272
	ds_read_b128 v[206:209], v135 offset:55296
	ds_read_b128 v[210:213], v135 offset:56320
	s_add_u32 s34, s33, 0x180
	s_addc_u32 s35, s63, 0
	s_mov_b32 m0, s51
	s_nop 0
	global_load_lds_dwordx4 v65, s[34:35]
	s_nop 0
	s_mov_b32 m0, s52
	s_nop 0
	global_load_lds_dwordx4 v114, s[34:35]
	s_add_u32 s34, s33, 0x40180
	s_addc_u32 s35, s63, 0
	s_mov_b32 m0, s55
	s_nop 0
	global_load_lds_dwordx4 v65, s[34:35]
	s_nop 0
	s_mov_b32 m0, s56
	s_nop 0
	global_load_lds_dwordx4 v114, s[34:35]
	s_nop 0
	s_mov_b32 m0, s53
	s_nop 0
	global_load_lds_dwordx4 v139, s[26:27]
	s_nop 0
	s_mov_b32 m0, s54
	s_nop 0
	global_load_lds_dwordx4 v138, s[26:27]
	s_waitcnt vmcnt(8)
	s_waitcnt lgkmcnt(0)
	s_barrier
	s_setprio 1
	s_waitcnt lgkmcnt(0)
	v_mfma_f32_16x16x32_bf16 v[60:63], v[146:149], v[178:181], v[60:63]
	v_mfma_f32_16x16x32_bf16 v[56:59], v[154:157], v[178:181], v[56:59]
	s_waitcnt lgkmcnt(5)
	v_mfma_f32_16x16x32_bf16 v[52:55], v[146:149], v[186:189], v[52:55]
	v_mfma_f32_16x16x32_bf16 v[48:51], v[154:157], v[186:189], v[48:51]
	s_waitcnt lgkmcnt(3)
	v_mfma_f32_16x16x32_bf16 v[44:47], v[146:149], v[198:201], v[44:47]
	v_mfma_f32_16x16x32_bf16 v[40:43], v[154:157], v[198:201], v[40:43]
	s_waitcnt lgkmcnt(1)
	v_mfma_f32_16x16x32_bf16 v[36:39], v[146:149], v[206:209], v[36:39]
	v_mfma_f32_16x16x32_bf16 v[32:35], v[154:157], v[206:209], v[32:35]
	v_mfma_f32_16x16x32_bf16 v[60:63], v[150:153], v[182:185], v[60:63]
	v_mfma_f32_16x16x32_bf16 v[56:59], v[158:161], v[182:185], v[56:59]
	v_mfma_f32_16x16x32_bf16 v[52:55], v[150:153], v[194:197], v[52:55]
	v_mfma_f32_16x16x32_bf16 v[48:51], v[158:161], v[194:197], v[48:51]
	v_mfma_f32_16x16x32_bf16 v[44:47], v[150:153], v[202:205], v[44:47]
	v_mfma_f32_16x16x32_bf16 v[40:43], v[158:161], v[202:205], v[40:43]
	s_waitcnt lgkmcnt(0)
	v_mfma_f32_16x16x32_bf16 v[36:39], v[150:153], v[210:213], v[36:39]
	v_mfma_f32_16x16x32_bf16 v[32:35], v[158:161], v[210:213], v[32:35]
	s_setprio 0
	s_setprio 1
	v_mfma_f32_16x16x32_bf16 v[28:31], v[162:165], v[178:181], v[28:31]
	v_mfma_f32_16x16x32_bf16 v[24:27], v[170:173], v[178:181], v[24:27]
	v_mfma_f32_16x16x32_bf16 v[20:23], v[162:165], v[186:189], v[20:23]
	v_mfma_f32_16x16x32_bf16 v[16:19], v[170:173], v[186:189], v[16:19]
	v_mfma_f32_16x16x32_bf16 v[12:15], v[162:165], v[198:201], v[12:15]
	v_mfma_f32_16x16x32_bf16 v[8:11], v[170:173], v[198:201], v[8:11]
	v_mfma_f32_16x16x32_bf16 v[4:7], v[162:165], v[206:209], v[4:7]
	v_mfma_f32_16x16x32_bf16 v[0:3], v[170:173], v[206:209], v[0:3]
	v_mfma_f32_16x16x32_bf16 v[28:31], v[166:169], v[182:185], v[28:31]
	v_mfma_f32_16x16x32_bf16 v[24:27], v[174:177], v[182:185], v[24:27]
	v_mfma_f32_16x16x32_bf16 v[20:23], v[166:169], v[194:197], v[20:23]
	v_mfma_f32_16x16x32_bf16 v[16:19], v[174:177], v[194:197], v[16:19]
	v_mfma_f32_16x16x32_bf16 v[12:15], v[166:169], v[202:205], v[12:15]
	v_mfma_f32_16x16x32_bf16 v[8:11], v[174:177], v[202:205], v[8:11]
	v_mfma_f32_16x16x32_bf16 v[4:7], v[166:169], v[210:213], v[4:7]
	v_mfma_f32_16x16x32_bf16 v[0:3], v[174:177], v[210:213], v[0:3]
	s_setprio 0
	s_barrier
	s_add_i32 s21, s21, 2
	s_add_u32 s2, s2, 0x100
	s_addc_u32 s3, s3, 0
	s_cmp_lt_u32 s21, 12
	s_cbranch_scc1 .LBB0_1425
	ds_read_b128 v[146:149], v141
	ds_read_b128 v[150:153], v141 offset:1024
	ds_read_b128 v[154:157], v141 offset:2048
	ds_read_b128 v[158:161], v141 offset:3072
	ds_read_b128 v[162:165], v142
	ds_read_b128 v[166:169], v142 offset:1024
	ds_read_b128 v[170:173], v142 offset:2048
	ds_read_b128 v[174:177], v142 offset:3072
	s_mov_b32 s2, 0x87ff
	v_min_u32_sdwa v140, v248, s2 dst_sel:DWORD dst_unused:UNUSED_PAD src0_sel:WORD_0 src1_sel:DWORD
	v_and_b32_e32 v145, 0x7ff, v139
	v_lshl_or_b32 v140, v140, 11, v145
	v_cndmask_b32_e64 v190, v139, v140, s[4:5]
	v_min_u32_sdwa v139, v249, s2 dst_sel:DWORD dst_unused:UNUSED_PAD src0_sel:WORD_0 src1_sel:DWORD
	v_and_b32_e32 v145, 0x7ff, v138
	v_lshl_or_b32 v139, v139, 11, v145
	v_cndmask_b32_e64 v191, v138, v139, s[4:5]
	v_min_u32_sdwa v138, v250, s2 dst_sel:DWORD dst_unused:UNUSED_PAD src0_sel:WORD_0 src1_sel:DWORD
	v_and_b32_e32 v145, 0x7ff, v133
	v_min_u32_sdwa v141, v251, s2 dst_sel:DWORD dst_unused:UNUSED_PAD src0_sel:WORD_0 src1_sel:DWORD
	v_and_b32_e32 v142, 0x7ff, v132
	v_lshl_or_b32 v138, v138, 11, v145
	v_lshl_or_b32 v141, v141, 11, v142
	v_cndmask_b32_e64 v234, v133, v138, s[4:5]
	v_cndmask_b32_e64 v235, v132, v141, s[4:5]
	ds_read_b128 v[178:181], v135
	ds_read_b128 v[182:185], v135 offset:1024
	ds_read_b128 v[186:189], v135 offset:2048
	ds_read_b128 v[194:197], v135 offset:3072
	ds_read_b128 v[198:201], v135 offset:4096
	ds_read_b128 v[202:205], v135 offset:5120
	ds_read_b128 v[206:209], v135 offset:6144
	ds_read_b128 v[210:213], v135 offset:7168
	s_mov_b32 m0, s57
	s_nop 0
	global_load_lds_dwordx4 v133, s[18:19]
	s_nop 0
	s_mov_b32 m0, s58
	s_nop 0
	global_load_lds_dwordx4 v132, s[18:19]
	s_waitcnt vmcnt(8)
	s_waitcnt lgkmcnt(0)
	s_barrier
	s_setprio 1
	s_waitcnt lgkmcnt(0)
	v_mfma_f32_16x16x32_bf16 v[128:131], v[146:149], v[178:181], v[128:131]
	v_mfma_f32_16x16x32_bf16 v[124:127], v[154:157], v[178:181], v[124:127]
	s_waitcnt lgkmcnt(5)
	v_mfma_f32_16x16x32_bf16 v[120:123], v[146:149], v[186:189], v[120:123]
	s_waitcnt lgkmcnt(3)
	v_mfma_f32_16x16x32_bf16 v[106:109], v[154:157], v[198:201], v[106:109]
	s_waitcnt lgkmcnt(1)
	v_mfma_f32_16x16x32_bf16 v[102:105], v[146:149], v[206:209], v[102:105]
	v_mfma_f32_16x16x32_bf16 v[128:131], v[150:153], v[182:185], v[128:131]
	v_mfma_f32_16x16x32_bf16 v[124:127], v[158:161], v[182:185], v[124:127]
	v_mfma_f32_16x16x32_bf16 v[120:123], v[150:153], v[194:197], v[120:123]
	v_mfma_f32_16x16x32_bf16 v[116:119], v[154:157], v[186:189], v[116:119]
	v_mfma_f32_16x16x32_bf16 v[110:113], v[146:149], v[198:201], v[110:113]
	v_mfma_f32_16x16x32_bf16 v[106:109], v[158:161], v[202:205], v[106:109]
	s_waitcnt lgkmcnt(0)
	v_mfma_f32_16x16x32_bf16 v[102:105], v[150:153], v[210:213], v[102:105]
	v_mfma_f32_16x16x32_bf16 v[98:101], v[154:157], v[206:209], v[98:101]
	v_mfma_f32_16x16x32_bf16 v[214:217], v[158:161], v[194:197], v[116:119]
	v_mfma_f32_16x16x32_bf16 v[218:221], v[150:153], v[202:205], v[110:113]
	v_mfma_f32_16x16x32_bf16 v[222:225], v[158:161], v[210:213], v[98:101]
	s_setprio 0
	s_setprio 1
	v_mfma_f32_16x16x32_bf16 v[90:93], v[170:173], v[178:181], v[90:93]
	v_mfma_f32_16x16x32_bf16 v[86:89], v[162:165], v[186:189], v[86:89]
	v_mfma_f32_16x16x32_bf16 v[74:77], v[170:173], v[198:201], v[74:77]
	v_mfma_f32_16x16x32_bf16 v[70:73], v[162:165], v[206:209], v[70:73]
	v_mfma_f32_16x16x32_bf16 v[66:69], v[170:173], v[206:209], v[66:69]
	v_mfma_f32_16x16x32_bf16 v[94:97], v[162:165], v[178:181], v[94:97]
	v_mfma_f32_16x16x32_bf16 v[90:93], v[174:177], v[182:185], v[90:93]
	v_mfma_f32_16x16x32_bf16 v[86:89], v[166:169], v[194:197], v[86:89]
	v_mfma_f32_16x16x32_bf16 v[82:85], v[170:173], v[186:189], v[82:85]
	v_mfma_f32_16x16x32_bf16 v[78:81], v[162:165], v[198:201], v[78:81]
	v_mfma_f32_16x16x32_bf16 v[74:77], v[174:177], v[202:205], v[74:77]
	v_mfma_f32_16x16x32_bf16 v[70:73], v[166:169], v[210:213], v[70:73]
	v_mfma_f32_16x16x32_bf16 v[66:69], v[174:177], v[210:213], v[66:69]
	v_mfma_f32_16x16x32_bf16 v[226:229], v[166:169], v[182:185], v[94:97]
	v_mfma_f32_16x16x32_bf16 v[178:181], v[174:177], v[194:197], v[82:85]
	v_mfma_f32_16x16x32_bf16 v[182:185], v[166:169], v[202:205], v[78:81]
	s_setprio 0
	s_barrier
	s_nop 0
	ds_read_b128 v[78:81], v135 offset:16384
	ds_read_b128 v[82:85], v135 offset:17408
	ds_read_b128 v[94:97], v135 offset:18432
	ds_read_b128 v[98:101], v135 offset:19456
	ds_read_b128 v[110:113], v135 offset:20480
	ds_read_b128 v[116:119], v135 offset:21504
	ds_read_b128 v[186:189], v135 offset:22528
	ds_read_b128 v[194:197], v135 offset:23552
	s_mov_b32 m0, s41
	s_nop 0
	global_load_lds_dwordx4 v65, s[22:23]
	s_nop 0
	s_mov_b32 m0, s42
	s_nop 0
	global_load_lds_dwordx4 v114, s[22:23]
	s_add_u32 s2, s22, 0x40000
	s_addc_u32 s3, s23, 0
	s_mov_b32 m0, s43
	s_nop 0
	global_load_lds_dwordx4 v65, s[2:3]
	s_nop 0
	s_mov_b32 m0, s44
	s_nop 0
	global_load_lds_dwordx4 v114, s[2:3]
	s_mov_b32 m0, s40
	s_nop 0
	global_load_lds_dwordx4 v190, s[6:7]
	s_nop 0
	s_mov_b32 m0, s45
	s_nop 0
	global_load_lds_dwordx4 v191, s[6:7]
	s_waitcnt vmcnt(8)
	s_waitcnt lgkmcnt(0)
	s_barrier
	s_setprio 1
	s_waitcnt lgkmcnt(0)
	v_mfma_f32_16x16x32_bf16 v[60:63], v[146:149], v[78:81], v[60:63]
	s_waitcnt lgkmcnt(5)
	v_mfma_f32_16x16x32_bf16 v[52:55], v[146:149], v[94:97], v[52:55]
	s_waitcnt lgkmcnt(3)
	v_mfma_f32_16x16x32_bf16 v[40:43], v[154:157], v[110:113], v[40:43]
	s_waitcnt lgkmcnt(1)
	v_mfma_f32_16x16x32_bf16 v[36:39], v[146:149], v[186:189], v[36:39]
	v_mfma_f32_16x16x32_bf16 v[60:63], v[150:153], v[82:85], v[60:63]
	v_mfma_f32_16x16x32_bf16 v[56:59], v[154:157], v[78:81], v[56:59]
	v_mfma_f32_16x16x32_bf16 v[52:55], v[150:153], v[98:101], v[52:55]
	v_mfma_f32_16x16x32_bf16 v[48:51], v[154:157], v[94:97], v[48:51]
	v_mfma_f32_16x16x32_bf16 v[44:47], v[146:149], v[110:113], v[44:47]
	v_mfma_f32_16x16x32_bf16 v[40:43], v[158:161], v[116:119], v[40:43]
	s_waitcnt lgkmcnt(0)
	v_mfma_f32_16x16x32_bf16 v[36:39], v[150:153], v[194:197], v[36:39]
	v_mfma_f32_16x16x32_bf16 v[32:35], v[154:157], v[186:189], v[32:35]
	v_mfma_f32_16x16x32_bf16 v[198:201], v[158:161], v[82:85], v[56:59]
	v_mfma_f32_16x16x32_bf16 v[202:205], v[158:161], v[98:101], v[48:51]
	v_mfma_f32_16x16x32_bf16 v[206:209], v[150:153], v[116:119], v[44:47]
	v_mfma_f32_16x16x32_bf16 v[146:149], v[158:161], v[194:197], v[32:35]
	s_setprio 0
	s_setprio 1
	v_mfma_f32_16x16x32_bf16 v[24:27], v[170:173], v[78:81], v[24:27]
	v_mfma_f32_16x16x32_bf16 v[20:23], v[162:165], v[94:97], v[20:23]
	v_mfma_f32_16x16x32_bf16 v[8:11], v[170:173], v[110:113], v[8:11]
	v_mfma_f32_16x16x32_bf16 v[4:7], v[162:165], v[186:189], v[4:7]
	v_mfma_f32_16x16x32_bf16 v[28:31], v[162:165], v[78:81], v[28:31]
	v_mfma_f32_16x16x32_bf16 v[24:27], v[174:177], v[82:85], v[24:27]
	v_mfma_f32_16x16x32_bf16 v[20:23], v[166:169], v[98:101], v[20:23]
	v_mfma_f32_16x16x32_bf16 v[16:19], v[170:173], v[94:97], v[16:19]
	v_mfma_f32_16x16x32_bf16 v[12:15], v[162:165], v[110:113], v[12:15]
	v_mfma_f32_16x16x32_bf16 v[8:11], v[174:177], v[116:119], v[8:11]
	v_mfma_f32_16x16x32_bf16 v[4:7], v[166:169], v[194:197], v[4:7]
	v_mfma_f32_16x16x32_bf16 v[0:3], v[170:173], v[186:189], v[0:3]
	v_mfma_f32_16x16x32_bf16 v[150:153], v[166:169], v[82:85], v[28:31]
	v_mfma_f32_16x16x32_bf16 v[154:157], v[174:177], v[98:101], v[16:19]
	v_mfma_f32_16x16x32_bf16 v[158:161], v[166:169], v[116:119], v[12:15]
	v_mfma_f32_16x16x32_bf16 v[162:165], v[174:177], v[194:197], v[0:3]
	s_setprio 0
	s_barrier
	s_nop 1
	ds_read_b128 v[0:3], v143
	ds_read_b128 v[12:15], v143 offset:1024
	ds_read_b128 v[166:169], v143 offset:2048
	ds_read_b128 v[170:173], v143 offset:3072
	ds_read_b128 v[174:177], v144
	ds_read_b128 v[186:189], v144 offset:1024
	ds_read_b128 v[194:197], v144 offset:2048
	ds_read_b128 v[142:145], v144 offset:3072
	ds_read_b128 v[16:19], v135 offset:32768
	ds_read_b128 v[28:31], v135 offset:33792
	ds_read_b128 v[32:35], v135 offset:34816
	ds_read_b128 v[44:47], v135 offset:35840
	ds_read_b128 v[48:51], v135 offset:36864
	ds_read_b128 v[210:213], v135 offset:37888
	ds_read_b128 v[230:233], v135 offset:38912
	ds_read_b128 v[244:247], v135 offset:39936
	s_mov_b32 m0, s46
	s_nop 0
	global_load_lds_dwordx4 v234, s[6:7]
	s_nop 0
	s_mov_b32 m0, s47
	s_nop 0
	global_load_lds_dwordx4 v235, s[6:7]
	s_waitcnt vmcnt(8)
	s_waitcnt lgkmcnt(0)
	s_barrier
	s_setprio 1
	s_waitcnt lgkmcnt(0)
	v_mfma_f32_16x16x32_bf16 v[56:59], v[0:3], v[16:19], v[128:131]
	s_waitcnt lgkmcnt(6)
	v_mfma_f32_16x16x32_bf16 v[128:131], v[12:15], v[28:31], v[56:59]
	v_mfma_f32_16x16x32_bf16 v[56:59], v[166:169], v[16:19], v[124:127]
	v_mfma_f32_16x16x32_bf16 v[116:119], v[170:173], v[28:31], v[56:59]
	s_waitcnt lgkmcnt(5)
	v_mfma_f32_16x16x32_bf16 v[56:59], v[0:3], v[32:35], v[120:123]
	s_waitcnt lgkmcnt(4)
	v_mfma_f32_16x16x32_bf16 v[110:113], v[12:15], v[44:47], v[56:59]
	v_mfma_f32_16x16x32_bf16 v[56:59], v[166:169], v[32:35], v[214:217]
	v_mfma_f32_16x16x32_bf16 v[98:101], v[170:173], v[44:47], v[56:59]
	s_waitcnt lgkmcnt(3)
	v_mfma_f32_16x16x32_bf16 v[56:59], v[0:3], v[48:51], v[218:221]
	s_waitcnt lgkmcnt(2)
	v_mfma_f32_16x16x32_bf16 v[94:97], v[12:15], v[210:213], v[56:59]
	v_mfma_f32_16x16x32_bf16 v[56:59], v[166:169], v[48:51], v[106:109]
	v_mfma_f32_16x16x32_bf16 v[82:85], v[170:173], v[210:213], v[56:59]
	s_waitcnt lgkmcnt(1)
	v_mfma_f32_16x16x32_bf16 v[56:59], v[0:3], v[230:233], v[102:105]
	s_waitcnt lgkmcnt(0)
	v_mfma_f32_16x16x32_bf16 v[78:81], v[12:15], v[244:247], v[56:59]
	v_mfma_f32_16x16x32_bf16 v[56:59], v[166:169], v[230:233], v[222:225]
	v_mfma_f32_16x16x32_bf16 v[56:59], v[170:173], v[244:247], v[56:59]
	s_setprio 0
	s_setprio 1
	v_mfma_f32_16x16x32_bf16 v[102:105], v[174:177], v[16:19], v[226:229]
	v_mfma_f32_16x16x32_bf16 v[16:19], v[194:197], v[16:19], v[90:93]
	v_mfma_f32_16x16x32_bf16 v[120:123], v[142:145], v[28:31], v[16:19]
	v_mfma_f32_16x16x32_bf16 v[16:19], v[174:177], v[32:35], v[86:89]
	v_mfma_f32_16x16x32_bf16 v[106:109], v[186:189], v[44:47], v[16:19]
	v_mfma_f32_16x16x32_bf16 v[16:19], v[194:197], v[32:35], v[178:181]
	v_mfma_f32_16x16x32_bf16 v[124:127], v[186:189], v[28:31], v[102:105]
	v_mfma_f32_16x16x32_bf16 v[102:105], v[142:145], v[44:47], v[16:19]
	v_mfma_f32_16x16x32_bf16 v[16:19], v[174:177], v[48:51], v[182:185]
	v_mfma_f32_16x16x32_bf16 v[90:93], v[186:189], v[210:213], v[16:19]
	v_mfma_f32_16x16x32_bf16 v[16:19], v[194:197], v[48:51], v[74:77]
	v_mfma_f32_16x16x32_bf16 v[86:89], v[142:145], v[210:213], v[16:19]
	v_mfma_f32_16x16x32_bf16 v[16:19], v[174:177], v[230:233], v[70:73]
	v_mfma_f32_16x16x32_bf16 v[74:77], v[186:189], v[244:247], v[16:19]
	v_mfma_f32_16x16x32_bf16 v[16:19], v[194:197], v[230:233], v[66:69]
	v_mfma_f32_16x16x32_bf16 v[70:73], v[142:145], v[244:247], v[16:19]
	s_setprio 0
	s_barrier
	ds_read_b128 v[178:181], v135 offset:49152
	ds_read_b128 v[182:185], v135 offset:50176
	ds_read_b128 v[210:213], v135 offset:51200
	ds_read_b128 v[214:217], v135 offset:52224
	ds_read_b128 v[218:221], v135 offset:53248
	ds_read_b128 v[222:225], v135 offset:54272
	ds_read_b128 v[226:229], v135 offset:55296
	ds_read_b128 v[230:233], v135 offset:56320
	s_add_u32 s2, s22, 0x80
	s_addc_u32 s3, s23, 0
	s_mov_b32 m0, s51
	s_nop 0
	global_load_lds_dwordx4 v65, s[2:3]
	s_nop 0
	s_mov_b32 m0, s52
	s_nop 0
	global_load_lds_dwordx4 v114, s[2:3]
	s_add_u32 s2, s22, 0x40080
	s_addc_u32 s3, s23, 0
	s_mov_b32 m0, s55
	s_nop 0
	global_load_lds_dwordx4 v65, s[2:3]
	s_nop 0
	s_mov_b32 m0, s56
	s_nop 0
	global_load_lds_dwordx4 v114, s[2:3]
	s_mov_b32 m0, s53
	s_nop 0
	global_load_lds_dwordx4 v190, s[14:15]
	s_nop 0
	s_mov_b32 m0, s54
	s_nop 0
	global_load_lds_dwordx4 v191, s[14:15]
	s_waitcnt vmcnt(8)
	s_waitcnt lgkmcnt(0)
	s_barrier
	s_setprio 1
	s_waitcnt lgkmcnt(0)
	v_mfma_f32_16x16x32_bf16 v[16:19], v[0:3], v[178:181], v[60:63]
	s_waitcnt lgkmcnt(6)
	v_mfma_f32_16x16x32_bf16 v[66:69], v[12:15], v[182:185], v[16:19]
	v_mfma_f32_16x16x32_bf16 v[16:19], v[166:169], v[178:181], v[198:201]
	v_mfma_f32_16x16x32_bf16 v[48:51], v[170:173], v[182:185], v[16:19]
	s_waitcnt lgkmcnt(5)
	v_mfma_f32_16x16x32_bf16 v[16:19], v[0:3], v[210:213], v[52:55]
	s_waitcnt lgkmcnt(4)
	v_mfma_f32_16x16x32_bf16 v[44:47], v[12:15], v[214:217], v[16:19]
	v_mfma_f32_16x16x32_bf16 v[16:19], v[166:169], v[210:213], v[202:205]
	v_mfma_f32_16x16x32_bf16 v[32:35], v[170:173], v[214:217], v[16:19]
	s_waitcnt lgkmcnt(3)
	v_mfma_f32_16x16x32_bf16 v[16:19], v[0:3], v[218:221], v[206:209]
	s_waitcnt lgkmcnt(1)
	v_mfma_f32_16x16x32_bf16 v[0:3], v[0:3], v[226:229], v[36:39]
	v_mfma_f32_16x16x32_bf16 v[28:31], v[12:15], v[222:225], v[16:19]
	v_mfma_f32_16x16x32_bf16 v[16:19], v[166:169], v[218:221], v[40:43]
	s_waitcnt lgkmcnt(0)
	v_mfma_f32_16x16x32_bf16 v[12:15], v[12:15], v[230:233], v[0:3]
	v_mfma_f32_16x16x32_bf16 v[0:3], v[166:169], v[226:229], v[146:149]
	v_mfma_f32_16x16x32_bf16 v[16:19], v[170:173], v[222:225], v[16:19]
	v_mfma_f32_16x16x32_bf16 v[0:3], v[170:173], v[230:233], v[0:3]
	s_setprio 0
	s_setprio 1
	v_mfma_f32_16x16x32_bf16 v[20:23], v[174:177], v[210:213], v[20:23]
	v_mfma_f32_16x16x32_bf16 v[36:39], v[174:177], v[178:181], v[150:153]
	v_mfma_f32_16x16x32_bf16 v[40:43], v[186:189], v[214:217], v[20:23]
	v_mfma_f32_16x16x32_bf16 v[20:23], v[194:197], v[210:213], v[154:157]
	v_mfma_f32_16x16x32_bf16 v[60:63], v[186:189], v[182:185], v[36:39]
	v_mfma_f32_16x16x32_bf16 v[24:27], v[194:197], v[178:181], v[24:27]
	v_mfma_f32_16x16x32_bf16 v[36:39], v[142:145], v[214:217], v[20:23]
	v_mfma_f32_16x16x32_bf16 v[20:23], v[174:177], v[218:221], v[158:161]
	v_mfma_f32_16x16x32_bf16 v[8:11], v[194:197], v[218:221], v[8:11]
	v_mfma_f32_16x16x32_bf16 v[4:7], v[174:177], v[226:229], v[4:7]
	v_mfma_f32_16x16x32_bf16 v[52:55], v[142:145], v[182:185], v[24:27]
	v_mfma_f32_16x16x32_bf16 v[24:27], v[186:189], v[222:225], v[20:23]
	v_mfma_f32_16x16x32_bf16 v[20:23], v[142:145], v[222:225], v[8:11]
	v_mfma_f32_16x16x32_bf16 v[8:11], v[186:189], v[230:233], v[4:7]
	v_mfma_f32_16x16x32_bf16 v[4:7], v[194:197], v[226:229], v[162:165]
	v_mfma_f32_16x16x32_bf16 v[4:7], v[142:145], v[230:233], v[4:7]
	s_setprio 0
	s_barrier
	s_andn2_b64 vcc, exec, s[16:17]
	s_cbranch_vccnz .LBB0_1428
	s_barrier

.LBB0_1495:
	v_readlane_b32 s1, v254, 59
	s_cmp_eq_u32 s1, 3
	s_movk_i32 s0, 0x110
	s_cselect_b32 s29, 0x100, s0
	s_lshl_b32 s30, s29, 2
	v_readlane_b32 s4, v255, 0
	s_cmp_ge_i32 s4, s30
	v_mbcnt_lo_u32_b32 v0, -1, 0
	v_mbcnt_hi_u32_b32 v0, -1, v0
	s_cbranch_scc1 .LBB0_1513
	v_readlane_b32 s2, v254, 62
	v_readlane_b32 s3, v254, 63
	s_add_u32 s36, s2, 0x6400000
	s_addc_u32 s37, s3, 0
	s_lshl_b32 s0, s1, 25
	s_add_u32 s0, s2, s0
	s_addc_u32 s1, s3, 0
	s_add_u32 s38, s0, 0x31a00000
	s_addc_u32 s39, s1, 0
	s_lshl_b32 s8, s56, 10
	s_add_i32 s40, s8, 0
	s_ashr_i32 s1, s56, 2
	s_add_i32 s41, s40, 0x10000
	s_add_i32 s42, s40, 0x12000
	s_add_i32 s43, s40, 0x14000
	s_add_i32 s44, s40, 0x16000
	s_add_i32 s45, s40, 0x2000
	s_add_i32 s46, s40, 0x4000
	s_add_i32 s47, s40, 0x6000
	s_cmp_eq_u32 s1, 1
	s_cselect_b64 s[6:7], -1, 0
	s_ashr_i32 s49, s4, 31
	s_lshr_b32 s0, s49, 29
	s_add_i32 s0, s4, s0
	s_ashr_i32 s2, s0, 3
	s_and_b32 s0, s0, -8
	s_sub_i32 s0, s4, s0
	s_lshr_b32 s48, s29, 1
	s_lshr_b32 s3, s0, 31
	s_or_b32 s3, s48, s3
	s_mul_i32 s0, s0, s3
	s_add_i32 s0, s0, s2
	s_ashr_i32 s2, s0, 31
	s_lshr_b32 s2, s2, 27
	s_add_i32 s2, s0, s2
	s_ashr_i32 s3, s2, 5
	s_lshl_b32 s4, s3, 3
	s_sub_i32 s3, s29, s4
	s_min_i32 s5, s3, 8
	s_sext_i32_i8 s3, s5
	v_cvt_f32_i32_e32 v1, s3
	s_andn2_b32 s2, s2, 31
	s_sub_i32 s9, s0, s2
	v_cvt_f32_i32_e32 v2, s9
	v_rcp_iflag_f32_e32 v3, v1
	s_xor_b32 s0, s9, s3
	s_ashr_i32 s0, s0, 30
	s_or_b32 s0, s0, 1
	v_mul_f32_e32 v3, v2, v3
	v_trunc_f32_e32 v3, v3
	v_fma_f32 v2, -v3, v1, v2
	v_cmp_ge_f32_e64 s[2:3], |v2|, |v1|
	v_lshl_or_b32 v1, v0, 4, s8
	v_cvt_i32_f32_e32 v3, v3
	v_ashrrev_i32_e32 v2, 31, v1
	v_lshrrev_b32_e32 v2, 22, v2
	v_add_u32_e32 v2, v1, v2
	s_and_b64 s[2:3], s[2:3], exec
	v_ashrrev_i32_e32 v2, 10, v2
	v_readfirstlane_b32 s2, v3
	v_mul_i32_i24_e32 v3, 0x400, v2
	v_sub_u32_e32 v3, v1, v3
	v_lshrrev_b32_e32 v4, 4, v3
	v_bitop3_b32 v3, v4, v3, 32 bitop3:0x6c
	v_ashrrev_i32_e32 v5, 31, v3
	v_lshrrev_b32_e32 v5, 26, v5
	v_lshlrev_b32_e32 v4, 3, v2
	v_add_u32_e32 v5, v3, v5
	v_and_b32_e32 v4, -16, v4
	s_waitcnt vmcnt(0)
	v_ashrrev_i32_e32 v6, 6, v5
	v_and_b32_e32 v5, 0xc0, v5
	v_add_u32_e32 v4, v6, v4
	v_sub_u32_e32 v3, v3, v5
	v_lshlrev_b32_e32 v2, 5, v2
	v_ashrrev_i16_sdwa v3, v193, sext(v3) dst_sel:DWORD dst_unused:UNUSED_PAD src0_sel:DWORD src1_sel:BYTE_0
	v_lshlrev_b32_e32 v5, 1, v4
	v_lshrrev_b32_e32 v7, 2, v4
	v_and_b32_e32 v6, 3, v6
	s_mov_b32 s8, 0x1fffe0
	v_and_b32_e32 v2, 32, v2
	v_bfe_i32 v3, v3, 0, 16
	v_and_b32_e32 v5, 24, v5
	v_and_b32_e32 v7, 4, v7
	v_and_or_b32 v6, v4, s8, v6
	v_or3_b32 v5, v6, v7, v5
	v_add_lshl_u32 v2, v2, v3, 1
	v_add_u32_e32 v1, 0x2000, v1
	v_lshl_add_u32 v65, v4, 11, v2
	v_lshl_add_u32 v114, v5, 11, v2
	v_ashrrev_i32_e32 v2, 31, v1
	v_lshrrev_b32_e32 v2, 22, v2
	s_cselect_b32 s0, s0, 0
	v_add_u32_e32 v2, v1, v2
	s_add_i32 s0, s2, s0
	v_ashrrev_i32_e32 v2, 10, v2
	s_mul_i32 s2, s0, s5
	v_mul_i32_i24_e32 v3, 0x400, v2
	s_sub_i32 s2, s9, s2
	v_sub_u32_e32 v1, v1, v3
	s_sext_i32_i8 s2, s2
	v_lshrrev_b32_e32 v3, 4, v1
	s_add_i32 s20, s4, s2
	v_bitop3_b32 v1, v3, v1, 32 bitop3:0x6c
	s_ashr_i32 s21, s20, 31
	v_ashrrev_i32_e32 v4, 31, v1
	s_lshl_b64 s[2:3], s[20:21], 19
	s_ashr_i32 s4, s20, 4
	s_add_i32 s5, s20, 0xffffff00
	v_lshrrev_b32_e32 v4, 26, v4
	s_cmpk_lt_i32 s20, 0x100
	v_add_u32_e32 v4, v1, v4
	s_cselect_b32 s4, s4, s5
	v_ashrrev_i32_e32 v5, 6, v4
	v_and_b32_e32 v4, 0xffc0, v4
	s_ashr_i32 s5, s4, 31
	v_sub_u32_e32 v1, v1, v4
	s_lshl_b64 s[4:5], s[4:5], 21
	v_lshlrev_b32_e32 v3, 3, v2
	v_lshrrev_b16_e32 v4, 7, v1
	s_add_u32 s9, s38, s4
	v_and_b32_e32 v3, -16, v3
	v_and_b32_e32 v4, 1, v4
	s_addc_u32 s10, s39, s5
	s_bfe_i64 s[4:5], s[0:1], 0x80000
	v_add_u32_e32 v3, v5, v3
	v_add_u16_e32 v1, v1, v4
	s_lshl_b64 s[4:5], s[4:5], 19
	v_lshlrev_b32_e32 v2, 5, v2
	v_ashrrev_i16_sdwa v1, v193, sext(v1) dst_sel:DWORD dst_unused:UNUSED_PAD src0_sel:DWORD src1_sel:BYTE_0
	v_lshlrev_b32_e32 v4, 1, v3
	v_lshrrev_b32_e32 v6, 2, v3
	v_and_b32_e32 v5, 3, v5
	s_add_u32 s24, s9, s4
	v_and_b32_e32 v2, 32, v2
	v_bfe_i32 v1, v1, 0, 16
	v_and_b32_e32 v4, 24, v4
	v_and_b32_e32 v6, 4, v6
	v_and_or_b32 v5, v3, s8, v5
	s_addc_u32 s25, s10, s5
	v_or3_b32 v4, v5, v6, v4
	v_add_lshl_u32 v1, v2, v1, 1
	s_mov_b32 m0, s41
	s_nop 0
	global_load_lds_dwordx4 v114, s[24:25]
	s_add_u32 s4, s24, 0x40000
	v_lshl_add_u32 v141, v4, 11, v1
	s_mov_b32 m0, s42
	s_nop 0
	global_load_lds_dwordx4 v141, s[24:25]
	s_addc_u32 s5, s25, 0
	s_mov_b32 m0, s43
	s_nop 0
	global_load_lds_dwordx4 v114, s[4:5]
	s_add_u32 s22, s36, s2
	s_mov_b32 m0, s44
	s_nop 0
	global_load_lds_dwordx4 v141, s[4:5]
	s_addc_u32 s23, s37, s3
	s_mov_b32 m0, s40
	s_nop 0
	global_load_lds_dwordx4 v65, s[22:23]
	s_add_u32 s2, s22, 0x40000
	v_lshl_add_u32 v140, v3, 11, v1
	s_mov_b32 m0, s45
	s_nop 0
	global_load_lds_dwordx4 v140, s[22:23]
	s_addc_u32 s3, s23, 0
	s_mov_b32 m0, s46
	s_nop 0
	global_load_lds_dwordx4 v65, s[2:3]
	s_cmp_lg_u32 s1, 1
	s_mov_b32 m0, s47
	s_nop 0
	global_load_lds_dwordx4 v140, s[2:3]
	s_cbranch_scc1 .LBB0_1498
	s_barrier
.LBB0_1498:
	v_readlane_b32 s2, v254, 62
	v_readlane_b32 s3, v254, 63
	s_add_u32 s8, s2, 0x13000000
	s_addc_u32 s9, s3, 0
	s_add_u32 s2, s2, 0x1300000
	s_sext_i32_i8 s60, s0
	s_addc_u32 s3, s3, 0
	s_lshl_b32 s21, s1, 6
	s_lshl_b32 s0, s1, 13
	s_lshl_b32 s1, s56, 5
	s_and_b32 s50, s1, 0x60
	s_lshl_b32 s1, s50, 7
	s_add_i32 s51, s40, 0x18000
	s_add_i32 s52, s40, 0x1a000
	s_add_i32 s53, s40, 0x8000
	s_add_i32 s54, s40, 0xa000
	s_add_i32 s55, s40, 0x1c000
	s_mov_b32 s4, s56
	s_add_i32 s56, s40, 0x1e000
	s_add_i32 s57, s40, 0xc000
	s_cmp_lt_u32 s4, 4
	v_and_b32_e32 v1, 48, v0
	v_lshlrev_b32_e32 v2, 6, v0
	s_movk_i32 s4, 0x3c0
	v_lshlrev_b32_e32 v0, 2, v0
	s_cselect_b64 s[10:11], -1, 0
	s_add_i32 s58, s40, 0xe000
	v_and_or_b32 v1, v2, s4, v1
	v_and_b32_e32 v0, 32, v0
	v_bitop3_b32 v2, v1, s0, v0 bitop3:0xde
	s_add_u32 s0, s24, 0x80
	v_bitop3_b32 v0, v1, s1, v0 bitop3:0xde
	s_waitcnt vmcnt(2)
	s_barrier
	s_addc_u32 s1, s25, 0
	s_mov_b32 m0, s51
	s_nop 0
	global_load_lds_dwordx4 v114, s[0:1]
	s_mov_b32 s59, 0
	s_mov_b32 m0, s52
	s_nop 0
	global_load_lds_dwordx4 v141, s[0:1]
	s_add_u32 s0, s22, 0x80
	s_addc_u32 s1, s23, 0
	s_mov_b32 m0, s53
	s_nop 0
	global_load_lds_dwordx4 v65, s[0:1]
	v_add_u32_e32 v142, 0, v0
	s_mov_b32 m0, s54
	s_nop 0
	global_load_lds_dwordx4 v140, s[0:1]
	s_add_u32 s0, s24, 0x40080
	s_addc_u32 s1, s25, 0
	s_mov_b32 m0, s55
	s_nop 0
	global_load_lds_dwordx4 v114, s[0:1]
	v_add_u32_e32 v143, 0, v2
	s_mov_b32 m0, s56
	s_nop 0
	global_load_lds_dwordx4 v141, s[0:1]
	s_waitcnt vmcnt(6)
	s_barrier
	s_branch .LBB0_1501

.LBB0_1506:
	s_add_u32 s61, s22, s18
	s_addc_u32 s66, s23, s19
	v_add_u32_e32 v132, 0x10000, v142
	v_add_u32_e32 v133, 0x14000, v142
	s_add_u32 s34, s61, 0x100
	ds_read_b128 v[134:137], v132
	ds_read_b128 v[144:147], v132 offset:1024
	ds_read_b128 v[148:151], v132 offset:2048
	ds_read_b128 v[152:155], v132 offset:3072
	ds_read_b128 v[156:159], v133
	ds_read_b128 v[160:163], v133 offset:1024
	ds_read_b128 v[164:167], v133 offset:2048
	ds_read_b128 v[168:171], v133 offset:3072
	s_addc_u32 s35, s66, 0
	s_add_u32 s26, s61, 0x180
	s_addc_u32 s27, s66, 0
	s_add_u32 s15, s24, s18
	s_addc_u32 s33, s25, s19
	s_add_u32 s62, s15, 0x100
	s_addc_u32 s63, s33, 0
	ds_read_b128 v[172:175], v143
	ds_read_b128 v[176:179], v143 offset:1024
	ds_read_b128 v[180:183], v143 offset:2048
	ds_read_b128 v[184:187], v143 offset:3072
	ds_read_b128 v[188:191], v143 offset:4096
	ds_read_b128 v[194:197], v143 offset:5120
	ds_read_b128 v[198:201], v143 offset:6144
	ds_read_b128 v[202:205], v143 offset:7168
	s_add_u32 s64, s61, 0x40080
	s_addc_u32 s65, s66, 0
	s_mov_b32 m0, s57
	s_nop 0
	global_load_lds_dwordx4 v65, s[64:65]
	s_nop 0
	s_mov_b32 m0, s58
	s_nop 0
	global_load_lds_dwordx4 v140, s[64:65]
	s_waitcnt vmcnt(8)
	s_waitcnt lgkmcnt(0)
	s_barrier
	s_setprio 1
	s_waitcnt lgkmcnt(0)
	v_mfma_f32_16x16x32_bf16 v[128:131], v[134:137], v[172:175], v[128:131]
	v_mfma_f32_16x16x32_bf16 v[124:127], v[148:151], v[172:175], v[124:127]
	s_waitcnt lgkmcnt(5)
	v_mfma_f32_16x16x32_bf16 v[120:123], v[134:137], v[180:183], v[120:123]
	v_mfma_f32_16x16x32_bf16 v[116:119], v[148:151], v[180:183], v[116:119]
	s_waitcnt lgkmcnt(3)
	v_mfma_f32_16x16x32_bf16 v[110:113], v[134:137], v[188:191], v[110:113]
	v_mfma_f32_16x16x32_bf16 v[106:109], v[148:151], v[188:191], v[106:109]
	s_waitcnt lgkmcnt(1)
	v_mfma_f32_16x16x32_bf16 v[102:105], v[134:137], v[198:201], v[102:105]
	v_mfma_f32_16x16x32_bf16 v[98:101], v[148:151], v[198:201], v[98:101]
	v_mfma_f32_16x16x32_bf16 v[128:131], v[144:147], v[176:179], v[128:131]
	v_mfma_f32_16x16x32_bf16 v[124:127], v[152:155], v[176:179], v[124:127]
	v_mfma_f32_16x16x32_bf16 v[120:123], v[144:147], v[184:187], v[120:123]
	v_mfma_f32_16x16x32_bf16 v[116:119], v[152:155], v[184:187], v[116:119]
	v_mfma_f32_16x16x32_bf16 v[110:113], v[144:147], v[194:197], v[110:113]
	v_mfma_f32_16x16x32_bf16 v[106:109], v[152:155], v[194:197], v[106:109]
	s_waitcnt lgkmcnt(0)
	v_mfma_f32_16x16x32_bf16 v[102:105], v[144:147], v[202:205], v[102:105]
	v_mfma_f32_16x16x32_bf16 v[98:101], v[152:155], v[202:205], v[98:101]
	s_setprio 0
	s_setprio 1
	v_mfma_f32_16x16x32_bf16 v[94:97], v[156:159], v[172:175], v[94:97]
	v_mfma_f32_16x16x32_bf16 v[90:93], v[164:167], v[172:175], v[90:93]
	v_mfma_f32_16x16x32_bf16 v[86:89], v[156:159], v[180:183], v[86:89]
	v_mfma_f32_16x16x32_bf16 v[82:85], v[164:167], v[180:183], v[82:85]
	v_mfma_f32_16x16x32_bf16 v[78:81], v[156:159], v[188:191], v[78:81]
	v_mfma_f32_16x16x32_bf16 v[74:77], v[164:167], v[188:191], v[74:77]
	v_mfma_f32_16x16x32_bf16 v[70:73], v[156:159], v[198:201], v[70:73]
	v_mfma_f32_16x16x32_bf16 v[66:69], v[164:167], v[198:201], v[66:69]
	v_mfma_f32_16x16x32_bf16 v[94:97], v[160:163], v[176:179], v[94:97]
	v_mfma_f32_16x16x32_bf16 v[90:93], v[168:171], v[176:179], v[90:93]
	v_mfma_f32_16x16x32_bf16 v[86:89], v[160:163], v[184:187], v[86:89]
	v_mfma_f32_16x16x32_bf16 v[82:85], v[168:171], v[184:187], v[82:85]
	v_mfma_f32_16x16x32_bf16 v[78:81], v[160:163], v[194:197], v[78:81]
	v_mfma_f32_16x16x32_bf16 v[74:77], v[168:171], v[194:197], v[74:77]
	v_mfma_f32_16x16x32_bf16 v[70:73], v[160:163], v[202:205], v[70:73]
	v_mfma_f32_16x16x32_bf16 v[66:69], v[168:171], v[202:205], v[66:69]
	s_setprio 0
	s_barrier
	ds_read_b128 v[172:175], v143 offset:16384
	ds_read_b128 v[176:179], v143 offset:17408
	ds_read_b128 v[180:183], v143 offset:18432
	ds_read_b128 v[184:187], v143 offset:19456
	ds_read_b128 v[188:191], v143 offset:20480
	ds_read_b128 v[194:197], v143 offset:21504
	ds_read_b128 v[198:201], v143 offset:22528
	ds_read_b128 v[202:205], v143 offset:23552
	s_mov_b32 m0, s41
	s_nop 0
	global_load_lds_dwordx4 v114, s[62:63]
	s_nop 0
	s_mov_b32 m0, s42
	s_nop 0
	global_load_lds_dwordx4 v141, s[62:63]
	s_add_u32 s62, s15, 0x40100
	s_addc_u32 s63, s33, 0
	s_mov_b32 m0, s43
	s_nop 0
	global_load_lds_dwordx4 v114, s[62:63]
	s_nop 0
	s_mov_b32 m0, s44
	s_nop 0
	global_load_lds_dwordx4 v141, s[62:63]
	s_mov_b32 m0, s40
	s_nop 0
	global_load_lds_dwordx4 v65, s[34:35]
	s_nop 0
	s_mov_b32 m0, s45
	s_nop 0
	global_load_lds_dwordx4 v140, s[34:35]
	s_waitcnt vmcnt(8)
	s_waitcnt lgkmcnt(0)
	s_barrier
	s_setprio 1
	s_waitcnt lgkmcnt(0)
	v_mfma_f32_16x16x32_bf16 v[60:63], v[134:137], v[172:175], v[60:63]
	v_mfma_f32_16x16x32_bf16 v[56:59], v[148:151], v[172:175], v[56:59]
	s_waitcnt lgkmcnt(5)
	v_mfma_f32_16x16x32_bf16 v[52:55], v[134:137], v[180:183], v[52:55]
	v_mfma_f32_16x16x32_bf16 v[48:51], v[148:151], v[180:183], v[48:51]
	s_waitcnt lgkmcnt(3)
	v_mfma_f32_16x16x32_bf16 v[44:47], v[134:137], v[188:191], v[44:47]
	v_mfma_f32_16x16x32_bf16 v[40:43], v[148:151], v[188:191], v[40:43]
	s_waitcnt lgkmcnt(1)
	v_mfma_f32_16x16x32_bf16 v[36:39], v[134:137], v[198:201], v[36:39]
	v_mfma_f32_16x16x32_bf16 v[32:35], v[148:151], v[198:201], v[32:35]
	v_mfma_f32_16x16x32_bf16 v[60:63], v[144:147], v[176:179], v[60:63]
	v_mfma_f32_16x16x32_bf16 v[56:59], v[152:155], v[176:179], v[56:59]
	v_mfma_f32_16x16x32_bf16 v[52:55], v[144:147], v[184:187], v[52:55]
	v_mfma_f32_16x16x32_bf16 v[48:51], v[152:155], v[184:187], v[48:51]
	v_mfma_f32_16x16x32_bf16 v[44:47], v[144:147], v[194:197], v[44:47]
	v_mfma_f32_16x16x32_bf16 v[40:43], v[152:155], v[194:197], v[40:43]
	s_waitcnt lgkmcnt(0)
	v_mfma_f32_16x16x32_bf16 v[36:39], v[144:147], v[202:205], v[36:39]
	v_mfma_f32_16x16x32_bf16 v[32:35], v[152:155], v[202:205], v[32:35]
	s_setprio 0
	s_setprio 1
	v_mfma_f32_16x16x32_bf16 v[28:31], v[156:159], v[172:175], v[28:31]
	v_mfma_f32_16x16x32_bf16 v[24:27], v[164:167], v[172:175], v[24:27]
	v_mfma_f32_16x16x32_bf16 v[20:23], v[156:159], v[180:183], v[20:23]
	v_mfma_f32_16x16x32_bf16 v[16:19], v[164:167], v[180:183], v[16:19]
	v_mfma_f32_16x16x32_bf16 v[12:15], v[156:159], v[188:191], v[12:15]
	v_mfma_f32_16x16x32_bf16 v[8:11], v[164:167], v[188:191], v[8:11]
	v_mfma_f32_16x16x32_bf16 v[4:7], v[156:159], v[198:201], v[4:7]
	v_mfma_f32_16x16x32_bf16 v[0:3], v[164:167], v[198:201], v[0:3]
	v_mfma_f32_16x16x32_bf16 v[28:31], v[160:163], v[176:179], v[28:31]
	v_mfma_f32_16x16x32_bf16 v[24:27], v[168:171], v[176:179], v[24:27]
	v_mfma_f32_16x16x32_bf16 v[20:23], v[160:163], v[184:187], v[20:23]
	v_mfma_f32_16x16x32_bf16 v[16:19], v[168:171], v[184:187], v[16:19]
	v_mfma_f32_16x16x32_bf16 v[12:15], v[160:163], v[194:197], v[12:15]
	v_mfma_f32_16x16x32_bf16 v[8:11], v[168:171], v[194:197], v[8:11]
	v_mfma_f32_16x16x32_bf16 v[4:7], v[160:163], v[202:205], v[4:7]
	v_mfma_f32_16x16x32_bf16 v[0:3], v[168:171], v[202:205], v[0:3]
	s_setprio 0
	s_barrier
	v_add_u32_e32 v134, 0x18000, v142
	v_add_u32_e32 v135, 0x1c000, v142
	ds_read_b128 v[136:139], v134
	ds_read_b128 v[144:147], v134 offset:1024
	ds_read_b128 v[148:151], v134 offset:2048
	ds_read_b128 v[152:155], v134 offset:3072
	ds_read_b128 v[156:159], v135
	ds_read_b128 v[160:163], v135 offset:1024
	ds_read_b128 v[164:167], v135 offset:2048
	ds_read_b128 v[168:171], v135 offset:3072
	ds_read_b128 v[172:175], v143 offset:32768
	ds_read_b128 v[176:179], v143 offset:33792
	ds_read_b128 v[180:183], v143 offset:34816
	ds_read_b128 v[184:187], v143 offset:35840
	ds_read_b128 v[188:191], v143 offset:36864
	ds_read_b128 v[194:197], v143 offset:37888
	ds_read_b128 v[198:201], v143 offset:38912
	ds_read_b128 v[202:205], v143 offset:39936
	s_add_u32 s34, s61, 0x40100
	s_addc_u32 s35, s66, 0
	s_mov_b32 m0, s46
	s_nop 0
	global_load_lds_dwordx4 v65, s[34:35]
	s_nop 0
	s_mov_b32 m0, s47
	s_nop 0
	global_load_lds_dwordx4 v140, s[34:35]
	s_waitcnt vmcnt(8)
	s_waitcnt lgkmcnt(0)
	s_barrier
	s_setprio 1
	s_waitcnt lgkmcnt(0)
	v_mfma_f32_16x16x32_bf16 v[128:131], v[136:139], v[172:175], v[128:131]
	v_mfma_f32_16x16x32_bf16 v[124:127], v[148:151], v[172:175], v[124:127]
	s_waitcnt lgkmcnt(5)
	v_mfma_f32_16x16x32_bf16 v[120:123], v[136:139], v[180:183], v[120:123]
	v_mfma_f32_16x16x32_bf16 v[116:119], v[148:151], v[180:183], v[116:119]
	s_waitcnt lgkmcnt(3)
	v_mfma_f32_16x16x32_bf16 v[110:113], v[136:139], v[188:191], v[110:113]
	v_mfma_f32_16x16x32_bf16 v[106:109], v[148:151], v[188:191], v[106:109]
	s_waitcnt lgkmcnt(1)
	v_mfma_f32_16x16x32_bf16 v[102:105], v[136:139], v[198:201], v[102:105]
	v_mfma_f32_16x16x32_bf16 v[98:101], v[148:151], v[198:201], v[98:101]
	v_mfma_f32_16x16x32_bf16 v[128:131], v[144:147], v[176:179], v[128:131]
	v_mfma_f32_16x16x32_bf16 v[124:127], v[152:155], v[176:179], v[124:127]
	v_mfma_f32_16x16x32_bf16 v[120:123], v[144:147], v[184:187], v[120:123]
	v_mfma_f32_16x16x32_bf16 v[116:119], v[152:155], v[184:187], v[116:119]
	v_mfma_f32_16x16x32_bf16 v[110:113], v[144:147], v[194:197], v[110:113]
	v_mfma_f32_16x16x32_bf16 v[106:109], v[152:155], v[194:197], v[106:109]
	s_waitcnt lgkmcnt(0)
	v_mfma_f32_16x16x32_bf16 v[102:105], v[144:147], v[202:205], v[102:105]
	v_mfma_f32_16x16x32_bf16 v[98:101], v[152:155], v[202:205], v[98:101]
	s_setprio 0
	s_setprio 1
	v_mfma_f32_16x16x32_bf16 v[94:97], v[156:159], v[172:175], v[94:97]
	v_mfma_f32_16x16x32_bf16 v[90:93], v[164:167], v[172:175], v[90:93]
	v_mfma_f32_16x16x32_bf16 v[86:89], v[156:159], v[180:183], v[86:89]
	v_mfma_f32_16x16x32_bf16 v[82:85], v[164:167], v[180:183], v[82:85]
	v_mfma_f32_16x16x32_bf16 v[78:81], v[156:159], v[188:191], v[78:81]
	v_mfma_f32_16x16x32_bf16 v[74:77], v[164:167], v[188:191], v[74:77]
	v_mfma_f32_16x16x32_bf16 v[70:73], v[156:159], v[198:201], v[70:73]
	v_mfma_f32_16x16x32_bf16 v[66:69], v[164:167], v[198:201], v[66:69]
	v_mfma_f32_16x16x32_bf16 v[94:97], v[160:163], v[176:179], v[94:97]
	v_mfma_f32_16x16x32_bf16 v[90:93], v[168:171], v[176:179], v[90:93]
	v_mfma_f32_16x16x32_bf16 v[86:89], v[160:163], v[184:187], v[86:89]
	v_mfma_f32_16x16x32_bf16 v[82:85], v[168:171], v[184:187], v[82:85]
	v_mfma_f32_16x16x32_bf16 v[78:81], v[160:163], v[194:197], v[78:81]
	v_mfma_f32_16x16x32_bf16 v[74:77], v[168:171], v[194:197], v[74:77]
	v_mfma_f32_16x16x32_bf16 v[70:73], v[160:163], v[202:205], v[70:73]
	v_mfma_f32_16x16x32_bf16 v[66:69], v[168:171], v[202:205], v[66:69]
	s_setprio 0
	s_barrier
	ds_read_b128 v[172:175], v143 offset:49152
	ds_read_b128 v[176:179], v143 offset:50176
	ds_read_b128 v[180:183], v143 offset:51200
	ds_read_b128 v[184:187], v143 offset:52224
	ds_read_b128 v[188:191], v143 offset:53248
	ds_read_b128 v[194:197], v143 offset:54272
	ds_read_b128 v[198:201], v143 offset:55296
	ds_read_b128 v[202:205], v143 offset:56320
	s_add_u32 s34, s15, 0x180
	s_addc_u32 s35, s33, 0
	s_mov_b32 m0, s51
	s_nop 0
	global_load_lds_dwordx4 v114, s[34:35]
	s_nop 0
	s_mov_b32 m0, s52
	s_nop 0
	global_load_lds_dwordx4 v141, s[34:35]
	s_add_u32 s34, s15, 0x40180
	s_addc_u32 s35, s33, 0
	s_mov_b32 m0, s55
	s_nop 0
	global_load_lds_dwordx4 v114, s[34:35]
	s_nop 0
	s_mov_b32 m0, s56
	s_nop 0
	global_load_lds_dwordx4 v141, s[34:35]
	s_nop 0
	s_mov_b32 m0, s53
	s_nop 0
	global_load_lds_dwordx4 v65, s[26:27]
	s_nop 0
	s_mov_b32 m0, s54
	s_nop 0
	global_load_lds_dwordx4 v140, s[26:27]
	s_waitcnt vmcnt(8)
	s_waitcnt lgkmcnt(0)
	s_barrier
	s_setprio 1
	s_waitcnt lgkmcnt(0)
	v_mfma_f32_16x16x32_bf16 v[60:63], v[136:139], v[172:175], v[60:63]
	v_mfma_f32_16x16x32_bf16 v[56:59], v[148:151], v[172:175], v[56:59]
	s_waitcnt lgkmcnt(5)
	v_mfma_f32_16x16x32_bf16 v[52:55], v[136:139], v[180:183], v[52:55]
	v_mfma_f32_16x16x32_bf16 v[48:51], v[148:151], v[180:183], v[48:51]
	s_waitcnt lgkmcnt(3)
	v_mfma_f32_16x16x32_bf16 v[44:47], v[136:139], v[188:191], v[44:47]
	v_mfma_f32_16x16x32_bf16 v[40:43], v[148:151], v[188:191], v[40:43]
	s_waitcnt lgkmcnt(1)
	v_mfma_f32_16x16x32_bf16 v[36:39], v[136:139], v[198:201], v[36:39]
	v_mfma_f32_16x16x32_bf16 v[32:35], v[148:151], v[198:201], v[32:35]
	v_mfma_f32_16x16x32_bf16 v[60:63], v[144:147], v[176:179], v[60:63]
	v_mfma_f32_16x16x32_bf16 v[56:59], v[152:155], v[176:179], v[56:59]
	v_mfma_f32_16x16x32_bf16 v[52:55], v[144:147], v[184:187], v[52:55]
	v_mfma_f32_16x16x32_bf16 v[48:51], v[152:155], v[184:187], v[48:51]
	v_mfma_f32_16x16x32_bf16 v[44:47], v[144:147], v[194:197], v[44:47]
	v_mfma_f32_16x16x32_bf16 v[40:43], v[152:155], v[194:197], v[40:43]
	s_waitcnt lgkmcnt(0)
	v_mfma_f32_16x16x32_bf16 v[36:39], v[144:147], v[202:205], v[36:39]
	v_mfma_f32_16x16x32_bf16 v[32:35], v[152:155], v[202:205], v[32:35]
	s_setprio 0
	s_setprio 1
	v_mfma_f32_16x16x32_bf16 v[28:31], v[156:159], v[172:175], v[28:31]
	v_mfma_f32_16x16x32_bf16 v[24:27], v[164:167], v[172:175], v[24:27]
	v_mfma_f32_16x16x32_bf16 v[20:23], v[156:159], v[180:183], v[20:23]
	v_mfma_f32_16x16x32_bf16 v[16:19], v[164:167], v[180:183], v[16:19]
	v_mfma_f32_16x16x32_bf16 v[12:15], v[156:159], v[188:191], v[12:15]
	v_mfma_f32_16x16x32_bf16 v[8:11], v[164:167], v[188:191], v[8:11]
	v_mfma_f32_16x16x32_bf16 v[4:7], v[156:159], v[198:201], v[4:7]
	v_mfma_f32_16x16x32_bf16 v[0:3], v[164:167], v[198:201], v[0:3]
	v_mfma_f32_16x16x32_bf16 v[28:31], v[160:163], v[176:179], v[28:31]
	v_mfma_f32_16x16x32_bf16 v[24:27], v[168:171], v[176:179], v[24:27]
	v_mfma_f32_16x16x32_bf16 v[20:23], v[160:163], v[184:187], v[20:23]
	v_mfma_f32_16x16x32_bf16 v[16:19], v[168:171], v[184:187], v[16:19]
	v_mfma_f32_16x16x32_bf16 v[12:15], v[160:163], v[194:197], v[12:15]
	v_mfma_f32_16x16x32_bf16 v[8:11], v[168:171], v[194:197], v[8:11]
	v_mfma_f32_16x16x32_bf16 v[4:7], v[160:163], v[202:205], v[4:7]
	v_mfma_f32_16x16x32_bf16 v[0:3], v[168:171], v[202:205], v[0:3]
	s_setprio 0
	s_barrier
	s_add_i32 s13, s13, 2
	s_add_u32 s18, s18, 0x100
	s_addc_u32 s19, s19, 0
	s_cmp_lt_u32 s13, 12
	s_cbranch_scc1 .LBB0_1506
	ds_read_b128 v[136:139], v132
	ds_read_b128 v[144:147], v132 offset:1024
	ds_read_b128 v[148:151], v132 offset:2048
	ds_read_b128 v[152:155], v132 offset:3072
	ds_read_b128 v[156:159], v133
	ds_read_b128 v[160:163], v133 offset:1024
	ds_read_b128 v[164:167], v133 offset:2048
	ds_read_b128 v[168:171], v133 offset:3072
	s_ashr_i32 s15, s14, 31
	s_lshl_b64 s[18:19], s[14:15], 19
	s_add_u32 s18, s36, s18
	s_addc_u32 s19, s37, s19
	s_and_b64 s[4:5], s[4:5], exec
	s_cselect_b32 s24, s18, s22
	s_cselect_b32 s25, s19, s23
	s_add_u32 s4, s24, 0x80
	s_addc_u32 s5, s25, 0
	ds_read_b128 v[172:175], v143
	ds_read_b128 v[176:179], v143 offset:1024
	ds_read_b128 v[180:183], v143 offset:2048
	ds_read_b128 v[184:187], v143 offset:3072
	ds_read_b128 v[188:191], v143 offset:4096
	ds_read_b128 v[194:197], v143 offset:5120
	ds_read_b128 v[198:201], v143 offset:6144
	ds_read_b128 v[202:205], v143 offset:7168
	s_add_u32 s22, s22, 0x40780
	s_addc_u32 s23, s23, 0
	s_mov_b32 m0, s57
	s_nop 0
	global_load_lds_dwordx4 v65, s[22:23]
	s_nop 0
	s_mov_b32 m0, s58
	s_nop 0
	global_load_lds_dwordx4 v140, s[22:23]
	s_waitcnt vmcnt(8)
	s_waitcnt lgkmcnt(0)
	s_barrier
	s_setprio 1
	s_waitcnt lgkmcnt(0)
	v_mfma_f32_16x16x32_bf16 v[128:131], v[136:139], v[172:175], v[128:131]
	v_mfma_f32_16x16x32_bf16 v[124:127], v[148:151], v[172:175], v[124:127]
	s_waitcnt lgkmcnt(3)
	v_mfma_f32_16x16x32_bf16 v[110:113], v[136:139], v[188:191], v[110:113]
	v_mfma_f32_16x16x32_bf16 v[106:109], v[148:151], v[188:191], v[106:109]
	v_mfma_f32_16x16x32_bf16 v[128:131], v[144:147], v[176:179], v[128:131]
	v_mfma_f32_16x16x32_bf16 v[124:127], v[152:155], v[176:179], v[124:127]
	v_mfma_f32_16x16x32_bf16 v[120:123], v[136:139], v[180:183], v[120:123]
	v_mfma_f32_16x16x32_bf16 v[116:119], v[148:151], v[180:183], v[116:119]
	s_waitcnt lgkmcnt(2)
	v_mfma_f32_16x16x32_bf16 v[110:113], v[144:147], v[194:197], v[110:113]
	v_mfma_f32_16x16x32_bf16 v[106:109], v[152:155], v[194:197], v[106:109]
	s_waitcnt lgkmcnt(1)
	v_mfma_f32_16x16x32_bf16 v[102:105], v[136:139], v[198:201], v[102:105]
	v_mfma_f32_16x16x32_bf16 v[98:101], v[148:151], v[198:201], v[98:101]
	v_mfma_f32_16x16x32_bf16 v[206:209], v[144:147], v[184:187], v[120:123]
	v_mfma_f32_16x16x32_bf16 v[210:213], v[152:155], v[184:187], v[116:119]
	s_waitcnt lgkmcnt(0)
	v_mfma_f32_16x16x32_bf16 v[214:217], v[144:147], v[202:205], v[102:105]
	v_mfma_f32_16x16x32_bf16 v[218:221], v[152:155], v[202:205], v[98:101]
	s_setprio 0
	s_setprio 1
	v_mfma_f32_16x16x32_bf16 v[94:97], v[156:159], v[172:175], v[94:97]
	v_mfma_f32_16x16x32_bf16 v[90:93], v[164:167], v[172:175], v[90:93]
	v_mfma_f32_16x16x32_bf16 v[70:73], v[156:159], v[198:201], v[70:73]
	v_mfma_f32_16x16x32_bf16 v[66:69], v[164:167], v[198:201], v[66:69]
	v_mfma_f32_16x16x32_bf16 v[94:97], v[160:163], v[176:179], v[94:97]
	v_mfma_f32_16x16x32_bf16 v[90:93], v[168:171], v[176:179], v[90:93]
	v_mfma_f32_16x16x32_bf16 v[86:89], v[156:159], v[180:183], v[86:89]
	v_mfma_f32_16x16x32_bf16 v[82:85], v[164:167], v[180:183], v[82:85]
	v_mfma_f32_16x16x32_bf16 v[78:81], v[156:159], v[188:191], v[78:81]
	v_mfma_f32_16x16x32_bf16 v[74:77], v[164:167], v[188:191], v[74:77]
	v_mfma_f32_16x16x32_bf16 v[70:73], v[160:163], v[202:205], v[70:73]
	v_mfma_f32_16x16x32_bf16 v[66:69], v[168:171], v[202:205], v[66:69]
	v_mfma_f32_16x16x32_bf16 v[172:175], v[160:163], v[184:187], v[86:89]
	v_mfma_f32_16x16x32_bf16 v[176:179], v[168:171], v[184:187], v[82:85]
	v_mfma_f32_16x16x32_bf16 v[180:183], v[160:163], v[194:197], v[78:81]
	v_mfma_f32_16x16x32_bf16 v[184:187], v[168:171], v[194:197], v[74:77]
	s_setprio 0
	s_barrier
	s_nop 0
	ds_read_b128 v[74:77], v143 offset:16384
	ds_read_b128 v[78:81], v143 offset:17408
	ds_read_b128 v[82:85], v143 offset:18432
	ds_read_b128 v[86:89], v143 offset:19456
	ds_read_b128 v[98:101], v143 offset:20480
	ds_read_b128 v[102:105], v143 offset:21504
	ds_read_b128 v[116:119], v143 offset:22528
	ds_read_b128 v[120:123], v143 offset:23552
	s_mov_b32 m0, s41
	s_nop 0
	global_load_lds_dwordx4 v114, s[16:17]
	s_add_u32 s22, s16, 0x40000
	s_mov_b32 m0, s42
	s_nop 0
	global_load_lds_dwordx4 v141, s[16:17]
	s_addc_u32 s23, s17, 0
	s_mov_b32 m0, s43
	s_nop 0
	global_load_lds_dwordx4 v114, s[22:23]
	s_nop 0
	s_mov_b32 m0, s44
	s_nop 0
	global_load_lds_dwordx4 v141, s[22:23]
	s_nop 0
	s_mov_b32 m0, s40
	s_nop 0
	global_load_lds_dwordx4 v65, s[24:25]
	s_nop 0
	s_mov_b32 m0, s45
	s_nop 0
	global_load_lds_dwordx4 v140, s[24:25]
	s_waitcnt vmcnt(8)
	s_waitcnt lgkmcnt(0)
	s_barrier
	s_setprio 1
	s_waitcnt lgkmcnt(0)
	v_mfma_f32_16x16x32_bf16 v[52:55], v[136:139], v[82:85], v[52:55]
	v_mfma_f32_16x16x32_bf16 v[48:51], v[148:151], v[82:85], v[48:51]
	s_waitcnt lgkmcnt(1)
	v_mfma_f32_16x16x32_bf16 v[36:39], v[136:139], v[116:119], v[36:39]
	v_mfma_f32_16x16x32_bf16 v[32:35], v[148:151], v[116:119], v[32:35]
	v_mfma_f32_16x16x32_bf16 v[60:63], v[136:139], v[74:77], v[60:63]
	v_mfma_f32_16x16x32_bf16 v[56:59], v[148:151], v[74:77], v[56:59]
	v_mfma_f32_16x16x32_bf16 v[52:55], v[144:147], v[86:89], v[52:55]
	v_mfma_f32_16x16x32_bf16 v[48:51], v[152:155], v[86:89], v[48:51]
	v_mfma_f32_16x16x32_bf16 v[44:47], v[136:139], v[98:101], v[44:47]
	v_mfma_f32_16x16x32_bf16 v[40:43], v[148:151], v[98:101], v[40:43]
	s_waitcnt lgkmcnt(0)
	v_mfma_f32_16x16x32_bf16 v[36:39], v[144:147], v[120:123], v[36:39]
	v_mfma_f32_16x16x32_bf16 v[32:35], v[152:155], v[120:123], v[32:35]
	v_mfma_f32_16x16x32_bf16 v[188:191], v[144:147], v[78:81], v[60:63]
	v_mfma_f32_16x16x32_bf16 v[194:197], v[152:155], v[78:81], v[56:59]
	v_mfma_f32_16x16x32_bf16 v[198:201], v[144:147], v[102:105], v[44:47]
	v_mfma_f32_16x16x32_bf16 v[202:205], v[152:155], v[102:105], v[40:43]
	s_setprio 0
	s_setprio 1
	v_mfma_f32_16x16x32_bf16 v[20:23], v[156:159], v[82:85], v[20:23]
	v_mfma_f32_16x16x32_bf16 v[16:19], v[164:167], v[82:85], v[16:19]
	v_mfma_f32_16x16x32_bf16 v[12:15], v[156:159], v[98:101], v[12:15]
	v_mfma_f32_16x16x32_bf16 v[8:11], v[164:167], v[98:101], v[8:11]
	v_mfma_f32_16x16x32_bf16 v[28:31], v[156:159], v[74:77], v[28:31]
	v_mfma_f32_16x16x32_bf16 v[24:27], v[164:167], v[74:77], v[24:27]
	v_mfma_f32_16x16x32_bf16 v[20:23], v[160:163], v[86:89], v[20:23]
	v_mfma_f32_16x16x32_bf16 v[16:19], v[168:171], v[86:89], v[16:19]
	v_mfma_f32_16x16x32_bf16 v[12:15], v[160:163], v[102:105], v[12:15]
	v_mfma_f32_16x16x32_bf16 v[8:11], v[168:171], v[102:105], v[8:11]
	v_mfma_f32_16x16x32_bf16 v[4:7], v[156:159], v[116:119], v[4:7]
	v_mfma_f32_16x16x32_bf16 v[0:3], v[164:167], v[116:119], v[0:3]
	v_mfma_f32_16x16x32_bf16 v[136:139], v[160:163], v[78:81], v[28:31]
	v_mfma_f32_16x16x32_bf16 v[144:147], v[168:171], v[78:81], v[24:27]
	v_mfma_f32_16x16x32_bf16 v[148:151], v[160:163], v[120:123], v[4:7]
	v_mfma_f32_16x16x32_bf16 v[152:155], v[168:171], v[120:123], v[0:3]
	s_setprio 0
	s_barrier
	s_nop 1
	ds_read_b128 v[0:3], v134
	ds_read_b128 v[4:7], v134 offset:1024
	ds_read_b128 v[156:159], v134 offset:2048
	ds_read_b128 v[160:163], v134 offset:3072
	ds_read_b128 v[164:167], v135
	ds_read_b128 v[168:171], v135 offset:1024
	ds_read_b128 v[222:225], v135 offset:2048
	ds_read_b128 v[132:135], v135 offset:3072
	ds_read_b128 v[24:27], v143 offset:32768
	ds_read_b128 v[28:31], v143 offset:33792
	ds_read_b128 v[40:43], v143 offset:34816
	ds_read_b128 v[44:47], v143 offset:35840
	ds_read_b128 v[56:59], v143 offset:36864
	ds_read_b128 v[60:63], v143 offset:37888
	ds_read_b128 v[226:229], v143 offset:38912
	ds_read_b128 v[230:233], v143 offset:39936
	s_add_u32 s22, s24, 0x40000
	s_addc_u32 s23, s25, 0
	s_mov_b32 m0, s46
	s_nop 0
	global_load_lds_dwordx4 v65, s[22:23]
	s_nop 0
	s_mov_b32 m0, s47
	s_nop 0
	global_load_lds_dwordx4 v140, s[22:23]
	s_waitcnt vmcnt(8)
	s_waitcnt lgkmcnt(0)
	s_barrier
	s_setprio 1
	s_waitcnt lgkmcnt(0)
	v_mfma_f32_16x16x32_bf16 v[74:77], v[0:3], v[24:27], v[128:131]
	s_waitcnt lgkmcnt(6)
	v_mfma_f32_16x16x32_bf16 v[116:119], v[4:7], v[28:31], v[74:77]
	v_mfma_f32_16x16x32_bf16 v[74:77], v[156:159], v[24:27], v[124:127]
	v_mfma_f32_16x16x32_bf16 v[120:123], v[160:163], v[28:31], v[74:77]
	s_waitcnt lgkmcnt(5)
	v_mfma_f32_16x16x32_bf16 v[74:77], v[0:3], v[40:43], v[206:209]
	s_waitcnt lgkmcnt(4)
	v_mfma_f32_16x16x32_bf16 v[98:101], v[4:7], v[44:47], v[74:77]
	v_mfma_f32_16x16x32_bf16 v[74:77], v[156:159], v[40:43], v[210:213]
	v_mfma_f32_16x16x32_bf16 v[102:105], v[160:163], v[44:47], v[74:77]
	s_waitcnt lgkmcnt(3)
	v_mfma_f32_16x16x32_bf16 v[74:77], v[0:3], v[56:59], v[110:113]
	s_waitcnt lgkmcnt(2)
	v_mfma_f32_16x16x32_bf16 v[82:85], v[4:7], v[60:63], v[74:77]
	v_mfma_f32_16x16x32_bf16 v[74:77], v[156:159], v[56:59], v[106:109]
	v_mfma_f32_16x16x32_bf16 v[86:89], v[160:163], v[60:63], v[74:77]
	s_waitcnt lgkmcnt(1)
	v_mfma_f32_16x16x32_bf16 v[74:77], v[0:3], v[226:229], v[214:217]
	s_waitcnt lgkmcnt(0)
	v_mfma_f32_16x16x32_bf16 v[78:81], v[4:7], v[230:233], v[74:77]
	v_mfma_f32_16x16x32_bf16 v[74:77], v[156:159], v[226:229], v[218:221]
	v_mfma_f32_16x16x32_bf16 v[74:77], v[160:163], v[230:233], v[74:77]
	s_setprio 0
	s_setprio 1
	v_mfma_f32_16x16x32_bf16 v[94:97], v[164:167], v[24:27], v[94:97]
	v_mfma_f32_16x16x32_bf16 v[24:27], v[222:225], v[24:27], v[90:93]
	v_mfma_f32_16x16x32_bf16 v[128:131], v[132:135], v[28:31], v[24:27]
	v_mfma_f32_16x16x32_bf16 v[24:27], v[164:167], v[40:43], v[172:175]
	v_mfma_f32_16x16x32_bf16 v[106:109], v[168:171], v[44:47], v[24:27]
	v_mfma_f32_16x16x32_bf16 v[24:27], v[222:225], v[40:43], v[176:179]
	v_mfma_f32_16x16x32_bf16 v[110:113], v[132:135], v[44:47], v[24:27]
	v_mfma_f32_16x16x32_bf16 v[24:27], v[164:167], v[56:59], v[180:183]
	v_mfma_f32_16x16x32_bf16 v[90:93], v[168:171], v[60:63], v[24:27]
	v_mfma_f32_16x16x32_bf16 v[24:27], v[222:225], v[56:59], v[184:187]
	v_mfma_f32_16x16x32_bf16 v[124:127], v[168:171], v[28:31], v[94:97]
	v_mfma_f32_16x16x32_bf16 v[94:97], v[132:135], v[60:63], v[24:27]
	v_mfma_f32_16x16x32_bf16 v[24:27], v[164:167], v[226:229], v[70:73]
	v_mfma_f32_16x16x32_bf16 v[60:63], v[168:171], v[230:233], v[24:27]
	v_mfma_f32_16x16x32_bf16 v[24:27], v[222:225], v[226:229], v[66:69]
	v_mfma_f32_16x16x32_bf16 v[56:59], v[132:135], v[230:233], v[24:27]
	s_setprio 0
	s_barrier
	ds_read_b128 v[172:175], v143 offset:49152
	ds_read_b128 v[176:179], v143 offset:50176
	ds_read_b128 v[180:183], v143 offset:51200
	ds_read_b128 v[184:187], v143 offset:52224
	ds_read_b128 v[206:209], v143 offset:53248
	ds_read_b128 v[210:213], v143 offset:54272
	ds_read_b128 v[214:217], v143 offset:55296
	ds_read_b128 v[218:221], v143 offset:56320
	s_add_u32 s22, s16, 0x80
	s_addc_u32 s23, s17, 0
	s_mov_b32 m0, s51
	s_nop 0
	global_load_lds_dwordx4 v114, s[22:23]
	s_nop 0
	s_mov_b32 m0, s52
	s_nop 0
	global_load_lds_dwordx4 v141, s[22:23]
	s_add_u32 s22, s16, 0x40080
	s_addc_u32 s23, s17, 0
	s_mov_b32 m0, s55
	s_nop 0
	global_load_lds_dwordx4 v114, s[22:23]
	s_nop 0
	s_mov_b32 m0, s56
	s_nop 0
	global_load_lds_dwordx4 v141, s[22:23]
	s_nop 0
	s_mov_b32 m0, s53
	s_nop 0
	global_load_lds_dwordx4 v65, s[4:5]
	s_nop 0
	s_mov_b32 m0, s54
	s_nop 0
	global_load_lds_dwordx4 v140, s[4:5]
	s_waitcnt vmcnt(8)
	s_waitcnt lgkmcnt(0)
	s_barrier
	s_setprio 1
	s_waitcnt lgkmcnt(0)
	v_mfma_f32_16x16x32_bf16 v[24:27], v[0:3], v[172:175], v[188:191]
	s_waitcnt lgkmcnt(6)
	v_mfma_f32_16x16x32_bf16 v[66:69], v[4:7], v[176:179], v[24:27]
	v_mfma_f32_16x16x32_bf16 v[24:27], v[156:159], v[172:175], v[194:197]
	v_mfma_f32_16x16x32_bf16 v[70:73], v[160:163], v[176:179], v[24:27]
	s_waitcnt lgkmcnt(5)
	v_mfma_f32_16x16x32_bf16 v[24:27], v[0:3], v[180:183], v[52:55]
	s_waitcnt lgkmcnt(4)
	v_mfma_f32_16x16x32_bf16 v[40:43], v[4:7], v[184:187], v[24:27]
	v_mfma_f32_16x16x32_bf16 v[24:27], v[156:159], v[180:183], v[48:51]
	v_mfma_f32_16x16x32_bf16 v[44:47], v[160:163], v[184:187], v[24:27]
	s_waitcnt lgkmcnt(3)
	v_mfma_f32_16x16x32_bf16 v[24:27], v[0:3], v[206:209], v[198:201]
	s_waitcnt lgkmcnt(1)
	v_mfma_f32_16x16x32_bf16 v[0:3], v[0:3], v[214:217], v[36:39]
	v_mfma_f32_16x16x32_bf16 v[24:27], v[4:7], v[210:213], v[24:27]
	v_mfma_f32_16x16x32_bf16 v[28:31], v[156:159], v[206:209], v[202:205]
	s_waitcnt lgkmcnt(0)
	v_mfma_f32_16x16x32_bf16 v[0:3], v[4:7], v[218:221], v[0:3]
	v_mfma_f32_16x16x32_bf16 v[4:7], v[156:159], v[214:217], v[32:35]
	v_mfma_f32_16x16x32_bf16 v[28:31], v[160:163], v[210:213], v[28:31]
	v_mfma_f32_16x16x32_bf16 v[4:7], v[160:163], v[218:221], v[4:7]
	s_setprio 0
	s_setprio 1
	v_mfma_f32_16x16x32_bf16 v[32:35], v[164:167], v[172:175], v[136:139]
	v_mfma_f32_16x16x32_bf16 v[52:55], v[168:171], v[176:179], v[32:35]
	v_mfma_f32_16x16x32_bf16 v[32:35], v[222:225], v[172:175], v[144:147]
	v_mfma_f32_16x16x32_bf16 v[20:23], v[164:167], v[180:183], v[20:23]
	v_mfma_f32_16x16x32_bf16 v[16:19], v[222:225], v[180:183], v[16:19]
	v_mfma_f32_16x16x32_bf16 v[12:15], v[164:167], v[206:209], v[12:15]
	v_mfma_f32_16x16x32_bf16 v[8:11], v[222:225], v[206:209], v[8:11]
	v_mfma_f32_16x16x32_bf16 v[48:51], v[132:135], v[176:179], v[32:35]
	v_mfma_f32_16x16x32_bf16 v[36:39], v[168:171], v[184:187], v[20:23]
	v_mfma_f32_16x16x32_bf16 v[32:35], v[132:135], v[184:187], v[16:19]
	v_mfma_f32_16x16x32_bf16 v[20:23], v[168:171], v[210:213], v[12:15]
	v_mfma_f32_16x16x32_bf16 v[16:19], v[132:135], v[210:213], v[8:11]
	v_mfma_f32_16x16x32_bf16 v[8:11], v[164:167], v[214:217], v[148:151]
	v_mfma_f32_16x16x32_bf16 v[12:15], v[222:225], v[214:217], v[152:155]
	v_mfma_f32_16x16x32_bf16 v[8:11], v[168:171], v[218:221], v[8:11]
	v_mfma_f32_16x16x32_bf16 v[12:15], v[132:135], v[218:221], v[12:15]
	s_setprio 0
	s_barrier
	s_andn2_b64 vcc, exec, s[10:11]
	s_cbranch_vccnz .LBB0_1509
	s_barrier
